# baseline (speedup 1.0000x reference)
.LBB6_11:
	v_lshlrev_b32_e32 v2, 12, v2
	s_lshl_b32 s48, s65, 6
	v_lshlrev_b32_e32 v6, 12, v6
	v_and_b32_e32 v2, 0xffffe000, v2
	s_lshl_b32 s17, s66, 13
	s_and_b32 s48, s48, 0x3000
	v_and_b32_e32 v6, 0xffffe000, v6
	v_lshl_add_u32 v2, v3, 9, v2
	v_and_b32_e32 v10, 48, v210
	v_lshlrev_b32_e32 v11, 6, v210
	v_lshl_add_u32 v6, v7, 9, v6
	s_add_u32 s46, s26, s46
	v_or_b32_e32 v2, v2, v4
	v_and_or_b32 v10, v11, s58, v10
	v_lshlrev_b32_e32 v11, 2, v210
	v_or_b32_e32 v6, v6, v8
	s_addc_u32 s47, s27, s47
	v_add_u32_sdwa v2, v2, sext(v5) dst_sel:DWORD dst_unused:UNUSED_PAD src0_sel:DWORD src1_sel:WORD_0
	v_and_b32_e32 v11, 32, v11
	v_add_u32_sdwa v6, v6, sext(v9) dst_sel:DWORD dst_unused:UNUSED_PAD src0_sel:DWORD src1_sel:WORD_0
	v_ashrrev_i32_e32 v3, 31, v2
	s_add_u32 s44, s24, s44
	v_xad_u32 v168, v10, v11, 0
	s_waitcnt vmcnt(6)
	v_ashrrev_i32_e32 v7, 31, v6
	v_lshlrev_b64 v[2:3], 1, v[2:3]
	s_addc_u32 s45, s25, s45
	v_add_u32_e32 v10, s48, v168
	v_lshlrev_b64 v[6:7], 1, v[6:7]
	v_lshl_add_u64 v[136:137], s[46:47], 0, v[2:3]
	v_lshl_add_u64 v[140:141], s[44:45], 0, v[2:3]
	v_mov_b32_e32 v2, 0
	v_add_u32_e32 v169, 0x10000, v10
	v_add_u32_e32 v170, 0x10400, v10
	v_add_u32_e32 v171, 0x10800, v10
	v_add_u32_e32 v172, 0x10c00, v10
	v_add_u32_e32 v161, 0x14000, v10
	v_add_u32_e32 v162, 0x14400, v10
	v_add_u32_e32 v163, 0x14800, v10
	v_add_u32_e32 v164, 0x14c00, v10
	v_add_u32_e32 v148, 0x18000, v10
	v_add_u32_e32 v149, 0x18400, v10
	v_add_u32_e32 v150, 0x18800, v10
	v_add_u32_e32 v151, 0x18c00, v10
	v_add_u32_e32 v142, 0x1c000, v10
	v_add_u32_e32 v143, 0x1c400, v10
	v_add_u32_e32 v144, 0x1c800, v10
	v_add_u32_e32 v145, 0x1cc00, v10
	v_lshl_add_u64 v[134:135], s[46:47], 0, v[6:7]
	v_lshl_add_u64 v[138:139], s[44:45], 0, v[6:7]
	s_mov_b32 s46, -2
	s_mov_b64 s[44:45], 0
	v_mov_b32_e32 v3, v2
	v_mov_b32_e32 v4, v2
	v_mov_b32_e32 v5, v2
	v_mov_b32_e32 v6, v2
	v_mov_b32_e32 v7, v2
	v_mov_b32_e32 v8, v2
	v_mov_b32_e32 v9, v2
	v_mov_b32_e32 v10, v2
	v_mov_b32_e32 v11, v2
	v_mov_b32_e32 v12, v2
	v_mov_b32_e32 v13, v2
	v_mov_b32_e32 v18, v2
	v_mov_b32_e32 v19, v2
	v_mov_b32_e32 v20, v2
	v_mov_b32_e32 v21, v2
	v_mov_b32_e32 v30, v2
	v_mov_b32_e32 v31, v2
	v_mov_b32_e32 v32, v2
	v_mov_b32_e32 v33, v2
	v_mov_b32_e32 v42, v2
	v_mov_b32_e32 v43, v2
	v_mov_b32_e32 v44, v2
	v_mov_b32_e32 v45, v2
	v_mov_b32_e32 v54, v2
	v_mov_b32_e32 v55, v2
	v_mov_b32_e32 v56, v2
	v_mov_b32_e32 v57, v2
	v_mov_b32_e32 v66, v2
	v_mov_b32_e32 v67, v2
	v_mov_b32_e32 v68, v2
	v_mov_b32_e32 v69, v2
	v_mov_b32_e32 v14, v2
	v_mov_b32_e32 v15, v2
	v_mov_b32_e32 v16, v2
	v_mov_b32_e32 v17, v2
	v_mov_b32_e32 v22, v2
	v_mov_b32_e32 v23, v2
	v_mov_b32_e32 v24, v2
	v_mov_b32_e32 v25, v2
	v_mov_b32_e32 v34, v2
	v_mov_b32_e32 v35, v2
	v_mov_b32_e32 v36, v2
	v_mov_b32_e32 v37, v2
	v_mov_b32_e32 v46, v2
	v_mov_b32_e32 v47, v2
	v_mov_b32_e32 v48, v2
	v_mov_b32_e32 v49, v2
	v_mov_b32_e32 v58, v2
	v_mov_b32_e32 v59, v2
	v_mov_b32_e32 v60, v2
	v_mov_b32_e32 v61, v2
	v_mov_b32_e32 v70, v2
	v_mov_b32_e32 v71, v2
	v_mov_b32_e32 v72, v2
	v_mov_b32_e32 v73, v2
	v_mov_b32_e32 v78, v2
	v_mov_b32_e32 v79, v2
	v_mov_b32_e32 v80, v2
	v_mov_b32_e32 v81, v2
	v_mov_b32_e32 v86, v2
	v_mov_b32_e32 v87, v2
	v_mov_b32_e32 v88, v2
	v_mov_b32_e32 v89, v2
	v_mov_b32_e32 v26, v2
	v_mov_b32_e32 v27, v2
	v_mov_b32_e32 v28, v2
	v_mov_b32_e32 v29, v2
	v_mov_b32_e32 v38, v2
	v_mov_b32_e32 v39, v2
	v_mov_b32_e32 v40, v2
	v_mov_b32_e32 v41, v2
	v_mov_b32_e32 v50, v2
	v_mov_b32_e32 v51, v2
	v_mov_b32_e32 v52, v2
	v_mov_b32_e32 v53, v2
	v_mov_b32_e32 v62, v2
	v_mov_b32_e32 v63, v2
	v_mov_b32_e32 v64, v2
	v_mov_b32_e32 v65, v2
	v_mov_b32_e32 v74, v2
	v_mov_b32_e32 v75, v2
	v_mov_b32_e32 v76, v2
	v_mov_b32_e32 v77, v2
	v_mov_b32_e32 v82, v2
	v_mov_b32_e32 v83, v2
	v_mov_b32_e32 v84, v2
	v_mov_b32_e32 v85, v2
	v_mov_b32_e32 v90, v2
	v_mov_b32_e32 v91, v2
	v_mov_b32_e32 v92, v2
	v_mov_b32_e32 v93, v2
	v_mov_b32_e32 v94, v2
	v_mov_b32_e32 v95, v2
	v_mov_b32_e32 v96, v2
	v_mov_b32_e32 v97, v2
	v_mov_b32_e32 v98, v2
	v_mov_b32_e32 v99, v2
	v_mov_b32_e32 v100, v2
	v_mov_b32_e32 v101, v2
	v_mov_b32_e32 v102, v2
	v_mov_b32_e32 v103, v2
	v_mov_b32_e32 v104, v2
	v_mov_b32_e32 v105, v2
	v_mov_b32_e32 v106, v2
	v_mov_b32_e32 v107, v2
	v_mov_b32_e32 v108, v2
	v_mov_b32_e32 v109, v2
	v_mov_b32_e32 v110, v2
	v_mov_b32_e32 v111, v2
	v_mov_b32_e32 v112, v2
	v_mov_b32_e32 v113, v2
	v_mov_b32_e32 v114, v2
	v_mov_b32_e32 v115, v2
	v_mov_b32_e32 v116, v2
	v_mov_b32_e32 v117, v2
	v_mov_b32_e32 v118, v2
	v_mov_b32_e32 v119, v2
	v_mov_b32_e32 v120, v2
	v_mov_b32_e32 v121, v2
	v_mov_b32_e32 v122, v2
	v_mov_b32_e32 v123, v2
	v_mov_b32_e32 v124, v2
	v_mov_b32_e32 v125, v2
	v_mov_b32_e32 v126, v2
	v_mov_b32_e32 v127, v2
	v_mov_b32_e32 v128, v2
	v_mov_b32_e32 v129, v2
	v_add_u32_e32 v174, 0xc000, v152
	v_add_u32_e32 v175, 0xe000, v152
	s_nop 0
	v_readfirstlane_b32 s72, v174
	v_readfirstlane_b32 s73, v175
	v_readfirstlane_b32 s74, v146
	v_readfirstlane_b32 s75, v147
	v_readfirstlane_b32 s76, v152
	v_readfirstlane_b32 s77, v153
	v_readfirstlane_b32 s78, v154
	v_readfirstlane_b32 s79, v155
	v_readfirstlane_b32 s80, v156
	v_readfirstlane_b32 s81, v157
	v_readfirstlane_b32 s82, v158
	v_readfirstlane_b32 s83, v159
	v_readfirstlane_b32 s84, v160
	v_readfirstlane_b32 s85, v165
	v_readfirstlane_b32 s86, v166
	v_readfirstlane_b32 s87, v167
	s_barrier
	s_barrier
	ds_read_b128 v[176:179], v169
	ds_read_b128 v[180:183], v170
	ds_read_b128 v[184:187], v171
	ds_read_b128 v[188:191], v172
.LBB6_12:
	v_add_u32_e32 v174, 0xc000, v152
	v_lshl_add_u64 v[192:193], v[136:137], 0, s[44:45]
	v_add_u32_e32 v175, 0xe000, v152
	v_add_u32_e32 v173, s17, v168
	v_lshl_add_u64 v[232:233], v[192:193], 0, s[30:31]
	s_mov_b32 m0, s72
	v_lshl_add_u64 v[248:249], v[134:135], 0, s[44:45]
	ds_read_b128 v[196:199], v173
	ds_read_b128 v[200:203], v173 offset:1024
	ds_read_b128 v[204:207], v173 offset:2048
	ds_read_b128 v[212:215], v173 offset:3072
	ds_read_b128 v[216:219], v173 offset:4096
	ds_read_b128 v[220:223], v173 offset:5120
	ds_read_b128 v[224:227], v173 offset:6144
	ds_read_b128 v[228:231], v173 offset:7168
	global_load_lds_dwordx4 v[232:233], off
	s_mov_b32 m0, s73
	v_lshl_add_u64 v[232:233], v[248:249], 0, s[30:31]
	global_load_lds_dwordx4 v[232:233], off
	s_waitcnt lgkmcnt(8)
	s_barrier
	s_waitcnt lgkmcnt(0)
	v_mfma_f32_16x16x32_f16 v[2:5], v[196:199], v[176:179], v[2:5]
	v_mfma_f32_16x16x32_f16 v[6:9], v[196:199], v[184:187], v[6:9]
	v_mfma_f32_16x16x32_f16 v[10:13], v[204:207], v[176:179], v[10:13]
	v_mfma_f32_16x16x32_f16 v[18:21], v[204:207], v[184:187], v[18:21]
	v_mfma_f32_16x16x32_f16 v[30:33], v[216:219], v[176:179], v[30:33]
	v_mfma_f32_16x16x32_f16 v[42:45], v[216:219], v[184:187], v[42:45]
	v_mfma_f32_16x16x32_f16 v[54:57], v[224:227], v[176:179], v[54:57]
	v_mfma_f32_16x16x32_f16 v[66:69], v[224:227], v[184:187], v[66:69]
	v_mfma_f32_16x16x32_f16 v[2:5], v[200:203], v[180:183], v[2:5]
	v_mfma_f32_16x16x32_f16 v[6:9], v[200:203], v[188:191], v[6:9]
	v_mfma_f32_16x16x32_f16 v[10:13], v[212:215], v[180:183], v[10:13]
	v_mfma_f32_16x16x32_f16 v[18:21], v[212:215], v[188:191], v[18:21]
	v_mfma_f32_16x16x32_f16 v[30:33], v[220:223], v[180:183], v[30:33]
	v_mfma_f32_16x16x32_f16 v[42:45], v[220:223], v[188:191], v[42:45]
	v_mfma_f32_16x16x32_f16 v[54:57], v[228:231], v[180:183], v[54:57]
	v_mfma_f32_16x16x32_f16 v[66:69], v[228:231], v[188:191], v[66:69]
	s_barrier
	v_lshl_add_u64 v[250:251], v[140:141], 0, s[44:45]
	v_lshl_add_u64 v[252:253], v[250:251], 0, s[34:35]
	s_mov_b32 m0, s74
	ds_read_b128 v[232:235], v161
	ds_read_b128 v[236:239], v162
	ds_read_b128 v[240:243], v163
	ds_read_b128 v[244:247], v164
	global_load_lds_dwordx4 v[252:253], off
	v_lshl_add_u64 v[252:253], v[138:139], 0, s[44:45]
	s_mov_b32 m0, s75
	v_lshl_add_u64 v[254:255], v[252:253], 0, s[34:35]
	global_load_lds_dwordx4 v[254:255], off
	s_barrier
	s_waitcnt lgkmcnt(0)
	v_mfma_f32_16x16x32_f16 v[14:17], v[196:199], v[232:235], v[14:17]
	v_mfma_f32_16x16x32_f16 v[22:25], v[196:199], v[240:243], v[22:25]
	v_mfma_f32_16x16x32_f16 v[34:37], v[204:207], v[232:235], v[34:37]
	v_mfma_f32_16x16x32_f16 v[46:49], v[204:207], v[240:243], v[46:49]
	v_mfma_f32_16x16x32_f16 v[58:61], v[216:219], v[232:235], v[58:61]
	v_mfma_f32_16x16x32_f16 v[70:73], v[216:219], v[240:243], v[70:73]
	v_mfma_f32_16x16x32_f16 v[78:81], v[224:227], v[232:235], v[78:81]
	v_mfma_f32_16x16x32_f16 v[86:89], v[224:227], v[240:243], v[86:89]
	v_mfma_f32_16x16x32_f16 v[14:17], v[200:203], v[236:239], v[14:17]
	v_mfma_f32_16x16x32_f16 v[22:25], v[200:203], v[244:247], v[22:25]
	v_mfma_f32_16x16x32_f16 v[34:37], v[212:215], v[236:239], v[34:37]
	v_mfma_f32_16x16x32_f16 v[46:49], v[212:215], v[244:247], v[46:49]
	v_mfma_f32_16x16x32_f16 v[58:61], v[220:223], v[236:239], v[58:61]
	v_mfma_f32_16x16x32_f16 v[70:73], v[220:223], v[244:247], v[70:73]
	v_mfma_f32_16x16x32_f16 v[78:81], v[228:231], v[236:239], v[78:81]
	v_mfma_f32_16x16x32_f16 v[86:89], v[228:231], v[244:247], v[86:89]
	v_lshl_add_u64 v[254:255], v[192:193], 0, s[34:35]
	s_mov_b32 m0, s76
	s_barrier
	ds_read_b128 v[196:199], v173 offset:16384
	ds_read_b128 v[200:203], v173 offset:17408
	ds_read_b128 v[204:207], v173 offset:18432
	ds_read_b128 v[212:215], v173 offset:19456
	ds_read_b128 v[216:219], v173 offset:20480
	ds_read_b128 v[220:223], v173 offset:21504
	ds_read_b128 v[224:227], v173 offset:22528
	ds_read_b128 v[228:231], v173 offset:23552
	global_load_lds_dwordx4 v[254:255], off
	s_mov_b32 m0, s77
	v_lshl_add_u64 v[254:255], v[248:249], 0, s[34:35]
	global_load_lds_dwordx4 v[254:255], off
	s_waitcnt vmcnt(10)
	s_barrier
	s_waitcnt lgkmcnt(0)
	v_mfma_f32_16x16x32_f16 v[26:29], v[196:199], v[176:179], v[26:29]
	v_mfma_f32_16x16x32_f16 v[38:41], v[196:199], v[184:187], v[38:41]
	v_mfma_f32_16x16x32_f16 v[50:53], v[204:207], v[176:179], v[50:53]
	v_mfma_f32_16x16x32_f16 v[62:65], v[204:207], v[184:187], v[62:65]
	v_mfma_f32_16x16x32_f16 v[74:77], v[216:219], v[176:179], v[74:77]
	v_mfma_f32_16x16x32_f16 v[82:85], v[216:219], v[184:187], v[82:85]
	v_mfma_f32_16x16x32_f16 v[90:93], v[224:227], v[176:179], v[90:93]
	v_mfma_f32_16x16x32_f16 v[94:97], v[224:227], v[184:187], v[94:97]
	v_mfma_f32_16x16x32_f16 v[26:29], v[200:203], v[180:183], v[26:29]
	v_mfma_f32_16x16x32_f16 v[38:41], v[200:203], v[188:191], v[38:41]
	v_mfma_f32_16x16x32_f16 v[50:53], v[212:215], v[180:183], v[50:53]
	v_mfma_f32_16x16x32_f16 v[62:65], v[212:215], v[188:191], v[62:65]
	v_mfma_f32_16x16x32_f16 v[74:77], v[220:223], v[180:183], v[74:77]
	v_mfma_f32_16x16x32_f16 v[82:85], v[220:223], v[188:191], v[82:85]
	v_mfma_f32_16x16x32_f16 v[90:93], v[228:231], v[180:183], v[90:93]
	v_mfma_f32_16x16x32_f16 v[94:97], v[228:231], v[188:191], v[94:97]
	s_barrier
	s_mov_b32 m0, s78
	v_lshl_add_u64 v[176:177], v[250:251], 0, s[36:37]
	global_load_lds_dwordx4 v[176:177], off
	s_mov_b32 m0, s79
	v_lshl_add_u64 v[176:177], v[252:253], 0, s[36:37]
	global_load_lds_dwordx4 v[176:177], off
	s_waitcnt vmcnt(6)
	s_barrier
	v_mfma_f32_16x16x32_f16 v[98:101], v[196:199], v[232:235], v[98:101]
	v_mfma_f32_16x16x32_f16 v[102:105], v[196:199], v[240:243], v[102:105]
	v_mfma_f32_16x16x32_f16 v[106:109], v[204:207], v[232:235], v[106:109]
	v_mfma_f32_16x16x32_f16 v[110:113], v[204:207], v[240:243], v[110:113]
	v_mfma_f32_16x16x32_f16 v[114:117], v[216:219], v[232:235], v[114:117]
	v_mfma_f32_16x16x32_f16 v[118:121], v[216:219], v[240:243], v[118:121]
	v_mfma_f32_16x16x32_f16 v[122:125], v[224:227], v[232:235], v[122:125]
	v_mfma_f32_16x16x32_f16 v[126:129], v[224:227], v[240:243], v[126:129]
	v_mfma_f32_16x16x32_f16 v[98:101], v[200:203], v[236:239], v[98:101]
	v_mfma_f32_16x16x32_f16 v[102:105], v[200:203], v[244:247], v[102:105]
	v_mfma_f32_16x16x32_f16 v[106:109], v[212:215], v[236:239], v[106:109]
	v_mfma_f32_16x16x32_f16 v[110:113], v[212:215], v[244:247], v[110:113]
	ds_read_b128 v[176:179], v148
	ds_read_b128 v[180:183], v149
	ds_read_b128 v[184:187], v150
	ds_read_b128 v[188:191], v151
	v_mfma_f32_16x16x32_f16 v[114:117], v[220:223], v[236:239], v[114:117]
	v_mfma_f32_16x16x32_f16 v[118:121], v[220:223], v[244:247], v[118:121]
	v_mfma_f32_16x16x32_f16 v[122:125], v[228:231], v[236:239], v[122:125]
	v_mfma_f32_16x16x32_f16 v[126:129], v[228:231], v[244:247], v[126:129]
	s_barrier
	v_lshl_add_u64 v[232:233], v[192:193], 0, s[36:37]
	s_mov_b32 m0, s80
	ds_read_b128 v[196:199], v173 offset:32768
	ds_read_b128 v[200:203], v173 offset:33792
	ds_read_b128 v[204:207], v173 offset:34816
	ds_read_b128 v[212:215], v173 offset:35840
	ds_read_b128 v[216:219], v173 offset:36864
	ds_read_b128 v[220:223], v173 offset:37888
	ds_read_b128 v[224:227], v173 offset:38912
	ds_read_b128 v[228:231], v173 offset:39936
	global_load_lds_dwordx4 v[232:233], off
	s_mov_b32 m0, s81
	v_lshl_add_u64 v[232:233], v[248:249], 0, s[36:37]
	global_load_lds_dwordx4 v[232:233], off
	s_waitcnt lgkmcnt(8)
	s_barrier
	s_waitcnt lgkmcnt(0)
	v_mfma_f32_16x16x32_f16 v[2:5], v[196:199], v[176:179], v[2:5]
	v_mfma_f32_16x16x32_f16 v[6:9], v[196:199], v[184:187], v[6:9]
	v_mfma_f32_16x16x32_f16 v[10:13], v[204:207], v[176:179], v[10:13]
	v_mfma_f32_16x16x32_f16 v[18:21], v[204:207], v[184:187], v[18:21]
	v_mfma_f32_16x16x32_f16 v[30:33], v[216:219], v[176:179], v[30:33]
	v_mfma_f32_16x16x32_f16 v[42:45], v[216:219], v[184:187], v[42:45]
	v_mfma_f32_16x16x32_f16 v[54:57], v[224:227], v[176:179], v[54:57]
	v_mfma_f32_16x16x32_f16 v[66:69], v[224:227], v[184:187], v[66:69]
	v_mfma_f32_16x16x32_f16 v[2:5], v[200:203], v[180:183], v[2:5]
	v_mfma_f32_16x16x32_f16 v[6:9], v[200:203], v[188:191], v[6:9]
	v_mfma_f32_16x16x32_f16 v[10:13], v[212:215], v[180:183], v[10:13]
	v_mfma_f32_16x16x32_f16 v[18:21], v[212:215], v[188:191], v[18:21]
	v_mfma_f32_16x16x32_f16 v[30:33], v[220:223], v[180:183], v[30:33]
	v_mfma_f32_16x16x32_f16 v[42:45], v[220:223], v[188:191], v[42:45]
	v_mfma_f32_16x16x32_f16 v[54:57], v[228:231], v[180:183], v[54:57]
	v_mfma_f32_16x16x32_f16 v[66:69], v[228:231], v[188:191], v[66:69]
	s_barrier
	v_lshl_add_u64 v[254:255], v[250:251], 0, s[38:39]
	s_mov_b32 m0, s82
	ds_read_b128 v[232:235], v142
	ds_read_b128 v[236:239], v143
	ds_read_b128 v[240:243], v144
	ds_read_b128 v[244:247], v145
	global_load_lds_dwordx4 v[254:255], off
	s_mov_b32 m0, s83
	v_lshl_add_u64 v[254:255], v[252:253], 0, s[38:39]
	global_load_lds_dwordx4 v[254:255], off
	s_barrier
	s_waitcnt lgkmcnt(0)
	v_mfma_f32_16x16x32_f16 v[14:17], v[196:199], v[232:235], v[14:17]
	v_mfma_f32_16x16x32_f16 v[22:25], v[196:199], v[240:243], v[22:25]
	v_mfma_f32_16x16x32_f16 v[34:37], v[204:207], v[232:235], v[34:37]
	v_mfma_f32_16x16x32_f16 v[46:49], v[204:207], v[240:243], v[46:49]
	v_mfma_f32_16x16x32_f16 v[58:61], v[216:219], v[232:235], v[58:61]
	v_mfma_f32_16x16x32_f16 v[70:73], v[216:219], v[240:243], v[70:73]
	v_mfma_f32_16x16x32_f16 v[78:81], v[224:227], v[232:235], v[78:81]
	v_mfma_f32_16x16x32_f16 v[86:89], v[224:227], v[240:243], v[86:89]
	v_mfma_f32_16x16x32_f16 v[14:17], v[200:203], v[236:239], v[14:17]
	v_mfma_f32_16x16x32_f16 v[22:25], v[200:203], v[244:247], v[22:25]
	v_mfma_f32_16x16x32_f16 v[34:37], v[212:215], v[236:239], v[34:37]
	v_mfma_f32_16x16x32_f16 v[46:49], v[212:215], v[244:247], v[46:49]
	v_mfma_f32_16x16x32_f16 v[58:61], v[220:223], v[236:239], v[58:61]
	v_mfma_f32_16x16x32_f16 v[70:73], v[220:223], v[244:247], v[70:73]
	v_mfma_f32_16x16x32_f16 v[78:81], v[228:231], v[236:239], v[78:81]
	v_mfma_f32_16x16x32_f16 v[86:89], v[228:231], v[244:247], v[86:89]
	v_lshl_add_u64 v[192:193], v[192:193], 0, s[38:39]
	s_mov_b32 m0, s84
	s_barrier
	ds_read_b128 v[196:199], v173 offset:49152
	ds_read_b128 v[200:203], v173 offset:50176
	ds_read_b128 v[204:207], v173 offset:51200
	ds_read_b128 v[212:215], v173 offset:52224
	ds_read_b128 v[216:219], v173 offset:53248
	ds_read_b128 v[220:223], v173 offset:54272
	ds_read_b128 v[224:227], v173 offset:55296
	ds_read_b128 v[228:231], v173 offset:56320
	global_load_lds_dwordx4 v[192:193], off
	s_mov_b32 m0, s85
	v_lshl_add_u64 v[192:193], v[248:249], 0, s[38:39]
	global_load_lds_dwordx4 v[192:193], off
	s_waitcnt vmcnt(10)
	s_barrier
	s_waitcnt lgkmcnt(0)
	v_mfma_f32_16x16x32_f16 v[26:29], v[196:199], v[176:179], v[26:29]
	v_mfma_f32_16x16x32_f16 v[38:41], v[196:199], v[184:187], v[38:41]
	v_mfma_f32_16x16x32_f16 v[50:53], v[204:207], v[176:179], v[50:53]
	v_mfma_f32_16x16x32_f16 v[62:65], v[204:207], v[184:187], v[62:65]
	v_mfma_f32_16x16x32_f16 v[74:77], v[216:219], v[176:179], v[74:77]
	v_mfma_f32_16x16x32_f16 v[82:85], v[216:219], v[184:187], v[82:85]
	v_mfma_f32_16x16x32_f16 v[90:93], v[224:227], v[176:179], v[90:93]
	v_mfma_f32_16x16x32_f16 v[94:97], v[224:227], v[184:187], v[94:97]
	v_mfma_f32_16x16x32_f16 v[26:29], v[200:203], v[180:183], v[26:29]
	v_mfma_f32_16x16x32_f16 v[38:41], v[200:203], v[188:191], v[38:41]
	v_mfma_f32_16x16x32_f16 v[50:53], v[212:215], v[180:183], v[50:53]
	v_mfma_f32_16x16x32_f16 v[62:65], v[212:215], v[188:191], v[62:65]
	v_mfma_f32_16x16x32_f16 v[74:77], v[220:223], v[180:183], v[74:77]
	v_mfma_f32_16x16x32_f16 v[82:85], v[220:223], v[188:191], v[82:85]
	v_mfma_f32_16x16x32_f16 v[90:93], v[228:231], v[180:183], v[90:93]
	v_mfma_f32_16x16x32_f16 v[94:97], v[228:231], v[188:191], v[94:97]
	s_barrier
	s_mov_b32 m0, s86
	v_lshl_add_u64 v[176:177], v[250:251], 0, s[40:41]
	global_load_lds_dwordx4 v[176:177], off
	s_mov_b32 m0, s87
	v_lshl_add_u64 v[176:177], v[252:253], 0, s[40:41]
	global_load_lds_dwordx4 v[176:177], off
	s_waitcnt vmcnt(6)
	s_barrier
	v_mfma_f32_16x16x32_f16 v[98:101], v[196:199], v[232:235], v[98:101]
	v_mfma_f32_16x16x32_f16 v[102:105], v[196:199], v[240:243], v[102:105]
	v_mfma_f32_16x16x32_f16 v[106:109], v[204:207], v[232:235], v[106:109]
	v_mfma_f32_16x16x32_f16 v[110:113], v[204:207], v[240:243], v[110:113]
	v_mfma_f32_16x16x32_f16 v[114:117], v[216:219], v[232:235], v[114:117]
	v_mfma_f32_16x16x32_f16 v[118:121], v[216:219], v[240:243], v[118:121]
	v_mfma_f32_16x16x32_f16 v[122:125], v[224:227], v[232:235], v[122:125]
	v_mfma_f32_16x16x32_f16 v[126:129], v[224:227], v[240:243], v[126:129]
	v_mfma_f32_16x16x32_f16 v[98:101], v[200:203], v[236:239], v[98:101]
	v_mfma_f32_16x16x32_f16 v[102:105], v[200:203], v[244:247], v[102:105]
	v_mfma_f32_16x16x32_f16 v[106:109], v[212:215], v[236:239], v[106:109]
	v_mfma_f32_16x16x32_f16 v[110:113], v[212:215], v[244:247], v[110:113]
	ds_read_b128 v[176:179], v169
	ds_read_b128 v[180:183], v170
	ds_read_b128 v[184:187], v171
	ds_read_b128 v[188:191], v172
	v_mfma_f32_16x16x32_f16 v[114:117], v[220:223], v[236:239], v[114:117]
	v_mfma_f32_16x16x32_f16 v[118:121], v[220:223], v[244:247], v[118:121]
	v_mfma_f32_16x16x32_f16 v[122:125], v[228:231], v[236:239], v[122:125]
	v_mfma_f32_16x16x32_f16 v[126:129], v[228:231], v[244:247], v[126:129]
	s_add_i32 s46, s46, 2
	s_add_u32 s44, s44, 0x100
	s_addc_u32 s45, s45, 0
	s_cmp_lt_u32 s46, 4
	s_barrier
	s_cbranch_scc1 .LBB6_12
	s_add_u32 s0, s0, 0x20380
	s_addc_u32 s1, s1, 0
	v_readfirstlane_b32 s17, v174
	v_lshl_add_u64 v[130:131], v[130:131], 1, s[0:1]
	s_mov_b32 m0, s17
	ds_read_b128 v[134:137], v169
	ds_read_b128 v[138:141], v170
	ds_read_b128 v[152:155], v171
	ds_read_b128 v[156:159], v172
	ds_read_b128 v[166:169], v173
	ds_read_b128 v[176:179], v173 offset:1024
	ds_read_b128 v[180:183], v173 offset:2048
	ds_read_b128 v[184:187], v173 offset:3072
	ds_read_b128 v[188:191], v173 offset:4096
	ds_read_b128 v[196:199], v173 offset:5120
	ds_read_b128 v[200:203], v173 offset:6144
	ds_read_b128 v[204:207], v173 offset:7168
	global_load_lds_dwordx4 v[130:131], off
	v_lshl_add_u64 v[130:131], v[132:133], 1, s[0:1]
	v_readfirstlane_b32 s0, v175
	s_mov_b32 m0, s0
	s_nop 0
	global_load_lds_dwordx4 v[130:131], off
	s_barrier
	s_waitcnt lgkmcnt(0)
	v_mfma_f32_16x16x32_f16 v[2:5], v[166:169], v[134:137], v[2:5]
	v_mfma_f32_16x16x32_f16 v[42:45], v[188:191], v[152:155], v[42:45]
	v_mfma_f32_16x16x32_f16 v[54:57], v[200:203], v[134:137], v[54:57]
	v_mfma_f32_16x16x32_f16 v[66:69], v[200:203], v[152:155], v[66:69]
	v_mfma_f32_16x16x32_f16 v[2:5], v[176:179], v[138:141], v[2:5]
	v_mfma_f32_16x16x32_f16 v[6:9], v[166:169], v[152:155], v[6:9]
	v_mfma_f32_16x16x32_f16 v[10:13], v[180:183], v[134:137], v[10:13]
	v_mfma_f32_16x16x32_f16 v[18:21], v[180:183], v[152:155], v[18:21]
	v_mfma_f32_16x16x32_f16 v[30:33], v[188:191], v[134:137], v[30:33]
	v_mfma_f32_16x16x32_f16 v[42:45], v[196:199], v[156:159], v[42:45]
	v_mfma_f32_16x16x32_f16 v[54:57], v[204:207], v[138:141], v[54:57]
	v_mfma_f32_16x16x32_f16 v[66:69], v[204:207], v[156:159], v[66:69]
	v_mfma_f32_16x16x32_f16 v[6:9], v[176:179], v[156:159], v[6:9]
	v_mfma_f32_16x16x32_f16 v[10:13], v[184:187], v[138:141], v[10:13]
	v_mfma_f32_16x16x32_f16 v[18:21], v[184:187], v[156:159], v[18:21]
	v_mfma_f32_16x16x32_f16 v[30:33], v[196:199], v[138:141], v[30:33]
	s_barrier
	ds_read_b128 v[130:133], v161
	ds_read_b128 v[212:215], v162
	ds_read_b128 v[160:163], v163
	ds_read_b128 v[216:219], v164
	s_barrier
	s_waitcnt lgkmcnt(0)
	v_mfma_f32_16x16x32_f16 v[14:17], v[166:169], v[130:133], v[14:17]
	v_mfma_f32_16x16x32_f16 v[78:81], v[200:203], v[130:133], v[78:81]
	v_mfma_f32_16x16x32_f16 v[14:17], v[176:179], v[212:215], v[14:17]
	v_mfma_f32_16x16x32_f16 v[22:25], v[166:169], v[160:163], v[22:25]
	v_mfma_f32_16x16x32_f16 v[34:37], v[180:183], v[130:133], v[34:37]
	v_mfma_f32_16x16x32_f16 v[46:49], v[180:183], v[160:163], v[46:49]
	v_mfma_f32_16x16x32_f16 v[58:61], v[188:191], v[130:133], v[58:61]
	v_mfma_f32_16x16x32_f16 v[70:73], v[188:191], v[160:163], v[70:73]
	v_mfma_f32_16x16x32_f16 v[164:167], v[204:207], v[212:215], v[78:81]
	v_mfma_f32_16x16x32_f16 v[78:81], v[200:203], v[160:163], v[86:89]
	v_mfma_f32_16x16x32_f16 v[22:25], v[176:179], v[216:219], v[22:25]
	v_mfma_f32_16x16x32_f16 v[34:37], v[184:187], v[212:215], v[34:37]
	v_mfma_f32_16x16x32_f16 v[46:49], v[184:187], v[216:219], v[46:49]
	v_mfma_f32_16x16x32_f16 v[58:61], v[196:199], v[212:215], v[58:61]
	v_mfma_f32_16x16x32_f16 v[70:73], v[196:199], v[216:219], v[70:73]
	v_mfma_f32_16x16x32_f16 v[86:89], v[204:207], v[216:219], v[78:81]
	s_barrier
	s_nop 0
	ds_read_b128 v[78:81], v173 offset:16384
	ds_read_b128 v[168:171], v173 offset:17408
	ds_read_b128 v[174:177], v173 offset:18432
	ds_read_b128 v[178:181], v173 offset:19456
	ds_read_b128 v[182:185], v173 offset:20480
	ds_read_b128 v[186:189], v173 offset:21504
	ds_read_b128 v[190:193], v173 offset:22528
	ds_read_b128 v[196:199], v173 offset:23552
	s_waitcnt vmcnt(4)
	s_barrier
	s_waitcnt lgkmcnt(0)
	v_mfma_f32_16x16x32_f16 v[26:29], v[78:81], v[134:137], v[26:29]
	v_mfma_f32_16x16x32_f16 v[38:41], v[78:81], v[152:155], v[38:41]
	v_mfma_f32_16x16x32_f16 v[26:29], v[168:171], v[138:141], v[26:29]
	v_mfma_f32_16x16x32_f16 v[38:41], v[168:171], v[156:159], v[38:41]
	v_mfma_f32_16x16x32_f16 v[50:53], v[174:177], v[134:137], v[50:53]
	v_mfma_f32_16x16x32_f16 v[62:65], v[174:177], v[152:155], v[62:65]
	v_mfma_f32_16x16x32_f16 v[74:77], v[182:185], v[134:137], v[74:77]
	v_mfma_f32_16x16x32_f16 v[82:85], v[182:185], v[152:155], v[82:85]
	v_mfma_f32_16x16x32_f16 v[90:93], v[190:193], v[134:137], v[90:93]
	v_mfma_f32_16x16x32_f16 v[94:97], v[190:193], v[152:155], v[94:97]
	v_mfma_f32_16x16x32_f16 v[50:53], v[178:181], v[138:141], v[50:53]
	v_mfma_f32_16x16x32_f16 v[62:65], v[178:181], v[156:159], v[62:65]
	v_mfma_f32_16x16x32_f16 v[74:77], v[186:189], v[138:141], v[74:77]
	v_mfma_f32_16x16x32_f16 v[82:85], v[186:189], v[156:159], v[82:85]
	v_mfma_f32_16x16x32_f16 v[90:93], v[196:199], v[138:141], v[90:93]
	v_mfma_f32_16x16x32_f16 v[94:97], v[196:199], v[156:159], v[94:97]
	v_mfma_f32_16x16x32_f16 v[98:101], v[78:81], v[130:133], v[98:101]
	v_mfma_f32_16x16x32_f16 v[78:81], v[78:81], v[160:163], v[102:105]
	v_mfma_f32_16x16x32_f16 v[102:105], v[168:171], v[216:219], v[78:81]
	v_mfma_f32_16x16x32_f16 v[78:81], v[174:177], v[130:133], v[106:109]
	v_mfma_f32_16x16x32_f16 v[106:109], v[178:181], v[212:215], v[78:81]
	v_mfma_f32_16x16x32_f16 v[78:81], v[174:177], v[160:163], v[110:113]
	v_mfma_f32_16x16x32_f16 v[200:203], v[178:181], v[216:219], v[78:81]
	v_mfma_f32_16x16x32_f16 v[78:81], v[182:185], v[130:133], v[114:117]
	v_mfma_f32_16x16x32_f16 v[204:207], v[186:189], v[212:215], v[78:81]
	v_mfma_f32_16x16x32_f16 v[78:81], v[182:185], v[160:163], v[118:121]
	v_mfma_f32_16x16x32_f16 v[220:223], v[186:189], v[216:219], v[78:81]
	v_mfma_f32_16x16x32_f16 v[78:81], v[190:193], v[130:133], v[122:125]
	v_mfma_f32_16x16x32_f16 v[98:101], v[168:171], v[212:215], v[98:101]
	v_mfma_f32_16x16x32_f16 v[212:215], v[196:199], v[212:215], v[78:81]
	v_mfma_f32_16x16x32_f16 v[78:81], v[190:193], v[160:163], v[126:129]
	v_mfma_f32_16x16x32_f16 v[196:199], v[196:199], v[216:219], v[78:81]
	s_barrier
	ds_read_b128 v[110:113], v148
	ds_read_b128 v[130:133], v149
	ds_read_b128 v[216:219], v150
	ds_read_b128 v[224:227], v151
	s_nop 0
	ds_read_b128 v[78:81], v173 offset:32768
	ds_read_b128 v[114:117], v173 offset:33792
	ds_read_b128 v[118:121], v173 offset:34816
	ds_read_b128 v[134:137], v173 offset:35840
	ds_read_b128 v[138:141], v173 offset:36864
	ds_read_b128 v[168:171], v173 offset:37888
	ds_read_b128 v[174:177], v173 offset:38912
	ds_read_b128 v[228:231], v173 offset:39936
	s_waitcnt vmcnt(2)
	s_barrier
	s_waitcnt lgkmcnt(0)
	v_mfma_f32_16x16x32_f16 v[2:5], v[78:81], v[110:113], v[2:5]
	v_mfma_f32_16x16x32_f16 v[190:193], v[114:117], v[130:133], v[2:5]
	v_mfma_f32_16x16x32_f16 v[2:5], v[78:81], v[216:219], v[6:9]
	v_mfma_f32_16x16x32_f16 v[158:161], v[114:117], v[224:227], v[2:5]
	v_mfma_f32_16x16x32_f16 v[2:5], v[118:121], v[110:113], v[10:13]
	v_mfma_f32_16x16x32_f16 v[186:189], v[134:137], v[130:133], v[2:5]
	v_mfma_f32_16x16x32_f16 v[2:5], v[118:121], v[216:219], v[18:21]
	v_mfma_f32_16x16x32_f16 v[154:157], v[134:137], v[224:227], v[2:5]
	v_mfma_f32_16x16x32_f16 v[2:5], v[138:141], v[110:113], v[30:33]
	v_mfma_f32_16x16x32_f16 v[182:185], v[168:171], v[130:133], v[2:5]
	v_mfma_f32_16x16x32_f16 v[2:5], v[138:141], v[216:219], v[42:45]
	v_mfma_f32_16x16x32_f16 v[150:153], v[168:171], v[224:227], v[2:5]
	v_mfma_f32_16x16x32_f16 v[2:5], v[174:177], v[110:113], v[54:57]
	v_mfma_f32_16x16x32_f16 v[178:181], v[228:231], v[130:133], v[2:5]
	v_mfma_f32_16x16x32_f16 v[2:5], v[174:177], v[216:219], v[66:69]
	v_mfma_f32_16x16x32_f16 v[146:149], v[228:231], v[224:227], v[2:5]
	s_barrier
	s_nop 4
	ds_read_b128 v[2:5], v142
	ds_read_b128 v[6:9], v143
	ds_read_b128 v[10:13], v144
	ds_read_b128 v[18:21], v145
	s_waitcnt vmcnt(0)
	s_barrier
	s_waitcnt lgkmcnt(0)
	v_mfma_f32_16x16x32_f16 v[14:17], v[78:81], v[2:5], v[14:17]
	v_mfma_f32_16x16x32_f16 v[126:129], v[114:117], v[6:9], v[14:17]
	v_mfma_f32_16x16x32_f16 v[14:17], v[78:81], v[10:13], v[22:25]
	v_mfma_f32_16x16x32_f16 v[78:81], v[114:117], v[18:21], v[14:17]
	v_mfma_f32_16x16x32_f16 v[14:17], v[118:121], v[2:5], v[34:37]
	v_mfma_f32_16x16x32_f16 v[122:125], v[134:137], v[6:9], v[14:17]
	v_mfma_f32_16x16x32_f16 v[14:17], v[118:121], v[10:13], v[46:49]
	v_mfma_f32_16x16x32_f16 v[66:69], v[134:137], v[18:21], v[14:17]
	v_mfma_f32_16x16x32_f16 v[14:17], v[138:141], v[2:5], v[58:61]
	v_mfma_f32_16x16x32_f16 v[118:121], v[168:171], v[6:9], v[14:17]
	v_mfma_f32_16x16x32_f16 v[14:17], v[138:141], v[10:13], v[70:73]
	v_mfma_f32_16x16x32_f16 v[54:57], v[168:171], v[18:21], v[14:17]
	v_mfma_f32_16x16x32_f16 v[14:17], v[174:177], v[2:5], v[164:167]
	v_mfma_f32_16x16x32_f16 v[114:117], v[228:231], v[6:9], v[14:17]
	v_mfma_f32_16x16x32_f16 v[14:17], v[174:177], v[10:13], v[86:89]
	v_mfma_f32_16x16x32_f16 v[42:45], v[228:231], v[18:21], v[14:17]
	s_barrier
	s_nop 4
	ds_read_b128 v[14:17], v173 offset:49152
	ds_read_b128 v[22:25], v173 offset:50176
	ds_read_b128 v[30:33], v173 offset:51200
	ds_read_b128 v[34:37], v173 offset:52224
	ds_read_b128 v[46:49], v173 offset:53248
	ds_read_b128 v[58:61], v173 offset:54272
	ds_read_b128 v[70:73], v173 offset:55296
	ds_read_b128 v[86:89], v173 offset:56320
	s_barrier
	s_waitcnt lgkmcnt(0)
	v_mfma_f32_16x16x32_f16 v[26:29], v[14:17], v[110:113], v[26:29]
	v_mfma_f32_16x16x32_f16 v[174:177], v[22:25], v[130:133], v[26:29]
	v_mfma_f32_16x16x32_f16 v[26:29], v[14:17], v[216:219], v[38:41]
	v_mfma_f32_16x16x32_f16 v[142:145], v[22:25], v[224:227], v[26:29]
	v_mfma_f32_16x16x32_f16 v[26:29], v[30:33], v[110:113], v[50:53]
	v_mfma_f32_16x16x32_f16 v[170:173], v[34:37], v[130:133], v[26:29]
	v_mfma_f32_16x16x32_f16 v[26:29], v[30:33], v[216:219], v[62:65]
	v_mfma_f32_16x16x32_f16 v[138:141], v[34:37], v[224:227], v[26:29]
	v_mfma_f32_16x16x32_f16 v[26:29], v[46:49], v[110:113], v[74:77]
	v_mfma_f32_16x16x32_f16 v[166:169], v[58:61], v[130:133], v[26:29]
	v_mfma_f32_16x16x32_f16 v[26:29], v[46:49], v[216:219], v[82:85]
	v_mfma_f32_16x16x32_f16 v[134:137], v[58:61], v[224:227], v[26:29]
	v_mfma_f32_16x16x32_f16 v[26:29], v[70:73], v[110:113], v[90:93]
	v_mfma_f32_16x16x32_f16 v[162:165], v[86:89], v[130:133], v[26:29]
	v_mfma_f32_16x16x32_f16 v[26:29], v[70:73], v[216:219], v[94:97]
	v_mfma_f32_16x16x32_f16 v[130:133], v[86:89], v[224:227], v[26:29]
	v_mfma_f32_16x16x32_f16 v[26:29], v[14:17], v[2:5], v[98:101]
	v_mfma_f32_16x16x32_f16 v[14:17], v[14:17], v[10:13], v[102:105]
	v_mfma_f32_16x16x32_f16 v[38:41], v[22:25], v[18:21], v[14:17]
	v_mfma_f32_16x16x32_f16 v[14:17], v[30:33], v[2:5], v[106:109]
	v_mfma_f32_16x16x32_f16 v[106:109], v[34:37], v[6:9], v[14:17]
	v_mfma_f32_16x16x32_f16 v[14:17], v[30:33], v[10:13], v[200:203]
	v_mfma_f32_16x16x32_f16 v[110:113], v[22:25], v[6:9], v[26:29]
	v_mfma_f32_16x16x32_f16 v[26:29], v[34:37], v[18:21], v[14:17]
	v_mfma_f32_16x16x32_f16 v[14:17], v[46:49], v[2:5], v[204:207]
	v_mfma_f32_16x16x32_f16 v[2:5], v[70:73], v[2:5], v[212:215]
	v_mfma_f32_16x16x32_f16 v[102:105], v[58:61], v[6:9], v[14:17]
	v_mfma_f32_16x16x32_f16 v[14:17], v[46:49], v[10:13], v[220:223]
	v_mfma_f32_16x16x32_f16 v[98:101], v[86:89], v[6:9], v[2:5]
	v_mfma_f32_16x16x32_f16 v[2:5], v[70:73], v[10:13], v[196:199]
	v_mfma_f32_16x16x32_f16 v[14:17], v[58:61], v[18:21], v[14:17]
	v_mfma_f32_16x16x32_f16 v[2:5], v[86:89], v[18:21], v[2:5]
	s_cmpk_gt_u32 s65, 0xff
	s_barrier
	s_cbranch_scc1 .LBB6_15
	s_barrier

.LBB7_238:
	v_lshlrev_b32_e32 v2, 12, v2
	s_lshl_b32 s50, s65, 6
	v_lshlrev_b32_e32 v6, 12, v6
	v_and_b32_e32 v2, 0xffffe000, v2
	s_lshl_b32 s5, s66, 13
	s_and_b32 s50, s50, 0x3000
	v_and_b32_e32 v6, 0xffffe000, v6
	v_lshl_add_u32 v2, v3, 9, v2
	v_and_b32_e32 v10, 48, v210
	v_lshlrev_b32_e32 v11, 6, v210
	v_lshl_add_u32 v6, v7, 9, v6
	s_add_u32 s48, s8, s48
	v_or_b32_e32 v2, v2, v4
	v_and_or_b32 v10, v11, s58, v10
	v_lshlrev_b32_e32 v11, 2, v210
	v_or_b32_e32 v6, v6, v8
	s_addc_u32 s49, s9, s49
	v_add_u32_sdwa v2, v2, sext(v5) dst_sel:DWORD dst_unused:UNUSED_PAD src0_sel:DWORD src1_sel:WORD_0
	v_and_b32_e32 v11, 32, v11
	v_add_u32_sdwa v6, v6, sext(v9) dst_sel:DWORD dst_unused:UNUSED_PAD src0_sel:DWORD src1_sel:WORD_0
	v_ashrrev_i32_e32 v3, 31, v2
	s_add_u32 s46, s10, s46
	v_xad_u32 v168, v10, v11, 0
	s_waitcnt vmcnt(6)
	v_ashrrev_i32_e32 v7, 31, v6
	v_lshlrev_b64 v[2:3], 1, v[2:3]
	s_addc_u32 s47, s11, s47
	v_add_u32_e32 v10, s50, v168
	v_lshlrev_b64 v[6:7], 1, v[6:7]
	v_lshl_add_u64 v[136:137], s[48:49], 0, v[2:3]
	v_lshl_add_u64 v[140:141], s[46:47], 0, v[2:3]
	v_mov_b32_e32 v2, 0
	v_add_u32_e32 v169, 0x10000, v10
	v_add_u32_e32 v170, 0x10400, v10
	v_add_u32_e32 v171, 0x10800, v10
	v_add_u32_e32 v172, 0x10c00, v10
	v_add_u32_e32 v161, 0x14000, v10
	v_add_u32_e32 v162, 0x14400, v10
	v_add_u32_e32 v163, 0x14800, v10
	v_add_u32_e32 v164, 0x14c00, v10
	v_add_u32_e32 v148, 0x18000, v10
	v_add_u32_e32 v149, 0x18400, v10
	v_add_u32_e32 v150, 0x18800, v10
	v_add_u32_e32 v151, 0x18c00, v10
	v_add_u32_e32 v142, 0x1c000, v10
	v_add_u32_e32 v143, 0x1c400, v10
	v_add_u32_e32 v144, 0x1c800, v10
	v_add_u32_e32 v145, 0x1cc00, v10
	v_lshl_add_u64 v[134:135], s[48:49], 0, v[6:7]
	v_lshl_add_u64 v[138:139], s[46:47], 0, v[6:7]
	s_mov_b32 s48, -2
	s_mov_b64 s[46:47], 0
	v_mov_b32_e32 v3, v2
	v_mov_b32_e32 v4, v2
	v_mov_b32_e32 v5, v2
	v_mov_b32_e32 v6, v2
	v_mov_b32_e32 v7, v2
	v_mov_b32_e32 v8, v2
	v_mov_b32_e32 v9, v2
	v_mov_b32_e32 v10, v2
	v_mov_b32_e32 v11, v2
	v_mov_b32_e32 v12, v2
	v_mov_b32_e32 v13, v2
	v_mov_b32_e32 v18, v2
	v_mov_b32_e32 v19, v2
	v_mov_b32_e32 v20, v2
	v_mov_b32_e32 v21, v2
	v_mov_b32_e32 v30, v2
	v_mov_b32_e32 v31, v2
	v_mov_b32_e32 v32, v2
	v_mov_b32_e32 v33, v2
	v_mov_b32_e32 v42, v2
	v_mov_b32_e32 v43, v2
	v_mov_b32_e32 v44, v2
	v_mov_b32_e32 v45, v2
	v_mov_b32_e32 v54, v2
	v_mov_b32_e32 v55, v2
	v_mov_b32_e32 v56, v2
	v_mov_b32_e32 v57, v2
	v_mov_b32_e32 v66, v2
	v_mov_b32_e32 v67, v2
	v_mov_b32_e32 v68, v2
	v_mov_b32_e32 v69, v2
	v_mov_b32_e32 v14, v2
	v_mov_b32_e32 v15, v2
	v_mov_b32_e32 v16, v2
	v_mov_b32_e32 v17, v2
	v_mov_b32_e32 v22, v2
	v_mov_b32_e32 v23, v2
	v_mov_b32_e32 v24, v2
	v_mov_b32_e32 v25, v2
	v_mov_b32_e32 v34, v2
	v_mov_b32_e32 v35, v2
	v_mov_b32_e32 v36, v2
	v_mov_b32_e32 v37, v2
	v_mov_b32_e32 v46, v2
	v_mov_b32_e32 v47, v2
	v_mov_b32_e32 v48, v2
	v_mov_b32_e32 v49, v2
	v_mov_b32_e32 v58, v2
	v_mov_b32_e32 v59, v2
	v_mov_b32_e32 v60, v2
	v_mov_b32_e32 v61, v2
	v_mov_b32_e32 v70, v2
	v_mov_b32_e32 v71, v2
	v_mov_b32_e32 v72, v2
	v_mov_b32_e32 v73, v2
	v_mov_b32_e32 v78, v2
	v_mov_b32_e32 v79, v2
	v_mov_b32_e32 v80, v2
	v_mov_b32_e32 v81, v2
	v_mov_b32_e32 v86, v2
	v_mov_b32_e32 v87, v2
	v_mov_b32_e32 v88, v2
	v_mov_b32_e32 v89, v2
	v_mov_b32_e32 v26, v2
	v_mov_b32_e32 v27, v2
	v_mov_b32_e32 v28, v2
	v_mov_b32_e32 v29, v2
	v_mov_b32_e32 v38, v2
	v_mov_b32_e32 v39, v2
	v_mov_b32_e32 v40, v2
	v_mov_b32_e32 v41, v2
	v_mov_b32_e32 v50, v2
	v_mov_b32_e32 v51, v2
	v_mov_b32_e32 v52, v2
	v_mov_b32_e32 v53, v2
	v_mov_b32_e32 v62, v2
	v_mov_b32_e32 v63, v2
	v_mov_b32_e32 v64, v2
	v_mov_b32_e32 v65, v2
	v_mov_b32_e32 v74, v2
	v_mov_b32_e32 v75, v2
	v_mov_b32_e32 v76, v2
	v_mov_b32_e32 v77, v2
	v_mov_b32_e32 v82, v2
	v_mov_b32_e32 v83, v2
	v_mov_b32_e32 v84, v2
	v_mov_b32_e32 v85, v2
	v_mov_b32_e32 v90, v2
	v_mov_b32_e32 v91, v2
	v_mov_b32_e32 v92, v2
	v_mov_b32_e32 v93, v2
	v_mov_b32_e32 v94, v2
	v_mov_b32_e32 v95, v2
	v_mov_b32_e32 v96, v2
	v_mov_b32_e32 v97, v2
	v_mov_b32_e32 v98, v2
	v_mov_b32_e32 v99, v2
	v_mov_b32_e32 v100, v2
	v_mov_b32_e32 v101, v2
	v_mov_b32_e32 v102, v2
	v_mov_b32_e32 v103, v2
	v_mov_b32_e32 v104, v2
	v_mov_b32_e32 v105, v2
	v_mov_b32_e32 v106, v2
	v_mov_b32_e32 v107, v2
	v_mov_b32_e32 v108, v2
	v_mov_b32_e32 v109, v2
	v_mov_b32_e32 v110, v2
	v_mov_b32_e32 v111, v2
	v_mov_b32_e32 v112, v2
	v_mov_b32_e32 v113, v2
	v_mov_b32_e32 v114, v2
	v_mov_b32_e32 v115, v2
	v_mov_b32_e32 v116, v2
	v_mov_b32_e32 v117, v2
	v_mov_b32_e32 v118, v2
	v_mov_b32_e32 v119, v2
	v_mov_b32_e32 v120, v2
	v_mov_b32_e32 v121, v2
	v_mov_b32_e32 v122, v2
	v_mov_b32_e32 v123, v2
	v_mov_b32_e32 v124, v2
	v_mov_b32_e32 v125, v2
	v_mov_b32_e32 v126, v2
	v_mov_b32_e32 v127, v2
	v_mov_b32_e32 v128, v2
	v_mov_b32_e32 v129, v2
	v_add_u32_e32 v174, 0xc000, v152
	v_add_u32_e32 v175, 0xe000, v152
	s_nop 0
	v_readfirstlane_b32 s72, v174
	v_readfirstlane_b32 s73, v175
	v_readfirstlane_b32 s74, v146
	v_readfirstlane_b32 s75, v147
	v_readfirstlane_b32 s76, v152
	v_readfirstlane_b32 s77, v153
	v_readfirstlane_b32 s78, v154
	v_readfirstlane_b32 s79, v155
	v_readfirstlane_b32 s80, v156
	v_readfirstlane_b32 s81, v157
	v_readfirstlane_b32 s82, v158
	v_readfirstlane_b32 s83, v159
	v_readfirstlane_b32 s84, v160
	v_readfirstlane_b32 s85, v165
	v_readfirstlane_b32 s86, v166
	v_readfirstlane_b32 s87, v167
	s_barrier
	s_barrier
	ds_read_b128 v[176:179], v169
	ds_read_b128 v[180:183], v170
	ds_read_b128 v[184:187], v171
	ds_read_b128 v[188:191], v172
.LBB7_239:
	v_add_u32_e32 v174, 0xc000, v152
	v_lshl_add_u64 v[192:193], v[136:137], 0, s[46:47]
	v_add_u32_e32 v175, 0xe000, v152
	v_add_u32_e32 v173, s5, v168
	v_lshl_add_u64 v[232:233], v[192:193], 0, s[34:35]
	s_mov_b32 m0, s72
	v_lshl_add_u64 v[248:249], v[134:135], 0, s[46:47]
	ds_read_b128 v[196:199], v173
	ds_read_b128 v[200:203], v173 offset:1024
	ds_read_b128 v[204:207], v173 offset:2048
	ds_read_b128 v[212:215], v173 offset:3072
	ds_read_b128 v[216:219], v173 offset:4096
	ds_read_b128 v[220:223], v173 offset:5120
	ds_read_b128 v[224:227], v173 offset:6144
	ds_read_b128 v[228:231], v173 offset:7168
	global_load_lds_dwordx4 v[232:233], off
	s_mov_b32 m0, s73
	v_lshl_add_u64 v[232:233], v[248:249], 0, s[34:35]
	global_load_lds_dwordx4 v[232:233], off
	s_waitcnt lgkmcnt(8)
	s_barrier
	s_waitcnt lgkmcnt(0)
	v_mfma_f32_16x16x32_f16 v[2:5], v[196:199], v[176:179], v[2:5]
	v_mfma_f32_16x16x32_f16 v[6:9], v[196:199], v[184:187], v[6:9]
	v_mfma_f32_16x16x32_f16 v[10:13], v[204:207], v[176:179], v[10:13]
	v_mfma_f32_16x16x32_f16 v[18:21], v[204:207], v[184:187], v[18:21]
	v_mfma_f32_16x16x32_f16 v[30:33], v[216:219], v[176:179], v[30:33]
	v_mfma_f32_16x16x32_f16 v[42:45], v[216:219], v[184:187], v[42:45]
	v_mfma_f32_16x16x32_f16 v[54:57], v[224:227], v[176:179], v[54:57]
	v_mfma_f32_16x16x32_f16 v[66:69], v[224:227], v[184:187], v[66:69]
	v_mfma_f32_16x16x32_f16 v[2:5], v[200:203], v[180:183], v[2:5]
	v_mfma_f32_16x16x32_f16 v[6:9], v[200:203], v[188:191], v[6:9]
	v_mfma_f32_16x16x32_f16 v[10:13], v[212:215], v[180:183], v[10:13]
	v_mfma_f32_16x16x32_f16 v[18:21], v[212:215], v[188:191], v[18:21]
	v_mfma_f32_16x16x32_f16 v[30:33], v[220:223], v[180:183], v[30:33]
	v_mfma_f32_16x16x32_f16 v[42:45], v[220:223], v[188:191], v[42:45]
	v_mfma_f32_16x16x32_f16 v[54:57], v[228:231], v[180:183], v[54:57]
	v_mfma_f32_16x16x32_f16 v[66:69], v[228:231], v[188:191], v[66:69]
	s_barrier
	v_lshl_add_u64 v[250:251], v[140:141], 0, s[46:47]
	v_lshl_add_u64 v[252:253], v[250:251], 0, s[36:37]
	s_mov_b32 m0, s74
	ds_read_b128 v[232:235], v161
	ds_read_b128 v[236:239], v162
	ds_read_b128 v[240:243], v163
	ds_read_b128 v[244:247], v164
	global_load_lds_dwordx4 v[252:253], off
	v_lshl_add_u64 v[252:253], v[138:139], 0, s[46:47]
	s_mov_b32 m0, s75
	v_lshl_add_u64 v[254:255], v[252:253], 0, s[36:37]
	global_load_lds_dwordx4 v[254:255], off
	s_barrier
	s_waitcnt lgkmcnt(0)
	v_mfma_f32_16x16x32_f16 v[14:17], v[196:199], v[232:235], v[14:17]
	v_mfma_f32_16x16x32_f16 v[22:25], v[196:199], v[240:243], v[22:25]
	v_mfma_f32_16x16x32_f16 v[34:37], v[204:207], v[232:235], v[34:37]
	v_mfma_f32_16x16x32_f16 v[46:49], v[204:207], v[240:243], v[46:49]
	v_mfma_f32_16x16x32_f16 v[58:61], v[216:219], v[232:235], v[58:61]
	v_mfma_f32_16x16x32_f16 v[70:73], v[216:219], v[240:243], v[70:73]
	v_mfma_f32_16x16x32_f16 v[78:81], v[224:227], v[232:235], v[78:81]
	v_mfma_f32_16x16x32_f16 v[86:89], v[224:227], v[240:243], v[86:89]
	v_mfma_f32_16x16x32_f16 v[14:17], v[200:203], v[236:239], v[14:17]
	v_mfma_f32_16x16x32_f16 v[22:25], v[200:203], v[244:247], v[22:25]
	v_mfma_f32_16x16x32_f16 v[34:37], v[212:215], v[236:239], v[34:37]
	v_mfma_f32_16x16x32_f16 v[46:49], v[212:215], v[244:247], v[46:49]
	v_mfma_f32_16x16x32_f16 v[58:61], v[220:223], v[236:239], v[58:61]
	v_mfma_f32_16x16x32_f16 v[70:73], v[220:223], v[244:247], v[70:73]
	v_mfma_f32_16x16x32_f16 v[78:81], v[228:231], v[236:239], v[78:81]
	v_mfma_f32_16x16x32_f16 v[86:89], v[228:231], v[244:247], v[86:89]
	v_lshl_add_u64 v[254:255], v[192:193], 0, s[36:37]
	s_mov_b32 m0, s76
	s_barrier
	ds_read_b128 v[196:199], v173 offset:16384
	ds_read_b128 v[200:203], v173 offset:17408
	ds_read_b128 v[204:207], v173 offset:18432
	ds_read_b128 v[212:215], v173 offset:19456
	ds_read_b128 v[216:219], v173 offset:20480
	ds_read_b128 v[220:223], v173 offset:21504
	ds_read_b128 v[224:227], v173 offset:22528
	ds_read_b128 v[228:231], v173 offset:23552
	global_load_lds_dwordx4 v[254:255], off
	s_mov_b32 m0, s77
	v_lshl_add_u64 v[254:255], v[248:249], 0, s[36:37]
	global_load_lds_dwordx4 v[254:255], off
	s_waitcnt vmcnt(10)
	s_barrier
	s_waitcnt lgkmcnt(0)
	v_mfma_f32_16x16x32_f16 v[26:29], v[196:199], v[176:179], v[26:29]
	v_mfma_f32_16x16x32_f16 v[38:41], v[196:199], v[184:187], v[38:41]
	v_mfma_f32_16x16x32_f16 v[50:53], v[204:207], v[176:179], v[50:53]
	v_mfma_f32_16x16x32_f16 v[62:65], v[204:207], v[184:187], v[62:65]
	v_mfma_f32_16x16x32_f16 v[74:77], v[216:219], v[176:179], v[74:77]
	v_mfma_f32_16x16x32_f16 v[82:85], v[216:219], v[184:187], v[82:85]
	v_mfma_f32_16x16x32_f16 v[90:93], v[224:227], v[176:179], v[90:93]
	v_mfma_f32_16x16x32_f16 v[94:97], v[224:227], v[184:187], v[94:97]
	v_mfma_f32_16x16x32_f16 v[26:29], v[200:203], v[180:183], v[26:29]
	v_mfma_f32_16x16x32_f16 v[38:41], v[200:203], v[188:191], v[38:41]
	v_mfma_f32_16x16x32_f16 v[50:53], v[212:215], v[180:183], v[50:53]
	v_mfma_f32_16x16x32_f16 v[62:65], v[212:215], v[188:191], v[62:65]
	v_mfma_f32_16x16x32_f16 v[74:77], v[220:223], v[180:183], v[74:77]
	v_mfma_f32_16x16x32_f16 v[82:85], v[220:223], v[188:191], v[82:85]
	v_mfma_f32_16x16x32_f16 v[90:93], v[228:231], v[180:183], v[90:93]
	v_mfma_f32_16x16x32_f16 v[94:97], v[228:231], v[188:191], v[94:97]
	s_barrier
	s_mov_b32 m0, s78
	v_lshl_add_u64 v[176:177], v[250:251], 0, s[38:39]
	global_load_lds_dwordx4 v[176:177], off
	s_mov_b32 m0, s79
	v_lshl_add_u64 v[176:177], v[252:253], 0, s[38:39]
	global_load_lds_dwordx4 v[176:177], off
	s_waitcnt vmcnt(6)
	s_barrier
	v_mfma_f32_16x16x32_f16 v[98:101], v[196:199], v[232:235], v[98:101]
	v_mfma_f32_16x16x32_f16 v[102:105], v[196:199], v[240:243], v[102:105]
	v_mfma_f32_16x16x32_f16 v[106:109], v[204:207], v[232:235], v[106:109]
	v_mfma_f32_16x16x32_f16 v[110:113], v[204:207], v[240:243], v[110:113]
	v_mfma_f32_16x16x32_f16 v[114:117], v[216:219], v[232:235], v[114:117]
	v_mfma_f32_16x16x32_f16 v[118:121], v[216:219], v[240:243], v[118:121]
	v_mfma_f32_16x16x32_f16 v[122:125], v[224:227], v[232:235], v[122:125]
	v_mfma_f32_16x16x32_f16 v[126:129], v[224:227], v[240:243], v[126:129]
	v_mfma_f32_16x16x32_f16 v[98:101], v[200:203], v[236:239], v[98:101]
	v_mfma_f32_16x16x32_f16 v[102:105], v[200:203], v[244:247], v[102:105]
	v_mfma_f32_16x16x32_f16 v[106:109], v[212:215], v[236:239], v[106:109]
	v_mfma_f32_16x16x32_f16 v[110:113], v[212:215], v[244:247], v[110:113]
	ds_read_b128 v[176:179], v148
	ds_read_b128 v[180:183], v149
	ds_read_b128 v[184:187], v150
	ds_read_b128 v[188:191], v151
	v_mfma_f32_16x16x32_f16 v[114:117], v[220:223], v[236:239], v[114:117]
	v_mfma_f32_16x16x32_f16 v[118:121], v[220:223], v[244:247], v[118:121]
	v_mfma_f32_16x16x32_f16 v[122:125], v[228:231], v[236:239], v[122:125]
	v_mfma_f32_16x16x32_f16 v[126:129], v[228:231], v[244:247], v[126:129]
	s_barrier
	v_lshl_add_u64 v[232:233], v[192:193], 0, s[38:39]
	s_mov_b32 m0, s80
	ds_read_b128 v[196:199], v173 offset:32768
	ds_read_b128 v[200:203], v173 offset:33792
	ds_read_b128 v[204:207], v173 offset:34816
	ds_read_b128 v[212:215], v173 offset:35840
	ds_read_b128 v[216:219], v173 offset:36864
	ds_read_b128 v[220:223], v173 offset:37888
	ds_read_b128 v[224:227], v173 offset:38912
	ds_read_b128 v[228:231], v173 offset:39936
	global_load_lds_dwordx4 v[232:233], off
	s_mov_b32 m0, s81
	v_lshl_add_u64 v[232:233], v[248:249], 0, s[38:39]
	global_load_lds_dwordx4 v[232:233], off
	s_waitcnt lgkmcnt(8)
	s_barrier
	s_waitcnt lgkmcnt(0)
	v_mfma_f32_16x16x32_f16 v[2:5], v[196:199], v[176:179], v[2:5]
	v_mfma_f32_16x16x32_f16 v[6:9], v[196:199], v[184:187], v[6:9]
	v_mfma_f32_16x16x32_f16 v[10:13], v[204:207], v[176:179], v[10:13]
	v_mfma_f32_16x16x32_f16 v[18:21], v[204:207], v[184:187], v[18:21]
	v_mfma_f32_16x16x32_f16 v[30:33], v[216:219], v[176:179], v[30:33]
	v_mfma_f32_16x16x32_f16 v[42:45], v[216:219], v[184:187], v[42:45]
	v_mfma_f32_16x16x32_f16 v[54:57], v[224:227], v[176:179], v[54:57]
	v_mfma_f32_16x16x32_f16 v[66:69], v[224:227], v[184:187], v[66:69]
	v_mfma_f32_16x16x32_f16 v[2:5], v[200:203], v[180:183], v[2:5]
	v_mfma_f32_16x16x32_f16 v[6:9], v[200:203], v[188:191], v[6:9]
	v_mfma_f32_16x16x32_f16 v[10:13], v[212:215], v[180:183], v[10:13]
	v_mfma_f32_16x16x32_f16 v[18:21], v[212:215], v[188:191], v[18:21]
	v_mfma_f32_16x16x32_f16 v[30:33], v[220:223], v[180:183], v[30:33]
	v_mfma_f32_16x16x32_f16 v[42:45], v[220:223], v[188:191], v[42:45]
	v_mfma_f32_16x16x32_f16 v[54:57], v[228:231], v[180:183], v[54:57]
	v_mfma_f32_16x16x32_f16 v[66:69], v[228:231], v[188:191], v[66:69]
	s_barrier
	v_lshl_add_u64 v[254:255], v[250:251], 0, s[40:41]
	s_mov_b32 m0, s82
	ds_read_b128 v[232:235], v142
	ds_read_b128 v[236:239], v143
	ds_read_b128 v[240:243], v144
	ds_read_b128 v[244:247], v145
	global_load_lds_dwordx4 v[254:255], off
	s_mov_b32 m0, s83
	v_lshl_add_u64 v[254:255], v[252:253], 0, s[40:41]
	global_load_lds_dwordx4 v[254:255], off
	s_barrier
	s_waitcnt lgkmcnt(0)
	v_mfma_f32_16x16x32_f16 v[14:17], v[196:199], v[232:235], v[14:17]
	v_mfma_f32_16x16x32_f16 v[22:25], v[196:199], v[240:243], v[22:25]
	v_mfma_f32_16x16x32_f16 v[34:37], v[204:207], v[232:235], v[34:37]
	v_mfma_f32_16x16x32_f16 v[46:49], v[204:207], v[240:243], v[46:49]
	v_mfma_f32_16x16x32_f16 v[58:61], v[216:219], v[232:235], v[58:61]
	v_mfma_f32_16x16x32_f16 v[70:73], v[216:219], v[240:243], v[70:73]
	v_mfma_f32_16x16x32_f16 v[78:81], v[224:227], v[232:235], v[78:81]
	v_mfma_f32_16x16x32_f16 v[86:89], v[224:227], v[240:243], v[86:89]
	v_mfma_f32_16x16x32_f16 v[14:17], v[200:203], v[236:239], v[14:17]
	v_mfma_f32_16x16x32_f16 v[22:25], v[200:203], v[244:247], v[22:25]
	v_mfma_f32_16x16x32_f16 v[34:37], v[212:215], v[236:239], v[34:37]
	v_mfma_f32_16x16x32_f16 v[46:49], v[212:215], v[244:247], v[46:49]
	v_mfma_f32_16x16x32_f16 v[58:61], v[220:223], v[236:239], v[58:61]
	v_mfma_f32_16x16x32_f16 v[70:73], v[220:223], v[244:247], v[70:73]
	v_mfma_f32_16x16x32_f16 v[78:81], v[228:231], v[236:239], v[78:81]
	v_mfma_f32_16x16x32_f16 v[86:89], v[228:231], v[244:247], v[86:89]
	v_lshl_add_u64 v[192:193], v[192:193], 0, s[40:41]
	s_mov_b32 m0, s84
	s_barrier
	ds_read_b128 v[196:199], v173 offset:49152
	ds_read_b128 v[200:203], v173 offset:50176
	ds_read_b128 v[204:207], v173 offset:51200
	ds_read_b128 v[212:215], v173 offset:52224
	ds_read_b128 v[216:219], v173 offset:53248
	ds_read_b128 v[220:223], v173 offset:54272
	ds_read_b128 v[224:227], v173 offset:55296
	ds_read_b128 v[228:231], v173 offset:56320
	global_load_lds_dwordx4 v[192:193], off
	s_mov_b32 m0, s85
	v_lshl_add_u64 v[192:193], v[248:249], 0, s[40:41]
	global_load_lds_dwordx4 v[192:193], off
	s_waitcnt vmcnt(10)
	s_barrier
	s_waitcnt lgkmcnt(0)
	v_mfma_f32_16x16x32_f16 v[26:29], v[196:199], v[176:179], v[26:29]
	v_mfma_f32_16x16x32_f16 v[38:41], v[196:199], v[184:187], v[38:41]
	v_mfma_f32_16x16x32_f16 v[50:53], v[204:207], v[176:179], v[50:53]
	v_mfma_f32_16x16x32_f16 v[62:65], v[204:207], v[184:187], v[62:65]
	v_mfma_f32_16x16x32_f16 v[74:77], v[216:219], v[176:179], v[74:77]
	v_mfma_f32_16x16x32_f16 v[82:85], v[216:219], v[184:187], v[82:85]
	v_mfma_f32_16x16x32_f16 v[90:93], v[224:227], v[176:179], v[90:93]
	v_mfma_f32_16x16x32_f16 v[94:97], v[224:227], v[184:187], v[94:97]
	v_mfma_f32_16x16x32_f16 v[26:29], v[200:203], v[180:183], v[26:29]
	v_mfma_f32_16x16x32_f16 v[38:41], v[200:203], v[188:191], v[38:41]
	v_mfma_f32_16x16x32_f16 v[50:53], v[212:215], v[180:183], v[50:53]
	v_mfma_f32_16x16x32_f16 v[62:65], v[212:215], v[188:191], v[62:65]
	v_mfma_f32_16x16x32_f16 v[74:77], v[220:223], v[180:183], v[74:77]
	v_mfma_f32_16x16x32_f16 v[82:85], v[220:223], v[188:191], v[82:85]
	v_mfma_f32_16x16x32_f16 v[90:93], v[228:231], v[180:183], v[90:93]
	v_mfma_f32_16x16x32_f16 v[94:97], v[228:231], v[188:191], v[94:97]
	s_barrier
	s_mov_b32 m0, s86
	v_lshl_add_u64 v[176:177], v[250:251], 0, s[42:43]
	global_load_lds_dwordx4 v[176:177], off
	s_mov_b32 m0, s87
	v_lshl_add_u64 v[176:177], v[252:253], 0, s[42:43]
	global_load_lds_dwordx4 v[176:177], off
	s_waitcnt vmcnt(6)
	s_barrier
	v_mfma_f32_16x16x32_f16 v[98:101], v[196:199], v[232:235], v[98:101]
	v_mfma_f32_16x16x32_f16 v[102:105], v[196:199], v[240:243], v[102:105]
	v_mfma_f32_16x16x32_f16 v[106:109], v[204:207], v[232:235], v[106:109]
	v_mfma_f32_16x16x32_f16 v[110:113], v[204:207], v[240:243], v[110:113]
	v_mfma_f32_16x16x32_f16 v[114:117], v[216:219], v[232:235], v[114:117]
	v_mfma_f32_16x16x32_f16 v[118:121], v[216:219], v[240:243], v[118:121]
	v_mfma_f32_16x16x32_f16 v[122:125], v[224:227], v[232:235], v[122:125]
	v_mfma_f32_16x16x32_f16 v[126:129], v[224:227], v[240:243], v[126:129]
	v_mfma_f32_16x16x32_f16 v[98:101], v[200:203], v[236:239], v[98:101]
	v_mfma_f32_16x16x32_f16 v[102:105], v[200:203], v[244:247], v[102:105]
	v_mfma_f32_16x16x32_f16 v[106:109], v[212:215], v[236:239], v[106:109]
	v_mfma_f32_16x16x32_f16 v[110:113], v[212:215], v[244:247], v[110:113]
	ds_read_b128 v[176:179], v169
	ds_read_b128 v[180:183], v170
	ds_read_b128 v[184:187], v171
	ds_read_b128 v[188:191], v172
	v_mfma_f32_16x16x32_f16 v[114:117], v[220:223], v[236:239], v[114:117]
	v_mfma_f32_16x16x32_f16 v[118:121], v[220:223], v[244:247], v[118:121]
	v_mfma_f32_16x16x32_f16 v[122:125], v[228:231], v[236:239], v[122:125]
	v_mfma_f32_16x16x32_f16 v[126:129], v[228:231], v[244:247], v[126:129]
	s_add_i32 s48, s48, 2
	s_add_u32 s46, s46, 0x100
	s_addc_u32 s47, s47, 0
	s_cmp_lt_u32 s48, 4
	s_barrier
	s_cbranch_scc1 .LBB7_239
	s_add_u32 s0, s0, 0x20380
	s_addc_u32 s1, s1, 0
	v_readfirstlane_b32 s5, v174
	v_lshl_add_u64 v[130:131], v[130:131], 1, s[0:1]
	s_mov_b32 m0, s5
	ds_read_b128 v[134:137], v169
	ds_read_b128 v[138:141], v170
	ds_read_b128 v[152:155], v171
	ds_read_b128 v[156:159], v172
	ds_read_b128 v[166:169], v173
	ds_read_b128 v[176:179], v173 offset:1024
	ds_read_b128 v[180:183], v173 offset:2048
	ds_read_b128 v[184:187], v173 offset:3072
	ds_read_b128 v[188:191], v173 offset:4096
	ds_read_b128 v[196:199], v173 offset:5120
	ds_read_b128 v[200:203], v173 offset:6144
	ds_read_b128 v[204:207], v173 offset:7168
	global_load_lds_dwordx4 v[130:131], off
	v_lshl_add_u64 v[130:131], v[132:133], 1, s[0:1]
	v_readfirstlane_b32 s0, v175
	s_mov_b32 m0, s0
	s_nop 0
	global_load_lds_dwordx4 v[130:131], off
	s_barrier
	s_waitcnt lgkmcnt(0)
	v_mfma_f32_16x16x32_f16 v[2:5], v[166:169], v[134:137], v[2:5]
	v_mfma_f32_16x16x32_f16 v[42:45], v[188:191], v[152:155], v[42:45]
	v_mfma_f32_16x16x32_f16 v[54:57], v[200:203], v[134:137], v[54:57]
	v_mfma_f32_16x16x32_f16 v[66:69], v[200:203], v[152:155], v[66:69]
	v_mfma_f32_16x16x32_f16 v[2:5], v[176:179], v[138:141], v[2:5]
	v_mfma_f32_16x16x32_f16 v[6:9], v[166:169], v[152:155], v[6:9]
	v_mfma_f32_16x16x32_f16 v[10:13], v[180:183], v[134:137], v[10:13]
	v_mfma_f32_16x16x32_f16 v[18:21], v[180:183], v[152:155], v[18:21]
	v_mfma_f32_16x16x32_f16 v[30:33], v[188:191], v[134:137], v[30:33]
	v_mfma_f32_16x16x32_f16 v[42:45], v[196:199], v[156:159], v[42:45]
	v_mfma_f32_16x16x32_f16 v[54:57], v[204:207], v[138:141], v[54:57]
	v_mfma_f32_16x16x32_f16 v[66:69], v[204:207], v[156:159], v[66:69]
	v_mfma_f32_16x16x32_f16 v[6:9], v[176:179], v[156:159], v[6:9]
	v_mfma_f32_16x16x32_f16 v[10:13], v[184:187], v[138:141], v[10:13]
	v_mfma_f32_16x16x32_f16 v[18:21], v[184:187], v[156:159], v[18:21]
	v_mfma_f32_16x16x32_f16 v[30:33], v[196:199], v[138:141], v[30:33]
	s_barrier
	ds_read_b128 v[130:133], v161
	ds_read_b128 v[212:215], v162
	ds_read_b128 v[160:163], v163
	ds_read_b128 v[216:219], v164
	s_barrier
	s_waitcnt lgkmcnt(0)
	v_mfma_f32_16x16x32_f16 v[14:17], v[166:169], v[130:133], v[14:17]
	v_mfma_f32_16x16x32_f16 v[78:81], v[200:203], v[130:133], v[78:81]
	v_mfma_f32_16x16x32_f16 v[14:17], v[176:179], v[212:215], v[14:17]
	v_mfma_f32_16x16x32_f16 v[22:25], v[166:169], v[160:163], v[22:25]
	v_mfma_f32_16x16x32_f16 v[34:37], v[180:183], v[130:133], v[34:37]
	v_mfma_f32_16x16x32_f16 v[46:49], v[180:183], v[160:163], v[46:49]
	v_mfma_f32_16x16x32_f16 v[58:61], v[188:191], v[130:133], v[58:61]
	v_mfma_f32_16x16x32_f16 v[70:73], v[188:191], v[160:163], v[70:73]
	v_mfma_f32_16x16x32_f16 v[164:167], v[204:207], v[212:215], v[78:81]
	v_mfma_f32_16x16x32_f16 v[78:81], v[200:203], v[160:163], v[86:89]
	v_mfma_f32_16x16x32_f16 v[22:25], v[176:179], v[216:219], v[22:25]
	v_mfma_f32_16x16x32_f16 v[34:37], v[184:187], v[212:215], v[34:37]
	v_mfma_f32_16x16x32_f16 v[46:49], v[184:187], v[216:219], v[46:49]
	v_mfma_f32_16x16x32_f16 v[58:61], v[196:199], v[212:215], v[58:61]
	v_mfma_f32_16x16x32_f16 v[70:73], v[196:199], v[216:219], v[70:73]
	v_mfma_f32_16x16x32_f16 v[86:89], v[204:207], v[216:219], v[78:81]
	s_barrier
	s_nop 0
	ds_read_b128 v[78:81], v173 offset:16384
	ds_read_b128 v[168:171], v173 offset:17408
	ds_read_b128 v[174:177], v173 offset:18432
	ds_read_b128 v[178:181], v173 offset:19456
	ds_read_b128 v[182:185], v173 offset:20480
	ds_read_b128 v[186:189], v173 offset:21504
	ds_read_b128 v[190:193], v173 offset:22528
	ds_read_b128 v[196:199], v173 offset:23552
	s_waitcnt vmcnt(4)
	s_barrier
	s_waitcnt lgkmcnt(0)
	v_mfma_f32_16x16x32_f16 v[26:29], v[78:81], v[134:137], v[26:29]
	v_mfma_f32_16x16x32_f16 v[38:41], v[78:81], v[152:155], v[38:41]
	v_mfma_f32_16x16x32_f16 v[26:29], v[168:171], v[138:141], v[26:29]
	v_mfma_f32_16x16x32_f16 v[38:41], v[168:171], v[156:159], v[38:41]
	v_mfma_f32_16x16x32_f16 v[50:53], v[174:177], v[134:137], v[50:53]
	v_mfma_f32_16x16x32_f16 v[62:65], v[174:177], v[152:155], v[62:65]
	v_mfma_f32_16x16x32_f16 v[74:77], v[182:185], v[134:137], v[74:77]
	v_mfma_f32_16x16x32_f16 v[82:85], v[182:185], v[152:155], v[82:85]
	v_mfma_f32_16x16x32_f16 v[90:93], v[190:193], v[134:137], v[90:93]
	v_mfma_f32_16x16x32_f16 v[94:97], v[190:193], v[152:155], v[94:97]
	v_mfma_f32_16x16x32_f16 v[50:53], v[178:181], v[138:141], v[50:53]
	v_mfma_f32_16x16x32_f16 v[62:65], v[178:181], v[156:159], v[62:65]
	v_mfma_f32_16x16x32_f16 v[74:77], v[186:189], v[138:141], v[74:77]
	v_mfma_f32_16x16x32_f16 v[82:85], v[186:189], v[156:159], v[82:85]
	v_mfma_f32_16x16x32_f16 v[90:93], v[196:199], v[138:141], v[90:93]
	v_mfma_f32_16x16x32_f16 v[94:97], v[196:199], v[156:159], v[94:97]
	v_mfma_f32_16x16x32_f16 v[98:101], v[78:81], v[130:133], v[98:101]
	v_mfma_f32_16x16x32_f16 v[78:81], v[78:81], v[160:163], v[102:105]
	v_mfma_f32_16x16x32_f16 v[102:105], v[168:171], v[216:219], v[78:81]
	v_mfma_f32_16x16x32_f16 v[78:81], v[174:177], v[130:133], v[106:109]
	v_mfma_f32_16x16x32_f16 v[106:109], v[178:181], v[212:215], v[78:81]
	v_mfma_f32_16x16x32_f16 v[78:81], v[174:177], v[160:163], v[110:113]
	v_mfma_f32_16x16x32_f16 v[200:203], v[178:181], v[216:219], v[78:81]
	v_mfma_f32_16x16x32_f16 v[78:81], v[182:185], v[130:133], v[114:117]
	v_mfma_f32_16x16x32_f16 v[204:207], v[186:189], v[212:215], v[78:81]
	v_mfma_f32_16x16x32_f16 v[78:81], v[182:185], v[160:163], v[118:121]
	v_mfma_f32_16x16x32_f16 v[220:223], v[186:189], v[216:219], v[78:81]
	v_mfma_f32_16x16x32_f16 v[78:81], v[190:193], v[130:133], v[122:125]
	v_mfma_f32_16x16x32_f16 v[98:101], v[168:171], v[212:215], v[98:101]
	v_mfma_f32_16x16x32_f16 v[212:215], v[196:199], v[212:215], v[78:81]
	v_mfma_f32_16x16x32_f16 v[78:81], v[190:193], v[160:163], v[126:129]
	v_mfma_f32_16x16x32_f16 v[196:199], v[196:199], v[216:219], v[78:81]
	s_barrier
	ds_read_b128 v[110:113], v148
	ds_read_b128 v[130:133], v149
	ds_read_b128 v[216:219], v150
	ds_read_b128 v[224:227], v151
	s_nop 0
	ds_read_b128 v[78:81], v173 offset:32768
	ds_read_b128 v[114:117], v173 offset:33792
	ds_read_b128 v[118:121], v173 offset:34816
	ds_read_b128 v[134:137], v173 offset:35840
	ds_read_b128 v[138:141], v173 offset:36864
	ds_read_b128 v[168:171], v173 offset:37888
	ds_read_b128 v[174:177], v173 offset:38912
	ds_read_b128 v[228:231], v173 offset:39936
	s_waitcnt vmcnt(2)
	s_barrier
	s_waitcnt lgkmcnt(0)
	v_mfma_f32_16x16x32_f16 v[2:5], v[78:81], v[110:113], v[2:5]
	v_mfma_f32_16x16x32_f16 v[190:193], v[114:117], v[130:133], v[2:5]
	v_mfma_f32_16x16x32_f16 v[2:5], v[78:81], v[216:219], v[6:9]
	v_mfma_f32_16x16x32_f16 v[158:161], v[114:117], v[224:227], v[2:5]
	v_mfma_f32_16x16x32_f16 v[2:5], v[118:121], v[110:113], v[10:13]
	v_mfma_f32_16x16x32_f16 v[186:189], v[134:137], v[130:133], v[2:5]
	v_mfma_f32_16x16x32_f16 v[2:5], v[118:121], v[216:219], v[18:21]
	v_mfma_f32_16x16x32_f16 v[154:157], v[134:137], v[224:227], v[2:5]
	v_mfma_f32_16x16x32_f16 v[2:5], v[138:141], v[110:113], v[30:33]
	v_mfma_f32_16x16x32_f16 v[182:185], v[168:171], v[130:133], v[2:5]
	v_mfma_f32_16x16x32_f16 v[2:5], v[138:141], v[216:219], v[42:45]
	v_mfma_f32_16x16x32_f16 v[150:153], v[168:171], v[224:227], v[2:5]
	v_mfma_f32_16x16x32_f16 v[2:5], v[174:177], v[110:113], v[54:57]
	v_mfma_f32_16x16x32_f16 v[178:181], v[228:231], v[130:133], v[2:5]
	v_mfma_f32_16x16x32_f16 v[2:5], v[174:177], v[216:219], v[66:69]
	v_mfma_f32_16x16x32_f16 v[146:149], v[228:231], v[224:227], v[2:5]
	s_barrier
	s_nop 4
	ds_read_b128 v[2:5], v142
	ds_read_b128 v[6:9], v143
	ds_read_b128 v[10:13], v144
	ds_read_b128 v[18:21], v145
	s_waitcnt vmcnt(0)
	s_barrier
	s_waitcnt lgkmcnt(0)
	v_mfma_f32_16x16x32_f16 v[14:17], v[78:81], v[2:5], v[14:17]
	v_mfma_f32_16x16x32_f16 v[126:129], v[114:117], v[6:9], v[14:17]
	v_mfma_f32_16x16x32_f16 v[14:17], v[78:81], v[10:13], v[22:25]
	v_mfma_f32_16x16x32_f16 v[78:81], v[114:117], v[18:21], v[14:17]
	v_mfma_f32_16x16x32_f16 v[14:17], v[118:121], v[2:5], v[34:37]
	v_mfma_f32_16x16x32_f16 v[122:125], v[134:137], v[6:9], v[14:17]
	v_mfma_f32_16x16x32_f16 v[14:17], v[118:121], v[10:13], v[46:49]
	v_mfma_f32_16x16x32_f16 v[66:69], v[134:137], v[18:21], v[14:17]
	v_mfma_f32_16x16x32_f16 v[14:17], v[138:141], v[2:5], v[58:61]
	v_mfma_f32_16x16x32_f16 v[118:121], v[168:171], v[6:9], v[14:17]
	v_mfma_f32_16x16x32_f16 v[14:17], v[138:141], v[10:13], v[70:73]
	v_mfma_f32_16x16x32_f16 v[54:57], v[168:171], v[18:21], v[14:17]
	v_mfma_f32_16x16x32_f16 v[14:17], v[174:177], v[2:5], v[164:167]
	v_mfma_f32_16x16x32_f16 v[114:117], v[228:231], v[6:9], v[14:17]
	v_mfma_f32_16x16x32_f16 v[14:17], v[174:177], v[10:13], v[86:89]
	v_mfma_f32_16x16x32_f16 v[42:45], v[228:231], v[18:21], v[14:17]
	s_barrier
	s_nop 4
	ds_read_b128 v[14:17], v173 offset:49152
	ds_read_b128 v[22:25], v173 offset:50176
	ds_read_b128 v[30:33], v173 offset:51200
	ds_read_b128 v[34:37], v173 offset:52224
	ds_read_b128 v[46:49], v173 offset:53248
	ds_read_b128 v[58:61], v173 offset:54272
	ds_read_b128 v[70:73], v173 offset:55296
	ds_read_b128 v[86:89], v173 offset:56320
	s_barrier
	s_waitcnt lgkmcnt(0)
	v_mfma_f32_16x16x32_f16 v[26:29], v[14:17], v[110:113], v[26:29]
	v_mfma_f32_16x16x32_f16 v[174:177], v[22:25], v[130:133], v[26:29]
	v_mfma_f32_16x16x32_f16 v[26:29], v[14:17], v[216:219], v[38:41]
	v_mfma_f32_16x16x32_f16 v[142:145], v[22:25], v[224:227], v[26:29]
	v_mfma_f32_16x16x32_f16 v[26:29], v[30:33], v[110:113], v[50:53]
	v_mfma_f32_16x16x32_f16 v[170:173], v[34:37], v[130:133], v[26:29]
	v_mfma_f32_16x16x32_f16 v[26:29], v[30:33], v[216:219], v[62:65]
	v_mfma_f32_16x16x32_f16 v[138:141], v[34:37], v[224:227], v[26:29]
	v_mfma_f32_16x16x32_f16 v[26:29], v[46:49], v[110:113], v[74:77]
	v_mfma_f32_16x16x32_f16 v[166:169], v[58:61], v[130:133], v[26:29]
	v_mfma_f32_16x16x32_f16 v[26:29], v[46:49], v[216:219], v[82:85]
	v_mfma_f32_16x16x32_f16 v[134:137], v[58:61], v[224:227], v[26:29]
	v_mfma_f32_16x16x32_f16 v[26:29], v[70:73], v[110:113], v[90:93]
	v_mfma_f32_16x16x32_f16 v[162:165], v[86:89], v[130:133], v[26:29]
	v_mfma_f32_16x16x32_f16 v[26:29], v[70:73], v[216:219], v[94:97]
	v_mfma_f32_16x16x32_f16 v[130:133], v[86:89], v[224:227], v[26:29]
	v_mfma_f32_16x16x32_f16 v[26:29], v[14:17], v[2:5], v[98:101]
	v_mfma_f32_16x16x32_f16 v[14:17], v[14:17], v[10:13], v[102:105]
	v_mfma_f32_16x16x32_f16 v[38:41], v[22:25], v[18:21], v[14:17]
	v_mfma_f32_16x16x32_f16 v[14:17], v[30:33], v[2:5], v[106:109]
	v_mfma_f32_16x16x32_f16 v[106:109], v[34:37], v[6:9], v[14:17]
	v_mfma_f32_16x16x32_f16 v[14:17], v[30:33], v[10:13], v[200:203]
	v_mfma_f32_16x16x32_f16 v[110:113], v[22:25], v[6:9], v[26:29]
	v_mfma_f32_16x16x32_f16 v[26:29], v[34:37], v[18:21], v[14:17]
	v_mfma_f32_16x16x32_f16 v[14:17], v[46:49], v[2:5], v[204:207]
	v_mfma_f32_16x16x32_f16 v[2:5], v[70:73], v[2:5], v[212:215]
	v_mfma_f32_16x16x32_f16 v[102:105], v[58:61], v[6:9], v[14:17]
	v_mfma_f32_16x16x32_f16 v[14:17], v[46:49], v[10:13], v[220:223]
	v_mfma_f32_16x16x32_f16 v[98:101], v[86:89], v[6:9], v[2:5]
	v_mfma_f32_16x16x32_f16 v[2:5], v[70:73], v[10:13], v[196:199]
	v_mfma_f32_16x16x32_f16 v[14:17], v[58:61], v[18:21], v[14:17]
	v_mfma_f32_16x16x32_f16 v[2:5], v[86:89], v[18:21], v[2:5]
	s_cmpk_gt_u32 s65, 0xff
	s_barrier
	s_cbranch_scc1 .LBB7_242
	s_barrier

.LBB8_40:
	v_lshlrev_b32_e32 v2, 12, v2
	s_lshl_b32 s49, s62, 6
	v_and_b32_e32 v2, 0xffffe000, v2
	v_lshlrev_b32_e32 v4, 12, v4
	s_lshl_b32 s48, s64, 13
	s_and_b32 s49, s49, 0x3000
	v_lshl_add_u32 v2, v3, 9, v2
	v_and_b32_e32 v4, 0xffffe000, v4
	v_and_b32_e32 v10, 48, v172
	v_lshlrev_b32_e32 v11, 6, v172
	v_or_b32_e32 v2, v2, v5
	s_add_u32 s46, s24, s46
	v_lshl_add_u32 v4, v7, 9, v4
	v_and_or_b32 v10, v11, s57, v10
	v_lshlrev_b32_e32 v11, 2, v172
	v_add_u32_sdwa v2, v2, sext(v6) dst_sel:DWORD dst_unused:UNUSED_PAD src0_sel:DWORD src1_sel:WORD_0
	s_addc_u32 s47, s25, s47
	v_or_b32_e32 v4, v4, v8
	v_and_b32_e32 v11, 32, v11
	v_ashrrev_i32_e32 v3, 31, v2
	v_add_u32_sdwa v4, v4, sext(v9) dst_sel:DWORD dst_unused:UNUSED_PAD src0_sel:DWORD src1_sel:WORD_0
	s_add_u32 s44, s22, s44
	v_xad_u32 v170, v10, v11, 0
	s_waitcnt vmcnt(6)
	v_lshlrev_b64 v[2:3], 1, v[2:3]
	v_ashrrev_i32_e32 v5, 31, v4
	s_addc_u32 s45, s23, s45
	v_add_u32_e32 v10, s49, v170
	v_lshl_add_u64 v[134:135], s[46:47], 0, v[2:3]
	v_lshlrev_b64 v[4:5], 1, v[4:5]
	v_lshl_add_u64 v[138:139], s[44:45], 0, v[2:3]
	v_mov_b32_e32 v2, 0
	v_add_u32_e32 v171, 0x10000, v10
	v_add_u32_e32 v173, 0x10400, v10
	v_add_u32_e32 v174, 0x10800, v10
	v_add_u32_e32 v175, 0x10c00, v10
	v_add_u32_e32 v162, 0x14000, v10
	v_add_u32_e32 v163, 0x14400, v10
	v_add_u32_e32 v164, 0x14800, v10
	v_add_u32_e32 v165, 0x14c00, v10
	v_add_u32_e32 v144, 0x18000, v10
	v_add_u32_e32 v145, 0x18400, v10
	v_add_u32_e32 v146, 0x18800, v10
	v_add_u32_e32 v147, 0x18c00, v10
	v_add_u32_e32 v150, 0x1c000, v10
	v_add_u32_e32 v151, 0x1c400, v10
	v_add_u32_e32 v152, 0x1c800, v10
	v_add_u32_e32 v153, 0x1cc00, v10
	v_lshl_add_u64 v[136:137], s[46:47], 0, v[4:5]
	v_lshl_add_u64 v[140:141], s[44:45], 0, v[4:5]
	s_mov_b32 s46, -2
	s_mov_b64 s[44:45], 0
	v_mov_b32_e32 v3, v2
	v_mov_b32_e32 v4, v2
	v_mov_b32_e32 v5, v2
	v_mov_b32_e32 v6, v2
	v_mov_b32_e32 v7, v2
	v_mov_b32_e32 v8, v2
	v_mov_b32_e32 v9, v2
	v_mov_b32_e32 v10, v2
	v_mov_b32_e32 v11, v2
	v_mov_b32_e32 v12, v2
	v_mov_b32_e32 v13, v2
	v_mov_b32_e32 v14, v2
	v_mov_b32_e32 v15, v2
	v_mov_b32_e32 v16, v2
	v_mov_b32_e32 v17, v2
	v_mov_b32_e32 v18, v2
	v_mov_b32_e32 v19, v2
	v_mov_b32_e32 v20, v2
	v_mov_b32_e32 v21, v2
	v_mov_b32_e32 v22, v2
	v_mov_b32_e32 v23, v2
	v_mov_b32_e32 v24, v2
	v_mov_b32_e32 v25, v2
	v_mov_b32_e32 v26, v2
	v_mov_b32_e32 v27, v2
	v_mov_b32_e32 v28, v2
	v_mov_b32_e32 v29, v2
	v_mov_b32_e32 v30, v2
	v_mov_b32_e32 v31, v2
	v_mov_b32_e32 v32, v2
	v_mov_b32_e32 v33, v2
	v_mov_b32_e32 v34, v2
	v_mov_b32_e32 v35, v2
	v_mov_b32_e32 v36, v2
	v_mov_b32_e32 v37, v2
	v_mov_b32_e32 v38, v2
	v_mov_b32_e32 v39, v2
	v_mov_b32_e32 v40, v2
	v_mov_b32_e32 v41, v2
	v_mov_b32_e32 v42, v2
	v_mov_b32_e32 v43, v2
	v_mov_b32_e32 v44, v2
	v_mov_b32_e32 v45, v2
	v_mov_b32_e32 v46, v2
	v_mov_b32_e32 v47, v2
	v_mov_b32_e32 v48, v2
	v_mov_b32_e32 v49, v2
	v_mov_b32_e32 v50, v2
	v_mov_b32_e32 v51, v2
	v_mov_b32_e32 v52, v2
	v_mov_b32_e32 v53, v2
	v_mov_b32_e32 v54, v2
	v_mov_b32_e32 v55, v2
	v_mov_b32_e32 v56, v2
	v_mov_b32_e32 v57, v2
	v_mov_b32_e32 v58, v2
	v_mov_b32_e32 v59, v2
	v_mov_b32_e32 v60, v2
	v_mov_b32_e32 v61, v2
	v_mov_b32_e32 v62, v2
	v_mov_b32_e32 v63, v2
	v_mov_b32_e32 v64, v2
	v_mov_b32_e32 v65, v2
	v_mov_b32_e32 v66, v2
	v_mov_b32_e32 v67, v2
	v_mov_b32_e32 v68, v2
	v_mov_b32_e32 v69, v2
	v_mov_b32_e32 v70, v2
	v_mov_b32_e32 v71, v2
	v_mov_b32_e32 v72, v2
	v_mov_b32_e32 v73, v2
	v_mov_b32_e32 v74, v2
	v_mov_b32_e32 v75, v2
	v_mov_b32_e32 v76, v2
	v_mov_b32_e32 v77, v2
	v_mov_b32_e32 v78, v2
	v_mov_b32_e32 v79, v2
	v_mov_b32_e32 v80, v2
	v_mov_b32_e32 v81, v2
	v_mov_b32_e32 v82, v2
	v_mov_b32_e32 v83, v2
	v_mov_b32_e32 v84, v2
	v_mov_b32_e32 v85, v2
	v_mov_b32_e32 v86, v2
	v_mov_b32_e32 v87, v2
	v_mov_b32_e32 v88, v2
	v_mov_b32_e32 v89, v2
	v_mov_b32_e32 v90, v2
	v_mov_b32_e32 v91, v2
	v_mov_b32_e32 v92, v2
	v_mov_b32_e32 v93, v2
	v_mov_b32_e32 v94, v2
	v_mov_b32_e32 v95, v2
	v_mov_b32_e32 v96, v2
	v_mov_b32_e32 v97, v2
	v_mov_b32_e32 v98, v2
	v_mov_b32_e32 v99, v2
	v_mov_b32_e32 v100, v2
	v_mov_b32_e32 v101, v2
	v_mov_b32_e32 v102, v2
	v_mov_b32_e32 v103, v2
	v_mov_b32_e32 v104, v2
	v_mov_b32_e32 v105, v2
	v_mov_b32_e32 v106, v2
	v_mov_b32_e32 v107, v2
	v_mov_b32_e32 v108, v2
	v_mov_b32_e32 v109, v2
	v_mov_b32_e32 v110, v2
	v_mov_b32_e32 v111, v2
	v_mov_b32_e32 v112, v2
	v_mov_b32_e32 v113, v2
	v_mov_b32_e32 v114, v2
	v_mov_b32_e32 v115, v2
	v_mov_b32_e32 v116, v2
	v_mov_b32_e32 v117, v2
	v_mov_b32_e32 v118, v2
	v_mov_b32_e32 v119, v2
	v_mov_b32_e32 v120, v2
	v_mov_b32_e32 v121, v2
	v_mov_b32_e32 v122, v2
	v_mov_b32_e32 v123, v2
	v_mov_b32_e32 v124, v2
	v_mov_b32_e32 v125, v2
	v_mov_b32_e32 v126, v2
	v_mov_b32_e32 v127, v2
	v_mov_b32_e32 v128, v2
	v_mov_b32_e32 v129, v2
	v_add_u32_e32 v177, 0xc000, v148
	v_add_u32_e32 v178, 0xe000, v148
	s_nop 0
	v_readfirstlane_b32 s75, v177
	v_readfirstlane_b32 s76, v178
	v_readfirstlane_b32 s77, v142
	v_readfirstlane_b32 s78, v143
	v_readfirstlane_b32 s79, v148
	v_readfirstlane_b32 s80, v149
	v_readfirstlane_b32 s81, v154
	v_readfirstlane_b32 s82, v155
	v_readfirstlane_b32 s83, v156
	v_readfirstlane_b32 s84, v157
	v_readfirstlane_b32 s85, v158
	v_readfirstlane_b32 s86, v160
	v_readfirstlane_b32 s87, v161
	v_readfirstlane_b32 s88, v166
	v_readfirstlane_b32 s89, v168
	v_readfirstlane_b32 s90, v169
	s_barrier
	s_barrier
	ds_read_b128 v[182:185], v171
	ds_read_b128 v[186:189], v173
	ds_read_b128 v[190:193], v174
	ds_read_b128 v[194:197], v175
.LBB8_41:
	v_add_u32_e32 v177, 0xc000, v148
	v_lshl_add_u64 v[246:247], v[134:135], 0, s[44:45]
	v_add_u32_e32 v176, s48, v170
	v_lshl_add_u64 v[178:179], v[246:247], 0, s[28:29]
	s_mov_b32 m0, s75
	ds_read_b128 v[198:201], v176
	ds_read_b128 v[202:205], v176 offset:1024
	ds_read_b128 v[206:209], v176 offset:2048
	ds_read_b128 v[210:213], v176 offset:3072
	ds_read_b128 v[214:217], v176 offset:4096
	ds_read_b128 v[218:221], v176 offset:5120
	ds_read_b128 v[222:225], v176 offset:6144
	ds_read_b128 v[226:229], v176 offset:7168
	global_load_lds_dwordx4 v[178:179], off
	v_add_u32_e32 v178, 0xe000, v148
	v_lshl_add_u64 v[248:249], v[136:137], 0, s[44:45]
	s_mov_b32 m0, s76
	v_lshl_add_u64 v[230:231], v[248:249], 0, s[28:29]
	global_load_lds_dwordx4 v[230:231], off
	s_waitcnt lgkmcnt(8)
	s_barrier
	s_waitcnt lgkmcnt(0)
	v_mfma_f32_16x16x32_f16 v[126:129], v[198:201], v[182:185], v[126:129]
	v_mfma_f32_16x16x32_f16 v[122:125], v[198:201], v[190:193], v[122:125]
	v_mfma_f32_16x16x32_f16 v[118:121], v[206:209], v[182:185], v[118:121]
	v_mfma_f32_16x16x32_f16 v[114:117], v[206:209], v[190:193], v[114:117]
	v_mfma_f32_16x16x32_f16 v[110:113], v[214:217], v[182:185], v[110:113]
	v_mfma_f32_16x16x32_f16 v[106:109], v[214:217], v[190:193], v[106:109]
	v_mfma_f32_16x16x32_f16 v[102:105], v[222:225], v[182:185], v[102:105]
	v_mfma_f32_16x16x32_f16 v[98:101], v[222:225], v[190:193], v[98:101]
	v_mfma_f32_16x16x32_f16 v[126:129], v[202:205], v[186:189], v[126:129]
	v_mfma_f32_16x16x32_f16 v[122:125], v[202:205], v[194:197], v[122:125]
	v_mfma_f32_16x16x32_f16 v[118:121], v[210:213], v[186:189], v[118:121]
	v_mfma_f32_16x16x32_f16 v[114:117], v[210:213], v[194:197], v[114:117]
	v_mfma_f32_16x16x32_f16 v[110:113], v[218:221], v[186:189], v[110:113]
	v_mfma_f32_16x16x32_f16 v[106:109], v[218:221], v[194:197], v[106:109]
	v_mfma_f32_16x16x32_f16 v[102:105], v[226:229], v[186:189], v[102:105]
	v_mfma_f32_16x16x32_f16 v[98:101], v[226:229], v[194:197], v[98:101]
	s_barrier
	v_lshl_add_u64 v[250:251], v[138:139], 0, s[44:45]
	v_lshl_add_u64 v[252:253], v[250:251], 0, s[30:31]
	s_mov_b32 m0, s77
	ds_read_b128 v[230:233], v162
	ds_read_b128 v[234:237], v163
	ds_read_b128 v[238:241], v164
	ds_read_b128 v[242:245], v165
	global_load_lds_dwordx4 v[252:253], off
	v_lshl_add_u64 v[252:253], v[140:141], 0, s[44:45]
	s_mov_b32 m0, s78
	v_lshl_add_u64 v[254:255], v[252:253], 0, s[30:31]
	global_load_lds_dwordx4 v[254:255], off
	s_barrier
	s_waitcnt lgkmcnt(0)
	v_mfma_f32_16x16x32_f16 v[94:97], v[198:201], v[230:233], v[94:97]
	v_mfma_f32_16x16x32_f16 v[90:93], v[198:201], v[238:241], v[90:93]
	v_mfma_f32_16x16x32_f16 v[86:89], v[206:209], v[230:233], v[86:89]
	v_mfma_f32_16x16x32_f16 v[82:85], v[206:209], v[238:241], v[82:85]
	v_mfma_f32_16x16x32_f16 v[78:81], v[214:217], v[230:233], v[78:81]
	v_mfma_f32_16x16x32_f16 v[74:77], v[214:217], v[238:241], v[74:77]
	v_mfma_f32_16x16x32_f16 v[70:73], v[222:225], v[230:233], v[70:73]
	v_mfma_f32_16x16x32_f16 v[66:69], v[222:225], v[238:241], v[66:69]
	v_mfma_f32_16x16x32_f16 v[94:97], v[202:205], v[234:237], v[94:97]
	v_mfma_f32_16x16x32_f16 v[90:93], v[202:205], v[242:245], v[90:93]
	v_mfma_f32_16x16x32_f16 v[86:89], v[210:213], v[234:237], v[86:89]
	v_mfma_f32_16x16x32_f16 v[82:85], v[210:213], v[242:245], v[82:85]
	v_mfma_f32_16x16x32_f16 v[78:81], v[218:221], v[234:237], v[78:81]
	v_mfma_f32_16x16x32_f16 v[74:77], v[218:221], v[242:245], v[74:77]
	v_mfma_f32_16x16x32_f16 v[70:73], v[226:229], v[234:237], v[70:73]
	v_mfma_f32_16x16x32_f16 v[66:69], v[226:229], v[242:245], v[66:69]
	v_lshl_add_u64 v[254:255], v[246:247], 0, s[30:31]
	s_mov_b32 m0, s79
	s_barrier
	ds_read_b128 v[198:201], v176 offset:16384
	ds_read_b128 v[202:205], v176 offset:17408
	ds_read_b128 v[206:209], v176 offset:18432
	ds_read_b128 v[210:213], v176 offset:19456
	ds_read_b128 v[214:217], v176 offset:20480
	ds_read_b128 v[218:221], v176 offset:21504
	ds_read_b128 v[222:225], v176 offset:22528
	ds_read_b128 v[226:229], v176 offset:23552
	global_load_lds_dwordx4 v[254:255], off
	s_mov_b32 m0, s80
	v_lshl_add_u64 v[254:255], v[248:249], 0, s[30:31]
	global_load_lds_dwordx4 v[254:255], off
	s_waitcnt vmcnt(10)
	s_barrier
	s_waitcnt lgkmcnt(0)
	v_mfma_f32_16x16x32_f16 v[62:65], v[198:201], v[182:185], v[62:65]
	v_mfma_f32_16x16x32_f16 v[58:61], v[198:201], v[190:193], v[58:61]
	v_mfma_f32_16x16x32_f16 v[54:57], v[206:209], v[182:185], v[54:57]
	v_mfma_f32_16x16x32_f16 v[50:53], v[206:209], v[190:193], v[50:53]
	v_mfma_f32_16x16x32_f16 v[46:49], v[214:217], v[182:185], v[46:49]
	v_mfma_f32_16x16x32_f16 v[42:45], v[214:217], v[190:193], v[42:45]
	v_mfma_f32_16x16x32_f16 v[38:41], v[222:225], v[182:185], v[38:41]
	v_mfma_f32_16x16x32_f16 v[34:37], v[222:225], v[190:193], v[34:37]
	v_mfma_f32_16x16x32_f16 v[62:65], v[202:205], v[186:189], v[62:65]
	v_mfma_f32_16x16x32_f16 v[58:61], v[202:205], v[194:197], v[58:61]
	v_mfma_f32_16x16x32_f16 v[54:57], v[210:213], v[186:189], v[54:57]
	v_mfma_f32_16x16x32_f16 v[50:53], v[210:213], v[194:197], v[50:53]
	v_mfma_f32_16x16x32_f16 v[46:49], v[218:221], v[186:189], v[46:49]
	v_mfma_f32_16x16x32_f16 v[42:45], v[218:221], v[194:197], v[42:45]
	v_mfma_f32_16x16x32_f16 v[38:41], v[226:229], v[186:189], v[38:41]
	v_mfma_f32_16x16x32_f16 v[34:37], v[226:229], v[194:197], v[34:37]
	s_barrier
	s_mov_b32 m0, s81
	v_lshl_add_u64 v[182:183], v[250:251], 0, s[34:35]
	global_load_lds_dwordx4 v[182:183], off
	s_mov_b32 m0, s82
	v_lshl_add_u64 v[182:183], v[252:253], 0, s[34:35]
	global_load_lds_dwordx4 v[182:183], off
	s_waitcnt vmcnt(6)
	s_barrier
	v_mfma_f32_16x16x32_f16 v[30:33], v[198:201], v[230:233], v[30:33]
	v_mfma_f32_16x16x32_f16 v[26:29], v[198:201], v[238:241], v[26:29]
	v_mfma_f32_16x16x32_f16 v[22:25], v[206:209], v[230:233], v[22:25]
	v_mfma_f32_16x16x32_f16 v[18:21], v[206:209], v[238:241], v[18:21]
	v_mfma_f32_16x16x32_f16 v[14:17], v[214:217], v[230:233], v[14:17]
	v_mfma_f32_16x16x32_f16 v[10:13], v[214:217], v[238:241], v[10:13]
	v_mfma_f32_16x16x32_f16 v[6:9], v[222:225], v[230:233], v[6:9]
	v_mfma_f32_16x16x32_f16 v[2:5], v[222:225], v[238:241], v[2:5]
	v_mfma_f32_16x16x32_f16 v[30:33], v[202:205], v[234:237], v[30:33]
	v_mfma_f32_16x16x32_f16 v[26:29], v[202:205], v[242:245], v[26:29]
	v_mfma_f32_16x16x32_f16 v[22:25], v[210:213], v[234:237], v[22:25]
	v_mfma_f32_16x16x32_f16 v[18:21], v[210:213], v[242:245], v[18:21]
	ds_read_b128 v[182:185], v144
	ds_read_b128 v[186:189], v145
	ds_read_b128 v[190:193], v146
	ds_read_b128 v[194:197], v147
	v_mfma_f32_16x16x32_f16 v[14:17], v[218:221], v[234:237], v[14:17]
	v_mfma_f32_16x16x32_f16 v[10:13], v[218:221], v[242:245], v[10:13]
	v_mfma_f32_16x16x32_f16 v[6:9], v[226:229], v[234:237], v[6:9]
	v_mfma_f32_16x16x32_f16 v[2:5], v[226:229], v[242:245], v[2:5]
	s_barrier
	v_lshl_add_u64 v[230:231], v[246:247], 0, s[34:35]
	s_mov_b32 m0, s83
	ds_read_b128 v[198:201], v176 offset:32768
	ds_read_b128 v[202:205], v176 offset:33792
	ds_read_b128 v[206:209], v176 offset:34816
	ds_read_b128 v[210:213], v176 offset:35840
	ds_read_b128 v[214:217], v176 offset:36864
	ds_read_b128 v[218:221], v176 offset:37888
	ds_read_b128 v[222:225], v176 offset:38912
	ds_read_b128 v[226:229], v176 offset:39936
	global_load_lds_dwordx4 v[230:231], off
	s_mov_b32 m0, s84
	v_lshl_add_u64 v[230:231], v[248:249], 0, s[34:35]
	global_load_lds_dwordx4 v[230:231], off
	s_waitcnt lgkmcnt(8)
	s_barrier
	s_waitcnt lgkmcnt(0)
	v_mfma_f32_16x16x32_f16 v[126:129], v[198:201], v[182:185], v[126:129]
	v_mfma_f32_16x16x32_f16 v[122:125], v[198:201], v[190:193], v[122:125]
	v_mfma_f32_16x16x32_f16 v[118:121], v[206:209], v[182:185], v[118:121]
	v_mfma_f32_16x16x32_f16 v[114:117], v[206:209], v[190:193], v[114:117]
	v_mfma_f32_16x16x32_f16 v[110:113], v[214:217], v[182:185], v[110:113]
	v_mfma_f32_16x16x32_f16 v[106:109], v[214:217], v[190:193], v[106:109]
	v_mfma_f32_16x16x32_f16 v[102:105], v[222:225], v[182:185], v[102:105]
	v_mfma_f32_16x16x32_f16 v[98:101], v[222:225], v[190:193], v[98:101]
	v_mfma_f32_16x16x32_f16 v[126:129], v[202:205], v[186:189], v[126:129]
	v_mfma_f32_16x16x32_f16 v[122:125], v[202:205], v[194:197], v[122:125]
	v_mfma_f32_16x16x32_f16 v[118:121], v[210:213], v[186:189], v[118:121]
	v_mfma_f32_16x16x32_f16 v[114:117], v[210:213], v[194:197], v[114:117]
	v_mfma_f32_16x16x32_f16 v[110:113], v[218:221], v[186:189], v[110:113]
	v_mfma_f32_16x16x32_f16 v[106:109], v[218:221], v[194:197], v[106:109]
	v_mfma_f32_16x16x32_f16 v[102:105], v[226:229], v[186:189], v[102:105]
	v_mfma_f32_16x16x32_f16 v[98:101], v[226:229], v[194:197], v[98:101]
	s_barrier
	v_lshl_add_u64 v[254:255], v[250:251], 0, s[36:37]
	s_mov_b32 m0, s85
	ds_read_b128 v[230:233], v150
	ds_read_b128 v[234:237], v151
	ds_read_b128 v[238:241], v152
	ds_read_b128 v[242:245], v153
	global_load_lds_dwordx4 v[254:255], off
	s_mov_b32 m0, s86
	v_lshl_add_u64 v[254:255], v[252:253], 0, s[36:37]
	global_load_lds_dwordx4 v[254:255], off
	s_barrier
	s_waitcnt lgkmcnt(0)
	v_mfma_f32_16x16x32_f16 v[94:97], v[198:201], v[230:233], v[94:97]
	v_mfma_f32_16x16x32_f16 v[90:93], v[198:201], v[238:241], v[90:93]
	v_mfma_f32_16x16x32_f16 v[86:89], v[206:209], v[230:233], v[86:89]
	v_mfma_f32_16x16x32_f16 v[82:85], v[206:209], v[238:241], v[82:85]
	v_mfma_f32_16x16x32_f16 v[78:81], v[214:217], v[230:233], v[78:81]
	v_mfma_f32_16x16x32_f16 v[74:77], v[214:217], v[238:241], v[74:77]
	v_mfma_f32_16x16x32_f16 v[70:73], v[222:225], v[230:233], v[70:73]
	v_mfma_f32_16x16x32_f16 v[66:69], v[222:225], v[238:241], v[66:69]
	v_mfma_f32_16x16x32_f16 v[94:97], v[202:205], v[234:237], v[94:97]
	v_mfma_f32_16x16x32_f16 v[90:93], v[202:205], v[242:245], v[90:93]
	v_mfma_f32_16x16x32_f16 v[86:89], v[210:213], v[234:237], v[86:89]
	v_mfma_f32_16x16x32_f16 v[82:85], v[210:213], v[242:245], v[82:85]
	v_mfma_f32_16x16x32_f16 v[78:81], v[218:221], v[234:237], v[78:81]
	v_mfma_f32_16x16x32_f16 v[74:77], v[218:221], v[242:245], v[74:77]
	v_mfma_f32_16x16x32_f16 v[70:73], v[226:229], v[234:237], v[70:73]
	v_mfma_f32_16x16x32_f16 v[66:69], v[226:229], v[242:245], v[66:69]
	v_lshl_add_u64 v[246:247], v[246:247], 0, s[36:37]
	s_mov_b32 m0, s87
	s_barrier
	ds_read_b128 v[198:201], v176 offset:49152
	ds_read_b128 v[202:205], v176 offset:50176
	ds_read_b128 v[206:209], v176 offset:51200
	ds_read_b128 v[210:213], v176 offset:52224
	ds_read_b128 v[214:217], v176 offset:53248
	ds_read_b128 v[218:221], v176 offset:54272
	ds_read_b128 v[222:225], v176 offset:55296
	ds_read_b128 v[226:229], v176 offset:56320
	global_load_lds_dwordx4 v[246:247], off
	s_mov_b32 m0, s88
	v_lshl_add_u64 v[246:247], v[248:249], 0, s[36:37]
	global_load_lds_dwordx4 v[246:247], off
	s_waitcnt vmcnt(10)
	s_barrier
	s_waitcnt lgkmcnt(0)
	v_mfma_f32_16x16x32_f16 v[62:65], v[198:201], v[182:185], v[62:65]
	v_mfma_f32_16x16x32_f16 v[58:61], v[198:201], v[190:193], v[58:61]
	v_mfma_f32_16x16x32_f16 v[54:57], v[206:209], v[182:185], v[54:57]
	v_mfma_f32_16x16x32_f16 v[50:53], v[206:209], v[190:193], v[50:53]
	v_mfma_f32_16x16x32_f16 v[46:49], v[214:217], v[182:185], v[46:49]
	v_mfma_f32_16x16x32_f16 v[42:45], v[214:217], v[190:193], v[42:45]
	v_mfma_f32_16x16x32_f16 v[38:41], v[222:225], v[182:185], v[38:41]
	v_mfma_f32_16x16x32_f16 v[34:37], v[222:225], v[190:193], v[34:37]
	v_mfma_f32_16x16x32_f16 v[62:65], v[202:205], v[186:189], v[62:65]
	v_mfma_f32_16x16x32_f16 v[58:61], v[202:205], v[194:197], v[58:61]
	v_mfma_f32_16x16x32_f16 v[54:57], v[210:213], v[186:189], v[54:57]
	v_mfma_f32_16x16x32_f16 v[50:53], v[210:213], v[194:197], v[50:53]
	v_mfma_f32_16x16x32_f16 v[46:49], v[218:221], v[186:189], v[46:49]
	v_mfma_f32_16x16x32_f16 v[42:45], v[218:221], v[194:197], v[42:45]
	v_mfma_f32_16x16x32_f16 v[38:41], v[226:229], v[186:189], v[38:41]
	v_mfma_f32_16x16x32_f16 v[34:37], v[226:229], v[194:197], v[34:37]
	s_barrier
	s_mov_b32 m0, s89
	v_lshl_add_u64 v[182:183], v[250:251], 0, s[38:39]
	global_load_lds_dwordx4 v[182:183], off
	s_mov_b32 m0, s90
	v_lshl_add_u64 v[182:183], v[252:253], 0, s[38:39]
	global_load_lds_dwordx4 v[182:183], off
	s_waitcnt vmcnt(6)
	s_barrier
	v_mfma_f32_16x16x32_f16 v[30:33], v[198:201], v[230:233], v[30:33]
	v_mfma_f32_16x16x32_f16 v[26:29], v[198:201], v[238:241], v[26:29]
	v_mfma_f32_16x16x32_f16 v[22:25], v[206:209], v[230:233], v[22:25]
	v_mfma_f32_16x16x32_f16 v[18:21], v[206:209], v[238:241], v[18:21]
	v_mfma_f32_16x16x32_f16 v[14:17], v[214:217], v[230:233], v[14:17]
	v_mfma_f32_16x16x32_f16 v[10:13], v[214:217], v[238:241], v[10:13]
	v_mfma_f32_16x16x32_f16 v[6:9], v[222:225], v[230:233], v[6:9]
	v_mfma_f32_16x16x32_f16 v[2:5], v[222:225], v[238:241], v[2:5]
	v_mfma_f32_16x16x32_f16 v[30:33], v[202:205], v[234:237], v[30:33]
	v_mfma_f32_16x16x32_f16 v[26:29], v[202:205], v[242:245], v[26:29]
	v_mfma_f32_16x16x32_f16 v[22:25], v[210:213], v[234:237], v[22:25]
	v_mfma_f32_16x16x32_f16 v[18:21], v[210:213], v[242:245], v[18:21]
	ds_read_b128 v[182:185], v171
	ds_read_b128 v[186:189], v173
	ds_read_b128 v[190:193], v174
	ds_read_b128 v[194:197], v175
	v_mfma_f32_16x16x32_f16 v[14:17], v[218:221], v[234:237], v[14:17]
	v_mfma_f32_16x16x32_f16 v[10:13], v[218:221], v[242:245], v[10:13]
	v_mfma_f32_16x16x32_f16 v[6:9], v[226:229], v[234:237], v[6:9]
	v_mfma_f32_16x16x32_f16 v[2:5], v[226:229], v[242:245], v[2:5]
	s_add_i32 s46, s46, 2
	s_add_u32 s44, s44, 0x100
	s_addc_u32 s45, s45, 0
	s_cmp_lt_u32 s46, 4
	s_barrier
	s_cbranch_scc1 .LBB8_41
	s_add_u32 s42, s42, 0x20380
	s_addc_u32 s43, s43, 0
	v_readfirstlane_b32 s44, v177
	v_lshl_add_u64 v[130:131], v[130:131], 1, s[42:43]
	s_mov_b32 m0, s44
	ds_read_b128 v[134:137], v171
	ds_read_b128 v[138:141], v173
	ds_read_b128 v[154:157], v174
	ds_read_b128 v[168:171], v175
	ds_read_b128 v[182:185], v176
	ds_read_b128 v[186:189], v176 offset:1024
	ds_read_b128 v[190:193], v176 offset:2048
	ds_read_b128 v[194:197], v176 offset:3072
	ds_read_b128 v[198:201], v176 offset:4096
	ds_read_b128 v[202:205], v176 offset:5120
	ds_read_b128 v[206:209], v176 offset:6144
	ds_read_b128 v[210:213], v176 offset:7168
	global_load_lds_dwordx4 v[130:131], off
	v_lshl_add_u64 v[130:131], v[132:133], 1, s[42:43]
	v_readfirstlane_b32 s42, v178
	s_mov_b32 m0, s42
	s_nop 0
	global_load_lds_dwordx4 v[130:131], off
	s_barrier
	s_waitcnt lgkmcnt(0)
	v_mfma_f32_16x16x32_f16 v[122:125], v[182:185], v[154:157], v[122:125]
	v_mfma_f32_16x16x32_f16 v[110:113], v[198:201], v[134:137], v[110:113]
	v_mfma_f32_16x16x32_f16 v[98:101], v[206:209], v[154:157], v[98:101]
	v_mfma_f32_16x16x32_f16 v[126:129], v[182:185], v[134:137], v[126:129]
	v_mfma_f32_16x16x32_f16 v[122:125], v[186:189], v[168:171], v[122:125]
	v_mfma_f32_16x16x32_f16 v[118:121], v[190:193], v[134:137], v[118:121]
	v_mfma_f32_16x16x32_f16 v[114:117], v[190:193], v[154:157], v[114:117]
	v_mfma_f32_16x16x32_f16 v[130:133], v[202:205], v[138:141], v[110:113]
	v_mfma_f32_16x16x32_f16 v[106:109], v[198:201], v[154:157], v[106:109]
	v_mfma_f32_16x16x32_f16 v[102:105], v[206:209], v[134:137], v[102:105]
	v_mfma_f32_16x16x32_f16 v[98:101], v[210:213], v[168:171], v[98:101]
	v_mfma_f32_16x16x32_f16 v[126:129], v[186:189], v[138:141], v[126:129]
	v_mfma_f32_16x16x32_f16 v[118:121], v[194:197], v[138:141], v[118:121]
	v_mfma_f32_16x16x32_f16 v[114:117], v[194:197], v[168:171], v[114:117]
	v_mfma_f32_16x16x32_f16 v[214:217], v[202:205], v[168:171], v[106:109]
	v_mfma_f32_16x16x32_f16 v[102:105], v[210:213], v[138:141], v[102:105]
	s_barrier
	ds_read_b128 v[106:109], v162
	ds_read_b128 v[110:113], v163
	ds_read_b128 v[160:163], v164
	ds_read_b128 v[218:221], v165
	s_barrier
	s_waitcnt lgkmcnt(0)
	v_mfma_f32_16x16x32_f16 v[82:85], v[190:193], v[160:163], v[82:85]
	v_mfma_f32_16x16x32_f16 v[78:81], v[198:201], v[106:109], v[78:81]
	v_mfma_f32_16x16x32_f16 v[74:77], v[198:201], v[160:163], v[74:77]
	v_mfma_f32_16x16x32_f16 v[70:73], v[206:209], v[106:109], v[70:73]
	v_mfma_f32_16x16x32_f16 v[66:69], v[206:209], v[160:163], v[66:69]
	v_mfma_f32_16x16x32_f16 v[94:97], v[182:185], v[106:109], v[94:97]
	v_mfma_f32_16x16x32_f16 v[90:93], v[182:185], v[160:163], v[90:93]
	v_mfma_f32_16x16x32_f16 v[86:89], v[190:193], v[106:109], v[86:89]
	v_mfma_f32_16x16x32_f16 v[82:85], v[194:197], v[218:221], v[82:85]
	v_mfma_f32_16x16x32_f16 v[78:81], v[202:205], v[110:113], v[78:81]
	v_mfma_f32_16x16x32_f16 v[74:77], v[202:205], v[218:221], v[74:77]
	v_mfma_f32_16x16x32_f16 v[70:73], v[210:213], v[110:113], v[70:73]
	v_mfma_f32_16x16x32_f16 v[66:69], v[210:213], v[218:221], v[66:69]
	v_mfma_f32_16x16x32_f16 v[222:225], v[186:189], v[110:113], v[94:97]
	v_mfma_f32_16x16x32_f16 v[182:185], v[186:189], v[218:221], v[90:93]
	v_mfma_f32_16x16x32_f16 v[86:89], v[194:197], v[110:113], v[86:89]
	s_barrier
	ds_read_b128 v[90:93], v176 offset:16384
	ds_read_b128 v[94:97], v176 offset:17408
	ds_read_b128 v[186:189], v176 offset:18432
	ds_read_b128 v[190:193], v176 offset:19456
	ds_read_b128 v[194:197], v176 offset:20480
	ds_read_b128 v[198:201], v176 offset:21504
	ds_read_b128 v[202:205], v176 offset:22528
	ds_read_b128 v[206:209], v176 offset:23552
	s_waitcnt vmcnt(4)
	s_barrier
	s_waitcnt lgkmcnt(0)
	v_mfma_f32_16x16x32_f16 v[46:49], v[194:197], v[134:137], v[46:49]
	v_mfma_f32_16x16x32_f16 v[42:45], v[194:197], v[154:157], v[42:45]
	v_mfma_f32_16x16x32_f16 v[38:41], v[202:205], v[134:137], v[38:41]
	v_mfma_f32_16x16x32_f16 v[34:37], v[202:205], v[154:157], v[34:37]
	v_mfma_f32_16x16x32_f16 v[62:65], v[90:93], v[134:137], v[62:65]
	v_mfma_f32_16x16x32_f16 v[58:61], v[90:93], v[154:157], v[58:61]
	v_mfma_f32_16x16x32_f16 v[54:57], v[186:189], v[134:137], v[54:57]
	v_mfma_f32_16x16x32_f16 v[50:53], v[186:189], v[154:157], v[50:53]
	v_mfma_f32_16x16x32_f16 v[46:49], v[198:201], v[138:141], v[46:49]
	v_mfma_f32_16x16x32_f16 v[42:45], v[198:201], v[168:171], v[42:45]
	v_mfma_f32_16x16x32_f16 v[38:41], v[206:209], v[138:141], v[38:41]
	v_mfma_f32_16x16x32_f16 v[34:37], v[206:209], v[168:171], v[34:37]
	v_mfma_f32_16x16x32_f16 v[210:213], v[94:97], v[138:141], v[62:65]
	v_mfma_f32_16x16x32_f16 v[226:229], v[94:97], v[168:171], v[58:61]
	v_mfma_f32_16x16x32_f16 v[230:233], v[190:193], v[138:141], v[54:57]
	v_mfma_f32_16x16x32_f16 v[234:237], v[190:193], v[168:171], v[50:53]
	v_mfma_f32_16x16x32_f16 v[2:5], v[202:205], v[160:163], v[2:5]
	v_mfma_f32_16x16x32_f16 v[30:33], v[90:93], v[106:109], v[30:33]
	v_mfma_f32_16x16x32_f16 v[26:29], v[90:93], v[160:163], v[26:29]
	v_mfma_f32_16x16x32_f16 v[22:25], v[186:189], v[106:109], v[22:25]
	v_mfma_f32_16x16x32_f16 v[18:21], v[186:189], v[160:163], v[18:21]
	v_mfma_f32_16x16x32_f16 v[14:17], v[194:197], v[106:109], v[14:17]
	v_mfma_f32_16x16x32_f16 v[10:13], v[194:197], v[160:163], v[10:13]
	v_mfma_f32_16x16x32_f16 v[6:9], v[202:205], v[106:109], v[6:9]
	v_mfma_f32_16x16x32_f16 v[2:5], v[206:209], v[218:221], v[2:5]
	v_mfma_f32_16x16x32_f16 v[138:141], v[94:97], v[110:113], v[30:33]
	v_mfma_f32_16x16x32_f16 v[168:171], v[94:97], v[218:221], v[26:29]
	v_mfma_f32_16x16x32_f16 v[238:241], v[190:193], v[110:113], v[22:25]
	v_mfma_f32_16x16x32_f16 v[186:189], v[190:193], v[218:221], v[18:21]
	v_mfma_f32_16x16x32_f16 v[190:193], v[198:201], v[110:113], v[14:17]
	v_mfma_f32_16x16x32_f16 v[194:197], v[198:201], v[218:221], v[10:13]
	v_mfma_f32_16x16x32_f16 v[198:201], v[206:209], v[110:113], v[6:9]
	s_barrier
	s_nop 0
	ds_read_b128 v[6:9], v144
	ds_read_b128 v[10:13], v145
	ds_read_b128 v[14:17], v146
	ds_read_b128 v[160:163], v147
	ds_read_b128 v[18:21], v176 offset:32768
	ds_read_b128 v[22:25], v176 offset:33792
	ds_read_b128 v[26:29], v176 offset:34816
	ds_read_b128 v[50:53], v176 offset:35840
	ds_read_b128 v[202:205], v176 offset:36864
	ds_read_b128 v[206:209], v176 offset:37888
	ds_read_b128 v[218:221], v176 offset:38912
	ds_read_b128 v[242:245], v176 offset:39936
	s_waitcnt vmcnt(2)
	s_barrier
	s_waitcnt lgkmcnt(0)
	v_mfma_f32_16x16x32_f16 v[30:33], v[18:21], v[6:9], v[126:129]
	v_mfma_f32_16x16x32_f16 v[154:157], v[22:25], v[10:13], v[30:33]
	v_mfma_f32_16x16x32_f16 v[30:33], v[18:21], v[14:17], v[122:125]
	v_mfma_f32_16x16x32_f16 v[110:113], v[22:25], v[160:163], v[30:33]
	v_mfma_f32_16x16x32_f16 v[30:33], v[26:29], v[6:9], v[118:121]
	v_mfma_f32_16x16x32_f16 v[146:149], v[50:53], v[10:13], v[30:33]
	v_mfma_f32_16x16x32_f16 v[30:33], v[26:29], v[14:17], v[114:117]
	v_mfma_f32_16x16x32_f16 v[106:109], v[50:53], v[160:163], v[30:33]
	v_mfma_f32_16x16x32_f16 v[30:33], v[202:205], v[6:9], v[130:133]
	v_mfma_f32_16x16x32_f16 v[142:145], v[206:209], v[10:13], v[30:33]
	v_mfma_f32_16x16x32_f16 v[30:33], v[202:205], v[14:17], v[214:217]
	v_mfma_f32_16x16x32_f16 v[94:97], v[206:209], v[160:163], v[30:33]
	v_mfma_f32_16x16x32_f16 v[30:33], v[218:221], v[6:9], v[102:105]
	v_mfma_f32_16x16x32_f16 v[134:137], v[242:245], v[10:13], v[30:33]
	v_mfma_f32_16x16x32_f16 v[30:33], v[218:221], v[14:17], v[98:101]
	v_mfma_f32_16x16x32_f16 v[90:93], v[242:245], v[160:163], v[30:33]
	s_barrier
	ds_read_b128 v[102:105], v150
	ds_read_b128 v[114:117], v151
	ds_read_b128 v[118:121], v152
	ds_read_b128 v[126:129], v153
	s_waitcnt vmcnt(0)
	s_barrier
	s_waitcnt lgkmcnt(0)
	v_mfma_f32_16x16x32_f16 v[30:33], v[18:21], v[102:105], v[222:225]
	v_mfma_f32_16x16x32_f16 v[18:21], v[18:21], v[118:121], v[182:185]
	v_mfma_f32_16x16x32_f16 v[62:65], v[22:25], v[114:117], v[30:33]
	v_mfma_f32_16x16x32_f16 v[30:33], v[22:25], v[126:129], v[18:21]
	v_mfma_f32_16x16x32_f16 v[18:21], v[26:29], v[102:105], v[86:89]
	v_mfma_f32_16x16x32_f16 v[58:61], v[50:53], v[114:117], v[18:21]
	v_mfma_f32_16x16x32_f16 v[18:21], v[26:29], v[118:121], v[82:85]
	v_mfma_f32_16x16x32_f16 v[26:29], v[50:53], v[126:129], v[18:21]
	v_mfma_f32_16x16x32_f16 v[18:21], v[202:205], v[102:105], v[78:81]
	v_mfma_f32_16x16x32_f16 v[54:57], v[206:209], v[114:117], v[18:21]
	v_mfma_f32_16x16x32_f16 v[18:21], v[202:205], v[118:121], v[74:77]
	v_mfma_f32_16x16x32_f16 v[22:25], v[206:209], v[126:129], v[18:21]
	v_mfma_f32_16x16x32_f16 v[18:21], v[218:221], v[102:105], v[70:73]
	v_mfma_f32_16x16x32_f16 v[50:53], v[242:245], v[114:117], v[18:21]
	v_mfma_f32_16x16x32_f16 v[18:21], v[218:221], v[118:121], v[66:69]
	v_mfma_f32_16x16x32_f16 v[18:21], v[242:245], v[126:129], v[18:21]
	s_barrier
	ds_read_b128 v[86:89], v176 offset:49152
	ds_read_b128 v[150:153], v176 offset:50176
	ds_read_b128 v[182:185], v176 offset:51200
	ds_read_b128 v[202:205], v176 offset:52224
	ds_read_b128 v[206:209], v176 offset:53248
	ds_read_b128 v[214:217], v176 offset:54272
	ds_read_b128 v[218:221], v176 offset:55296
	ds_read_b128 v[174:177], v176 offset:56320
	s_barrier
	s_waitcnt lgkmcnt(0)
	v_mfma_f32_16x16x32_f16 v[66:69], v[86:89], v[6:9], v[210:213]
	v_mfma_f32_16x16x32_f16 v[130:133], v[150:153], v[10:13], v[66:69]
	v_mfma_f32_16x16x32_f16 v[66:69], v[86:89], v[14:17], v[226:229]
	v_mfma_f32_16x16x32_f16 v[78:81], v[150:153], v[160:163], v[66:69]
	v_mfma_f32_16x16x32_f16 v[66:69], v[182:185], v[6:9], v[230:233]
	v_mfma_f32_16x16x32_f16 v[46:49], v[206:209], v[6:9], v[46:49]
	v_mfma_f32_16x16x32_f16 v[6:9], v[218:221], v[6:9], v[38:41]
	v_mfma_f32_16x16x32_f16 v[122:125], v[202:205], v[10:13], v[66:69]
	v_mfma_f32_16x16x32_f16 v[66:69], v[182:185], v[14:17], v[234:237]
	v_mfma_f32_16x16x32_f16 v[42:45], v[206:209], v[14:17], v[42:45]
	v_mfma_f32_16x16x32_f16 v[82:85], v[174:177], v[10:13], v[6:9]
	v_mfma_f32_16x16x32_f16 v[6:9], v[218:221], v[14:17], v[34:37]
	v_mfma_f32_16x16x32_f16 v[74:77], v[202:205], v[160:163], v[66:69]
	v_mfma_f32_16x16x32_f16 v[98:101], v[214:217], v[10:13], v[46:49]
	v_mfma_f32_16x16x32_f16 v[70:73], v[214:217], v[160:163], v[42:45]
	v_mfma_f32_16x16x32_f16 v[66:69], v[174:177], v[160:163], v[6:9]
	v_mfma_f32_16x16x32_f16 v[6:9], v[86:89], v[102:105], v[138:141]
	v_mfma_f32_16x16x32_f16 v[46:49], v[150:153], v[114:117], v[6:9]
	v_mfma_f32_16x16x32_f16 v[6:9], v[86:89], v[118:121], v[168:171]
	v_mfma_f32_16x16x32_f16 v[14:17], v[150:153], v[126:129], v[6:9]
	v_mfma_f32_16x16x32_f16 v[6:9], v[182:185], v[102:105], v[238:241]
	v_mfma_f32_16x16x32_f16 v[42:45], v[202:205], v[114:117], v[6:9]
	v_mfma_f32_16x16x32_f16 v[6:9], v[182:185], v[118:121], v[186:189]
	v_mfma_f32_16x16x32_f16 v[10:13], v[202:205], v[126:129], v[6:9]
	v_mfma_f32_16x16x32_f16 v[6:9], v[206:209], v[102:105], v[190:193]
	v_mfma_f32_16x16x32_f16 v[38:41], v[214:217], v[114:117], v[6:9]
	v_mfma_f32_16x16x32_f16 v[6:9], v[206:209], v[118:121], v[194:197]
	v_mfma_f32_16x16x32_f16 v[34:37], v[218:221], v[102:105], v[198:201]
	v_mfma_f32_16x16x32_f16 v[2:5], v[218:221], v[118:121], v[2:5]
	v_mfma_f32_16x16x32_f16 v[6:9], v[214:217], v[126:129], v[6:9]
	v_mfma_f32_16x16x32_f16 v[34:37], v[174:177], v[114:117], v[34:37]
	v_mfma_f32_16x16x32_f16 v[2:5], v[174:177], v[126:129], v[2:5]
	s_cmpk_gt_u32 s62, 0xff
	s_barrier
	s_cbranch_scc1 .LBB8_44
	s_barrier

.LBB9_37:
	v_and_b32_e32 v10, 48, v196
	v_lshlrev_b32_e32 v11, 6, v196
	v_and_or_b32 v10, v11, s49, v10
	v_lshlrev_b32_e32 v11, 2, v196
	v_and_b32_e32 v11, 32, v11
	s_lshl_b32 s39, s54, 6
	v_lshlrev_b32_e32 v2, 12, v2
	v_xad_u32 v168, v10, v11, 0
	s_and_b32 s39, s39, 0x3000
	v_lshlrev_b32_e32 v6, 12, v6
	v_and_b32_e32 v2, 0xffffe000, v2
	v_add_u32_e32 v10, s39, v168
	s_lshl_b32 s39, s55, 13
	v_and_b32_e32 v6, 0xffffe000, v6
	v_lshl_add_u32 v2, v3, 9, v2
	v_lshl_add_u32 v6, v7, 9, v6
	s_add_u32 s44, s24, s44
	v_or_b32_e32 v2, v2, v4
	v_or_b32_e32 v6, v6, v8
	s_addc_u32 s45, s25, s45
	v_add_u32_sdwa v2, v2, sext(v5) dst_sel:DWORD dst_unused:UNUSED_PAD src0_sel:DWORD src1_sel:WORD_0
	v_add_u32_sdwa v6, v6, sext(v9) dst_sel:DWORD dst_unused:UNUSED_PAD src0_sel:DWORD src1_sel:WORD_0
	v_ashrrev_i32_e32 v3, 31, v2
	s_add_u32 s42, s20, s42
	s_waitcnt vmcnt(6)
	v_ashrrev_i32_e32 v7, 31, v6
	v_lshlrev_b64 v[2:3], 1, v[2:3]
	s_addc_u32 s43, s21, s43
	v_lshlrev_b64 v[6:7], 1, v[6:7]
	v_lshl_add_u64 v[136:137], s[44:45], 0, v[2:3]
	v_lshl_add_u64 v[140:141], s[42:43], 0, v[2:3]
	v_mov_b32_e32 v2, 0
	v_add_u32_e32 v169, 0x10000, v10
	v_add_u32_e32 v170, 0x10400, v10
	v_add_u32_e32 v171, 0x10800, v10
	v_add_u32_e32 v172, 0x10c00, v10
	v_add_u32_e32 v161, 0x14000, v10
	v_add_u32_e32 v162, 0x14400, v10
	v_add_u32_e32 v163, 0x14800, v10
	v_add_u32_e32 v164, 0x14c00, v10
	v_add_u32_e32 v144, 0x18000, v10
	v_add_u32_e32 v145, 0x18400, v10
	v_add_u32_e32 v150, 0x18800, v10
	v_add_u32_e32 v151, 0x18c00, v10
	v_add_u32_e32 v146, 0x1c000, v10
	v_add_u32_e32 v147, 0x1c400, v10
	v_add_u32_e32 v148, 0x1c800, v10
	v_add_u32_e32 v149, 0x1cc00, v10
	v_lshl_add_u64 v[134:135], s[44:45], 0, v[6:7]
	v_lshl_add_u64 v[138:139], s[42:43], 0, v[6:7]
	s_mov_b32 s44, -2
	s_mov_b64 s[42:43], 0
	v_mov_b32_e32 v3, v2
	v_mov_b32_e32 v4, v2
	v_mov_b32_e32 v5, v2
	v_mov_b32_e32 v6, v2
	v_mov_b32_e32 v7, v2
	v_mov_b32_e32 v8, v2
	v_mov_b32_e32 v9, v2
	v_mov_b32_e32 v10, v2
	v_mov_b32_e32 v11, v2
	v_mov_b32_e32 v12, v2
	v_mov_b32_e32 v13, v2
	v_mov_b32_e32 v18, v2
	v_mov_b32_e32 v19, v2
	v_mov_b32_e32 v20, v2
	v_mov_b32_e32 v21, v2
	v_mov_b32_e32 v30, v2
	v_mov_b32_e32 v31, v2
	v_mov_b32_e32 v32, v2
	v_mov_b32_e32 v33, v2
	v_mov_b32_e32 v42, v2
	v_mov_b32_e32 v43, v2
	v_mov_b32_e32 v44, v2
	v_mov_b32_e32 v45, v2
	v_mov_b32_e32 v54, v2
	v_mov_b32_e32 v55, v2
	v_mov_b32_e32 v56, v2
	v_mov_b32_e32 v57, v2
	v_mov_b32_e32 v66, v2
	v_mov_b32_e32 v67, v2
	v_mov_b32_e32 v68, v2
	v_mov_b32_e32 v69, v2
	v_mov_b32_e32 v14, v2
	v_mov_b32_e32 v15, v2
	v_mov_b32_e32 v16, v2
	v_mov_b32_e32 v17, v2
	v_mov_b32_e32 v22, v2
	v_mov_b32_e32 v23, v2
	v_mov_b32_e32 v24, v2
	v_mov_b32_e32 v25, v2
	v_mov_b32_e32 v34, v2
	v_mov_b32_e32 v35, v2
	v_mov_b32_e32 v36, v2
	v_mov_b32_e32 v37, v2
	v_mov_b32_e32 v46, v2
	v_mov_b32_e32 v47, v2
	v_mov_b32_e32 v48, v2
	v_mov_b32_e32 v49, v2
	v_mov_b32_e32 v58, v2
	v_mov_b32_e32 v59, v2
	v_mov_b32_e32 v60, v2
	v_mov_b32_e32 v61, v2
	v_mov_b32_e32 v70, v2
	v_mov_b32_e32 v71, v2
	v_mov_b32_e32 v72, v2
	v_mov_b32_e32 v73, v2
	v_mov_b32_e32 v78, v2
	v_mov_b32_e32 v79, v2
	v_mov_b32_e32 v80, v2
	v_mov_b32_e32 v81, v2
	v_mov_b32_e32 v86, v2
	v_mov_b32_e32 v87, v2
	v_mov_b32_e32 v88, v2
	v_mov_b32_e32 v89, v2
	v_mov_b32_e32 v26, v2
	v_mov_b32_e32 v27, v2
	v_mov_b32_e32 v28, v2
	v_mov_b32_e32 v29, v2
	v_mov_b32_e32 v38, v2
	v_mov_b32_e32 v39, v2
	v_mov_b32_e32 v40, v2
	v_mov_b32_e32 v41, v2
	v_mov_b32_e32 v50, v2
	v_mov_b32_e32 v51, v2
	v_mov_b32_e32 v52, v2
	v_mov_b32_e32 v53, v2
	v_mov_b32_e32 v62, v2
	v_mov_b32_e32 v63, v2
	v_mov_b32_e32 v64, v2
	v_mov_b32_e32 v65, v2
	v_mov_b32_e32 v74, v2
	v_mov_b32_e32 v75, v2
	v_mov_b32_e32 v76, v2
	v_mov_b32_e32 v77, v2
	v_mov_b32_e32 v82, v2
	v_mov_b32_e32 v83, v2
	v_mov_b32_e32 v84, v2
	v_mov_b32_e32 v85, v2
	v_mov_b32_e32 v90, v2
	v_mov_b32_e32 v91, v2
	v_mov_b32_e32 v92, v2
	v_mov_b32_e32 v93, v2
	v_mov_b32_e32 v94, v2
	v_mov_b32_e32 v95, v2
	v_mov_b32_e32 v96, v2
	v_mov_b32_e32 v97, v2
	v_mov_b32_e32 v98, v2
	v_mov_b32_e32 v99, v2
	v_mov_b32_e32 v100, v2
	v_mov_b32_e32 v101, v2
	v_mov_b32_e32 v102, v2
	v_mov_b32_e32 v103, v2
	v_mov_b32_e32 v104, v2
	v_mov_b32_e32 v105, v2
	v_mov_b32_e32 v106, v2
	v_mov_b32_e32 v107, v2
	v_mov_b32_e32 v108, v2
	v_mov_b32_e32 v109, v2
	v_mov_b32_e32 v110, v2
	v_mov_b32_e32 v111, v2
	v_mov_b32_e32 v112, v2
	v_mov_b32_e32 v113, v2
	v_mov_b32_e32 v114, v2
	v_mov_b32_e32 v115, v2
	v_mov_b32_e32 v116, v2
	v_mov_b32_e32 v117, v2
	v_mov_b32_e32 v118, v2
	v_mov_b32_e32 v119, v2
	v_mov_b32_e32 v120, v2
	v_mov_b32_e32 v121, v2
	v_mov_b32_e32 v122, v2
	v_mov_b32_e32 v123, v2
	v_mov_b32_e32 v124, v2
	v_mov_b32_e32 v125, v2
	v_mov_b32_e32 v126, v2
	v_mov_b32_e32 v127, v2
	v_mov_b32_e32 v128, v2
	v_mov_b32_e32 v129, v2
	v_add_u32_e32 v174, 0xc000, v152
	v_add_u32_e32 v175, 0xe000, v152
	s_nop 0
	v_readfirstlane_b32 s65, v174
	v_readfirstlane_b32 s66, v175
	v_readfirstlane_b32 s67, v142
	v_readfirstlane_b32 s68, v143
	v_readfirstlane_b32 s69, v152
	v_readfirstlane_b32 s70, v153
	v_readfirstlane_b32 s71, v154
	v_readfirstlane_b32 s72, v155
	v_readfirstlane_b32 s73, v156
	v_readfirstlane_b32 s74, v157
	v_readfirstlane_b32 s75, v158
	v_readfirstlane_b32 s76, v159
	v_readfirstlane_b32 s77, v160
	v_readfirstlane_b32 s78, v165
	v_readfirstlane_b32 s79, v166
	v_readfirstlane_b32 s80, v167
	s_barrier
	s_barrier
	ds_read_b128 v[176:179], v169
	ds_read_b128 v[180:183], v170
	ds_read_b128 v[184:187], v171
	ds_read_b128 v[188:191], v172
.LBB9_38:
	v_add_u32_e32 v174, 0xc000, v152
	v_lshl_add_u64 v[192:193], v[136:137], 0, s[42:43]
	v_add_u32_e32 v175, 0xe000, v152
	v_add_u32_e32 v173, s39, v168
	v_lshl_add_u64 v[230:231], v[192:193], 0, s[10:11]
	s_mov_b32 m0, s65
	v_lshl_add_u64 v[246:247], v[134:135], 0, s[42:43]
	ds_read_b128 v[198:201], v173
	ds_read_b128 v[202:205], v173 offset:1024
	ds_read_b128 v[206:209], v173 offset:2048
	ds_read_b128 v[210:213], v173 offset:3072
	ds_read_b128 v[214:217], v173 offset:4096
	ds_read_b128 v[218:221], v173 offset:5120
	ds_read_b128 v[222:225], v173 offset:6144
	ds_read_b128 v[226:229], v173 offset:7168
	global_load_lds_dwordx4 v[230:231], off
	s_mov_b32 m0, s66
	v_lshl_add_u64 v[230:231], v[246:247], 0, s[10:11]
	global_load_lds_dwordx4 v[230:231], off
	s_waitcnt lgkmcnt(8)
	s_barrier
	s_waitcnt lgkmcnt(0)
	v_mfma_f32_16x16x32_f16 v[2:5], v[198:201], v[176:179], v[2:5]
	v_mfma_f32_16x16x32_f16 v[6:9], v[198:201], v[184:187], v[6:9]
	v_mfma_f32_16x16x32_f16 v[10:13], v[206:209], v[176:179], v[10:13]
	v_mfma_f32_16x16x32_f16 v[18:21], v[206:209], v[184:187], v[18:21]
	v_mfma_f32_16x16x32_f16 v[30:33], v[214:217], v[176:179], v[30:33]
	v_mfma_f32_16x16x32_f16 v[42:45], v[214:217], v[184:187], v[42:45]
	v_mfma_f32_16x16x32_f16 v[54:57], v[222:225], v[176:179], v[54:57]
	v_mfma_f32_16x16x32_f16 v[66:69], v[222:225], v[184:187], v[66:69]
	v_mfma_f32_16x16x32_f16 v[2:5], v[202:205], v[180:183], v[2:5]
	v_mfma_f32_16x16x32_f16 v[6:9], v[202:205], v[188:191], v[6:9]
	v_mfma_f32_16x16x32_f16 v[10:13], v[210:213], v[180:183], v[10:13]
	v_mfma_f32_16x16x32_f16 v[18:21], v[210:213], v[188:191], v[18:21]
	v_mfma_f32_16x16x32_f16 v[30:33], v[218:221], v[180:183], v[30:33]
	v_mfma_f32_16x16x32_f16 v[42:45], v[218:221], v[188:191], v[42:45]
	v_mfma_f32_16x16x32_f16 v[54:57], v[226:229], v[180:183], v[54:57]
	v_mfma_f32_16x16x32_f16 v[66:69], v[226:229], v[188:191], v[66:69]
	s_barrier
	v_lshl_add_u64 v[248:249], v[140:141], 0, s[42:43]
	v_lshl_add_u64 v[250:251], v[248:249], 0, s[26:27]
	s_mov_b32 m0, s67
	ds_read_b128 v[230:233], v161
	ds_read_b128 v[234:237], v162
	ds_read_b128 v[238:241], v163
	ds_read_b128 v[242:245], v164
	global_load_lds_dwordx4 v[250:251], off
	v_lshl_add_u64 v[250:251], v[138:139], 0, s[42:43]
	s_mov_b32 m0, s68
	v_lshl_add_u64 v[252:253], v[250:251], 0, s[26:27]
	global_load_lds_dwordx4 v[252:253], off
	s_barrier
	s_waitcnt lgkmcnt(0)
	v_mfma_f32_16x16x32_f16 v[14:17], v[198:201], v[230:233], v[14:17]
	v_mfma_f32_16x16x32_f16 v[22:25], v[198:201], v[238:241], v[22:25]
	v_mfma_f32_16x16x32_f16 v[34:37], v[206:209], v[230:233], v[34:37]
	v_mfma_f32_16x16x32_f16 v[46:49], v[206:209], v[238:241], v[46:49]
	v_mfma_f32_16x16x32_f16 v[58:61], v[214:217], v[230:233], v[58:61]
	v_mfma_f32_16x16x32_f16 v[70:73], v[214:217], v[238:241], v[70:73]
	v_mfma_f32_16x16x32_f16 v[78:81], v[222:225], v[230:233], v[78:81]
	v_mfma_f32_16x16x32_f16 v[86:89], v[222:225], v[238:241], v[86:89]
	v_mfma_f32_16x16x32_f16 v[14:17], v[202:205], v[234:237], v[14:17]
	v_mfma_f32_16x16x32_f16 v[22:25], v[202:205], v[242:245], v[22:25]
	v_mfma_f32_16x16x32_f16 v[34:37], v[210:213], v[234:237], v[34:37]
	v_mfma_f32_16x16x32_f16 v[46:49], v[210:213], v[242:245], v[46:49]
	v_mfma_f32_16x16x32_f16 v[58:61], v[218:221], v[234:237], v[58:61]
	v_mfma_f32_16x16x32_f16 v[70:73], v[218:221], v[242:245], v[70:73]
	v_mfma_f32_16x16x32_f16 v[78:81], v[226:229], v[234:237], v[78:81]
	v_mfma_f32_16x16x32_f16 v[86:89], v[226:229], v[242:245], v[86:89]
	v_lshl_add_u64 v[252:253], v[192:193], 0, s[26:27]
	s_mov_b32 m0, s69
	s_barrier
	ds_read_b128 v[198:201], v173 offset:16384
	ds_read_b128 v[202:205], v173 offset:17408
	ds_read_b128 v[206:209], v173 offset:18432
	ds_read_b128 v[210:213], v173 offset:19456
	ds_read_b128 v[214:217], v173 offset:20480
	ds_read_b128 v[218:221], v173 offset:21504
	ds_read_b128 v[222:225], v173 offset:22528
	ds_read_b128 v[226:229], v173 offset:23552
	global_load_lds_dwordx4 v[252:253], off
	s_mov_b32 m0, s70
	v_lshl_add_u64 v[252:253], v[246:247], 0, s[26:27]
	global_load_lds_dwordx4 v[252:253], off
	s_waitcnt vmcnt(10)
	s_barrier
	s_waitcnt lgkmcnt(0)
	v_mfma_f32_16x16x32_f16 v[26:29], v[198:201], v[176:179], v[26:29]
	v_mfma_f32_16x16x32_f16 v[38:41], v[198:201], v[184:187], v[38:41]
	v_mfma_f32_16x16x32_f16 v[50:53], v[206:209], v[176:179], v[50:53]
	v_mfma_f32_16x16x32_f16 v[62:65], v[206:209], v[184:187], v[62:65]
	v_mfma_f32_16x16x32_f16 v[74:77], v[214:217], v[176:179], v[74:77]
	v_mfma_f32_16x16x32_f16 v[82:85], v[214:217], v[184:187], v[82:85]
	v_mfma_f32_16x16x32_f16 v[90:93], v[222:225], v[176:179], v[90:93]
	v_mfma_f32_16x16x32_f16 v[94:97], v[222:225], v[184:187], v[94:97]
	v_mfma_f32_16x16x32_f16 v[26:29], v[202:205], v[180:183], v[26:29]
	v_mfma_f32_16x16x32_f16 v[38:41], v[202:205], v[188:191], v[38:41]
	v_mfma_f32_16x16x32_f16 v[50:53], v[210:213], v[180:183], v[50:53]
	v_mfma_f32_16x16x32_f16 v[62:65], v[210:213], v[188:191], v[62:65]
	v_mfma_f32_16x16x32_f16 v[74:77], v[218:221], v[180:183], v[74:77]
	v_mfma_f32_16x16x32_f16 v[82:85], v[218:221], v[188:191], v[82:85]
	v_mfma_f32_16x16x32_f16 v[90:93], v[226:229], v[180:183], v[90:93]
	v_mfma_f32_16x16x32_f16 v[94:97], v[226:229], v[188:191], v[94:97]
	s_barrier
	s_mov_b32 m0, s71
	v_lshl_add_u64 v[176:177], v[248:249], 0, s[28:29]
	global_load_lds_dwordx4 v[176:177], off
	s_mov_b32 m0, s72
	v_lshl_add_u64 v[176:177], v[250:251], 0, s[28:29]
	global_load_lds_dwordx4 v[176:177], off
	s_waitcnt vmcnt(6)
	s_barrier
	v_mfma_f32_16x16x32_f16 v[98:101], v[198:201], v[230:233], v[98:101]
	v_mfma_f32_16x16x32_f16 v[102:105], v[198:201], v[238:241], v[102:105]
	v_mfma_f32_16x16x32_f16 v[106:109], v[206:209], v[230:233], v[106:109]
	v_mfma_f32_16x16x32_f16 v[110:113], v[206:209], v[238:241], v[110:113]
	v_mfma_f32_16x16x32_f16 v[114:117], v[214:217], v[230:233], v[114:117]
	v_mfma_f32_16x16x32_f16 v[118:121], v[214:217], v[238:241], v[118:121]
	v_mfma_f32_16x16x32_f16 v[122:125], v[222:225], v[230:233], v[122:125]
	v_mfma_f32_16x16x32_f16 v[126:129], v[222:225], v[238:241], v[126:129]
	v_mfma_f32_16x16x32_f16 v[98:101], v[202:205], v[234:237], v[98:101]
	v_mfma_f32_16x16x32_f16 v[102:105], v[202:205], v[242:245], v[102:105]
	v_mfma_f32_16x16x32_f16 v[106:109], v[210:213], v[234:237], v[106:109]
	v_mfma_f32_16x16x32_f16 v[110:113], v[210:213], v[242:245], v[110:113]
	ds_read_b128 v[176:179], v144
	ds_read_b128 v[180:183], v145
	ds_read_b128 v[184:187], v150
	ds_read_b128 v[188:191], v151
	v_mfma_f32_16x16x32_f16 v[114:117], v[218:221], v[234:237], v[114:117]
	v_mfma_f32_16x16x32_f16 v[118:121], v[218:221], v[242:245], v[118:121]
	v_mfma_f32_16x16x32_f16 v[122:125], v[226:229], v[234:237], v[122:125]
	v_mfma_f32_16x16x32_f16 v[126:129], v[226:229], v[242:245], v[126:129]
	s_barrier
	v_lshl_add_u64 v[230:231], v[192:193], 0, s[28:29]
	s_mov_b32 m0, s73
	ds_read_b128 v[198:201], v173 offset:32768
	ds_read_b128 v[202:205], v173 offset:33792
	ds_read_b128 v[206:209], v173 offset:34816
	ds_read_b128 v[210:213], v173 offset:35840
	ds_read_b128 v[214:217], v173 offset:36864
	ds_read_b128 v[218:221], v173 offset:37888
	ds_read_b128 v[222:225], v173 offset:38912
	ds_read_b128 v[226:229], v173 offset:39936
	global_load_lds_dwordx4 v[230:231], off
	s_mov_b32 m0, s74
	v_lshl_add_u64 v[230:231], v[246:247], 0, s[28:29]
	global_load_lds_dwordx4 v[230:231], off
	s_waitcnt lgkmcnt(8)
	s_barrier
	s_waitcnt lgkmcnt(0)
	v_mfma_f32_16x16x32_f16 v[2:5], v[198:201], v[176:179], v[2:5]
	v_mfma_f32_16x16x32_f16 v[6:9], v[198:201], v[184:187], v[6:9]
	v_mfma_f32_16x16x32_f16 v[10:13], v[206:209], v[176:179], v[10:13]
	v_mfma_f32_16x16x32_f16 v[18:21], v[206:209], v[184:187], v[18:21]
	v_mfma_f32_16x16x32_f16 v[30:33], v[214:217], v[176:179], v[30:33]
	v_mfma_f32_16x16x32_f16 v[42:45], v[214:217], v[184:187], v[42:45]
	v_mfma_f32_16x16x32_f16 v[54:57], v[222:225], v[176:179], v[54:57]
	v_mfma_f32_16x16x32_f16 v[66:69], v[222:225], v[184:187], v[66:69]
	v_mfma_f32_16x16x32_f16 v[2:5], v[202:205], v[180:183], v[2:5]
	v_mfma_f32_16x16x32_f16 v[6:9], v[202:205], v[188:191], v[6:9]
	v_mfma_f32_16x16x32_f16 v[10:13], v[210:213], v[180:183], v[10:13]
	v_mfma_f32_16x16x32_f16 v[18:21], v[210:213], v[188:191], v[18:21]
	v_mfma_f32_16x16x32_f16 v[30:33], v[218:221], v[180:183], v[30:33]
	v_mfma_f32_16x16x32_f16 v[42:45], v[218:221], v[188:191], v[42:45]
	v_mfma_f32_16x16x32_f16 v[54:57], v[226:229], v[180:183], v[54:57]
	v_mfma_f32_16x16x32_f16 v[66:69], v[226:229], v[188:191], v[66:69]
	s_barrier
	v_lshl_add_u64 v[252:253], v[248:249], 0, s[30:31]
	s_mov_b32 m0, s75
	ds_read_b128 v[230:233], v146
	ds_read_b128 v[234:237], v147
	ds_read_b128 v[238:241], v148
	ds_read_b128 v[242:245], v149
	global_load_lds_dwordx4 v[252:253], off
	s_mov_b32 m0, s76
	v_lshl_add_u64 v[252:253], v[250:251], 0, s[30:31]
	global_load_lds_dwordx4 v[252:253], off
	s_barrier
	s_waitcnt lgkmcnt(0)
	v_mfma_f32_16x16x32_f16 v[14:17], v[198:201], v[230:233], v[14:17]
	v_mfma_f32_16x16x32_f16 v[22:25], v[198:201], v[238:241], v[22:25]
	v_mfma_f32_16x16x32_f16 v[34:37], v[206:209], v[230:233], v[34:37]
	v_mfma_f32_16x16x32_f16 v[46:49], v[206:209], v[238:241], v[46:49]
	v_mfma_f32_16x16x32_f16 v[58:61], v[214:217], v[230:233], v[58:61]
	v_mfma_f32_16x16x32_f16 v[70:73], v[214:217], v[238:241], v[70:73]
	v_mfma_f32_16x16x32_f16 v[78:81], v[222:225], v[230:233], v[78:81]
	v_mfma_f32_16x16x32_f16 v[86:89], v[222:225], v[238:241], v[86:89]
	v_mfma_f32_16x16x32_f16 v[14:17], v[202:205], v[234:237], v[14:17]
	v_mfma_f32_16x16x32_f16 v[22:25], v[202:205], v[242:245], v[22:25]
	v_mfma_f32_16x16x32_f16 v[34:37], v[210:213], v[234:237], v[34:37]
	v_mfma_f32_16x16x32_f16 v[46:49], v[210:213], v[242:245], v[46:49]
	v_mfma_f32_16x16x32_f16 v[58:61], v[218:221], v[234:237], v[58:61]
	v_mfma_f32_16x16x32_f16 v[70:73], v[218:221], v[242:245], v[70:73]
	v_mfma_f32_16x16x32_f16 v[78:81], v[226:229], v[234:237], v[78:81]
	v_mfma_f32_16x16x32_f16 v[86:89], v[226:229], v[242:245], v[86:89]
	v_lshl_add_u64 v[192:193], v[192:193], 0, s[30:31]
	s_mov_b32 m0, s77
	s_barrier
	ds_read_b128 v[198:201], v173 offset:49152
	ds_read_b128 v[202:205], v173 offset:50176
	ds_read_b128 v[206:209], v173 offset:51200
	ds_read_b128 v[210:213], v173 offset:52224
	ds_read_b128 v[214:217], v173 offset:53248
	ds_read_b128 v[218:221], v173 offset:54272
	ds_read_b128 v[222:225], v173 offset:55296
	ds_read_b128 v[226:229], v173 offset:56320
	global_load_lds_dwordx4 v[192:193], off
	s_mov_b32 m0, s78
	v_lshl_add_u64 v[192:193], v[246:247], 0, s[30:31]
	global_load_lds_dwordx4 v[192:193], off
	s_waitcnt vmcnt(10)
	s_barrier
	s_waitcnt lgkmcnt(0)
	v_mfma_f32_16x16x32_f16 v[26:29], v[198:201], v[176:179], v[26:29]
	v_mfma_f32_16x16x32_f16 v[38:41], v[198:201], v[184:187], v[38:41]
	v_mfma_f32_16x16x32_f16 v[50:53], v[206:209], v[176:179], v[50:53]
	v_mfma_f32_16x16x32_f16 v[62:65], v[206:209], v[184:187], v[62:65]
	v_mfma_f32_16x16x32_f16 v[74:77], v[214:217], v[176:179], v[74:77]
	v_mfma_f32_16x16x32_f16 v[82:85], v[214:217], v[184:187], v[82:85]
	v_mfma_f32_16x16x32_f16 v[90:93], v[222:225], v[176:179], v[90:93]
	v_mfma_f32_16x16x32_f16 v[94:97], v[222:225], v[184:187], v[94:97]
	v_mfma_f32_16x16x32_f16 v[26:29], v[202:205], v[180:183], v[26:29]
	v_mfma_f32_16x16x32_f16 v[38:41], v[202:205], v[188:191], v[38:41]
	v_mfma_f32_16x16x32_f16 v[50:53], v[210:213], v[180:183], v[50:53]
	v_mfma_f32_16x16x32_f16 v[62:65], v[210:213], v[188:191], v[62:65]
	v_mfma_f32_16x16x32_f16 v[74:77], v[218:221], v[180:183], v[74:77]
	v_mfma_f32_16x16x32_f16 v[82:85], v[218:221], v[188:191], v[82:85]
	v_mfma_f32_16x16x32_f16 v[90:93], v[226:229], v[180:183], v[90:93]
	v_mfma_f32_16x16x32_f16 v[94:97], v[226:229], v[188:191], v[94:97]
	s_barrier
	s_mov_b32 m0, s79
	v_lshl_add_u64 v[176:177], v[248:249], 0, s[34:35]
	global_load_lds_dwordx4 v[176:177], off
	s_mov_b32 m0, s80
	v_lshl_add_u64 v[176:177], v[250:251], 0, s[34:35]
	global_load_lds_dwordx4 v[176:177], off
	s_waitcnt vmcnt(6)
	s_barrier
	v_mfma_f32_16x16x32_f16 v[98:101], v[198:201], v[230:233], v[98:101]
	v_mfma_f32_16x16x32_f16 v[102:105], v[198:201], v[238:241], v[102:105]
	v_mfma_f32_16x16x32_f16 v[106:109], v[206:209], v[230:233], v[106:109]
	v_mfma_f32_16x16x32_f16 v[110:113], v[206:209], v[238:241], v[110:113]
	v_mfma_f32_16x16x32_f16 v[114:117], v[214:217], v[230:233], v[114:117]
	v_mfma_f32_16x16x32_f16 v[118:121], v[214:217], v[238:241], v[118:121]
	v_mfma_f32_16x16x32_f16 v[122:125], v[222:225], v[230:233], v[122:125]
	v_mfma_f32_16x16x32_f16 v[126:129], v[222:225], v[238:241], v[126:129]
	v_mfma_f32_16x16x32_f16 v[98:101], v[202:205], v[234:237], v[98:101]
	v_mfma_f32_16x16x32_f16 v[102:105], v[202:205], v[242:245], v[102:105]
	v_mfma_f32_16x16x32_f16 v[106:109], v[210:213], v[234:237], v[106:109]
	v_mfma_f32_16x16x32_f16 v[110:113], v[210:213], v[242:245], v[110:113]
	ds_read_b128 v[176:179], v169
	ds_read_b128 v[180:183], v170
	ds_read_b128 v[184:187], v171
	ds_read_b128 v[188:191], v172
	v_mfma_f32_16x16x32_f16 v[114:117], v[218:221], v[234:237], v[114:117]
	v_mfma_f32_16x16x32_f16 v[118:121], v[218:221], v[242:245], v[118:121]
	v_mfma_f32_16x16x32_f16 v[122:125], v[226:229], v[234:237], v[122:125]
	v_mfma_f32_16x16x32_f16 v[126:129], v[226:229], v[242:245], v[126:129]
	s_add_i32 s44, s44, 2
	s_add_u32 s42, s42, 0x100
	s_addc_u32 s43, s43, 0
	s_cmp_lt_u32 s44, 4
	s_barrier
	s_cbranch_scc1 .LBB9_38
	s_add_u32 s40, s40, 0x20380
	s_addc_u32 s41, s41, 0
	v_readfirstlane_b32 s39, v174
	v_lshl_add_u64 v[130:131], v[130:131], 1, s[40:41]
	s_mov_b32 m0, s39
	v_readfirstlane_b32 s39, v175
	ds_read_b128 v[134:137], v169
	ds_read_b128 v[138:141], v170
	ds_read_b128 v[152:155], v171
	ds_read_b128 v[156:159], v172
	ds_read_b128 v[166:169], v173
	ds_read_b128 v[176:179], v173 offset:1024
	ds_read_b128 v[180:183], v173 offset:2048
	ds_read_b128 v[184:187], v173 offset:3072
	ds_read_b128 v[188:191], v173 offset:4096
	ds_read_b128 v[198:201], v173 offset:5120
	ds_read_b128 v[202:205], v173 offset:6144
	ds_read_b128 v[206:209], v173 offset:7168
	global_load_lds_dwordx4 v[130:131], off
	s_mov_b32 m0, s39
	v_lshl_add_u64 v[130:131], v[132:133], 1, s[40:41]
	global_load_lds_dwordx4 v[130:131], off
	s_barrier
	s_waitcnt lgkmcnt(0)
	v_mfma_f32_16x16x32_f16 v[2:5], v[166:169], v[134:137], v[2:5]
	v_mfma_f32_16x16x32_f16 v[6:9], v[166:169], v[152:155], v[6:9]
	v_mfma_f32_16x16x32_f16 v[30:33], v[188:191], v[134:137], v[30:33]
	v_mfma_f32_16x16x32_f16 v[2:5], v[176:179], v[138:141], v[2:5]
	v_mfma_f32_16x16x32_f16 v[6:9], v[176:179], v[156:159], v[6:9]
	v_mfma_f32_16x16x32_f16 v[10:13], v[180:183], v[134:137], v[10:13]
	v_mfma_f32_16x16x32_f16 v[18:21], v[180:183], v[152:155], v[18:21]
	v_mfma_f32_16x16x32_f16 v[30:33], v[198:201], v[138:141], v[30:33]
	v_mfma_f32_16x16x32_f16 v[42:45], v[188:191], v[152:155], v[42:45]
	v_mfma_f32_16x16x32_f16 v[54:57], v[202:205], v[134:137], v[54:57]
	v_mfma_f32_16x16x32_f16 v[66:69], v[202:205], v[152:155], v[66:69]
	v_mfma_f32_16x16x32_f16 v[10:13], v[184:187], v[138:141], v[10:13]
	v_mfma_f32_16x16x32_f16 v[18:21], v[184:187], v[156:159], v[18:21]
	v_mfma_f32_16x16x32_f16 v[42:45], v[198:201], v[156:159], v[42:45]
	v_mfma_f32_16x16x32_f16 v[54:57], v[206:209], v[138:141], v[54:57]
	v_mfma_f32_16x16x32_f16 v[66:69], v[206:209], v[156:159], v[66:69]
	s_barrier
	ds_read_b128 v[130:133], v161
	ds_read_b128 v[210:213], v162
	ds_read_b128 v[160:163], v163
	ds_read_b128 v[214:217], v164
	s_barrier
	s_waitcnt lgkmcnt(0)
	v_mfma_f32_16x16x32_f16 v[58:61], v[188:191], v[130:133], v[58:61]
	v_mfma_f32_16x16x32_f16 v[14:17], v[166:169], v[130:133], v[14:17]
	v_mfma_f32_16x16x32_f16 v[22:25], v[166:169], v[160:163], v[22:25]
	v_mfma_f32_16x16x32_f16 v[164:167], v[198:201], v[210:213], v[58:61]
	v_mfma_f32_16x16x32_f16 v[58:61], v[188:191], v[160:163], v[70:73]
	v_mfma_f32_16x16x32_f16 v[46:49], v[180:183], v[160:163], v[46:49]
	v_mfma_f32_16x16x32_f16 v[168:171], v[198:201], v[214:217], v[58:61]
	v_mfma_f32_16x16x32_f16 v[58:61], v[202:205], v[130:133], v[78:81]
	v_mfma_f32_16x16x32_f16 v[14:17], v[176:179], v[210:213], v[14:17]
	v_mfma_f32_16x16x32_f16 v[34:37], v[180:183], v[130:133], v[34:37]
	v_mfma_f32_16x16x32_f16 v[46:49], v[184:187], v[214:217], v[46:49]
	v_mfma_f32_16x16x32_f16 v[78:81], v[206:209], v[210:213], v[58:61]
	v_mfma_f32_16x16x32_f16 v[58:61], v[202:205], v[160:163], v[86:89]
	v_mfma_f32_16x16x32_f16 v[22:25], v[176:179], v[214:217], v[22:25]
	v_mfma_f32_16x16x32_f16 v[34:37], v[184:187], v[210:213], v[34:37]
	v_mfma_f32_16x16x32_f16 v[86:89], v[206:209], v[214:217], v[58:61]
	s_barrier
	s_nop 2
	ds_read_b128 v[58:61], v173 offset:16384
	ds_read_b128 v[70:73], v173 offset:17408
	ds_read_b128 v[174:177], v173 offset:18432
	ds_read_b128 v[178:181], v173 offset:19456
	ds_read_b128 v[182:185], v173 offset:20480
	ds_read_b128 v[186:189], v173 offset:21504
	ds_read_b128 v[190:193], v173 offset:22528
	ds_read_b128 v[198:201], v173 offset:23552
	s_waitcnt vmcnt(4)
	s_barrier
	s_waitcnt lgkmcnt(0)
	v_mfma_f32_16x16x32_f16 v[26:29], v[58:61], v[134:137], v[26:29]
	v_mfma_f32_16x16x32_f16 v[26:29], v[70:73], v[138:141], v[26:29]
	v_mfma_f32_16x16x32_f16 v[38:41], v[58:61], v[152:155], v[38:41]
	v_mfma_f32_16x16x32_f16 v[50:53], v[174:177], v[134:137], v[50:53]
	v_mfma_f32_16x16x32_f16 v[62:65], v[174:177], v[152:155], v[62:65]
	v_mfma_f32_16x16x32_f16 v[74:77], v[182:185], v[134:137], v[74:77]
	v_mfma_f32_16x16x32_f16 v[82:85], v[182:185], v[152:155], v[82:85]
	v_mfma_f32_16x16x32_f16 v[90:93], v[190:193], v[134:137], v[90:93]
	v_mfma_f32_16x16x32_f16 v[94:97], v[190:193], v[152:155], v[94:97]
	v_mfma_f32_16x16x32_f16 v[38:41], v[70:73], v[156:159], v[38:41]
	v_mfma_f32_16x16x32_f16 v[50:53], v[178:181], v[138:141], v[50:53]
	v_mfma_f32_16x16x32_f16 v[62:65], v[178:181], v[156:159], v[62:65]
	v_mfma_f32_16x16x32_f16 v[74:77], v[186:189], v[138:141], v[74:77]
	v_mfma_f32_16x16x32_f16 v[82:85], v[186:189], v[156:159], v[82:85]
	v_mfma_f32_16x16x32_f16 v[90:93], v[198:201], v[138:141], v[90:93]
	v_mfma_f32_16x16x32_f16 v[94:97], v[198:201], v[156:159], v[94:97]
	v_mfma_f32_16x16x32_f16 v[98:101], v[58:61], v[130:133], v[98:101]
	v_mfma_f32_16x16x32_f16 v[58:61], v[58:61], v[160:163], v[102:105]
	v_mfma_f32_16x16x32_f16 v[102:105], v[70:73], v[214:217], v[58:61]
	v_mfma_f32_16x16x32_f16 v[58:61], v[174:177], v[130:133], v[106:109]
	v_mfma_f32_16x16x32_f16 v[106:109], v[178:181], v[210:213], v[58:61]
	v_mfma_f32_16x16x32_f16 v[58:61], v[174:177], v[160:163], v[110:113]
	v_mfma_f32_16x16x32_f16 v[202:205], v[178:181], v[214:217], v[58:61]
	v_mfma_f32_16x16x32_f16 v[58:61], v[182:185], v[130:133], v[114:117]
	v_mfma_f32_16x16x32_f16 v[206:209], v[186:189], v[210:213], v[58:61]
	v_mfma_f32_16x16x32_f16 v[58:61], v[182:185], v[160:163], v[118:121]
	v_mfma_f32_16x16x32_f16 v[218:221], v[186:189], v[214:217], v[58:61]
	v_mfma_f32_16x16x32_f16 v[58:61], v[190:193], v[130:133], v[122:125]
	v_mfma_f32_16x16x32_f16 v[98:101], v[70:73], v[210:213], v[98:101]
	v_mfma_f32_16x16x32_f16 v[210:213], v[198:201], v[210:213], v[58:61]
	v_mfma_f32_16x16x32_f16 v[58:61], v[190:193], v[160:163], v[126:129]
	v_mfma_f32_16x16x32_f16 v[198:201], v[198:201], v[214:217], v[58:61]
	s_barrier
	ds_read_b128 v[110:113], v144
	ds_read_b128 v[130:133], v145
	ds_read_b128 v[214:217], v150
	ds_read_b128 v[222:225], v151
	s_nop 0
	ds_read_b128 v[58:61], v173 offset:32768
	ds_read_b128 v[70:73], v173 offset:33792
	ds_read_b128 v[114:117], v173 offset:34816
	ds_read_b128 v[118:121], v173 offset:35840
	ds_read_b128 v[134:137], v173 offset:36864
	ds_read_b128 v[138:141], v173 offset:37888
	ds_read_b128 v[178:181], v173 offset:38912
	ds_read_b128 v[226:229], v173 offset:39936
	s_waitcnt vmcnt(2)
	s_barrier
	s_waitcnt lgkmcnt(0)
	v_mfma_f32_16x16x32_f16 v[2:5], v[58:61], v[110:113], v[2:5]
	v_mfma_f32_16x16x32_f16 v[190:193], v[70:73], v[130:133], v[2:5]
	v_mfma_f32_16x16x32_f16 v[2:5], v[58:61], v[214:217], v[6:9]
	v_mfma_f32_16x16x32_f16 v[158:161], v[70:73], v[222:225], v[2:5]
	v_mfma_f32_16x16x32_f16 v[2:5], v[114:117], v[110:113], v[10:13]
	v_mfma_f32_16x16x32_f16 v[186:189], v[118:121], v[130:133], v[2:5]
	v_mfma_f32_16x16x32_f16 v[2:5], v[114:117], v[214:217], v[18:21]
	v_mfma_f32_16x16x32_f16 v[154:157], v[118:121], v[222:225], v[2:5]
	v_mfma_f32_16x16x32_f16 v[2:5], v[134:137], v[110:113], v[30:33]
	v_mfma_f32_16x16x32_f16 v[182:185], v[138:141], v[130:133], v[2:5]
	v_mfma_f32_16x16x32_f16 v[2:5], v[134:137], v[214:217], v[42:45]
	v_mfma_f32_16x16x32_f16 v[150:153], v[138:141], v[222:225], v[2:5]
	v_mfma_f32_16x16x32_f16 v[2:5], v[178:181], v[110:113], v[54:57]
	v_mfma_f32_16x16x32_f16 v[174:177], v[226:229], v[130:133], v[2:5]
	v_mfma_f32_16x16x32_f16 v[2:5], v[178:181], v[214:217], v[66:69]
	v_mfma_f32_16x16x32_f16 v[142:145], v[226:229], v[222:225], v[2:5]
	s_barrier
	s_nop 4
	ds_read_b128 v[2:5], v146
	ds_read_b128 v[10:13], v147
	ds_read_b128 v[18:21], v148
	ds_read_b128 v[42:45], v149
	s_waitcnt vmcnt(0)
	s_barrier
	s_waitcnt lgkmcnt(0)
	v_mfma_f32_16x16x32_f16 v[6:9], v[58:61], v[2:5], v[14:17]
	v_mfma_f32_16x16x32_f16 v[126:129], v[70:73], v[10:13], v[6:9]
	v_mfma_f32_16x16x32_f16 v[6:9], v[58:61], v[18:21], v[22:25]
	v_mfma_f32_16x16x32_f16 v[70:73], v[70:73], v[42:45], v[6:9]
	v_mfma_f32_16x16x32_f16 v[6:9], v[114:117], v[2:5], v[34:37]
	v_mfma_f32_16x16x32_f16 v[122:125], v[118:121], v[10:13], v[6:9]
	v_mfma_f32_16x16x32_f16 v[6:9], v[114:117], v[18:21], v[46:49]
	v_mfma_f32_16x16x32_f16 v[58:61], v[118:121], v[42:45], v[6:9]
	v_mfma_f32_16x16x32_f16 v[6:9], v[134:137], v[2:5], v[164:167]
	v_mfma_f32_16x16x32_f16 v[118:121], v[138:141], v[10:13], v[6:9]
	v_mfma_f32_16x16x32_f16 v[6:9], v[134:137], v[18:21], v[168:171]
	v_mfma_f32_16x16x32_f16 v[46:49], v[138:141], v[42:45], v[6:9]
	v_mfma_f32_16x16x32_f16 v[6:9], v[178:181], v[2:5], v[78:81]
	v_mfma_f32_16x16x32_f16 v[114:117], v[226:229], v[10:13], v[6:9]
	v_mfma_f32_16x16x32_f16 v[6:9], v[178:181], v[18:21], v[86:89]
	v_mfma_f32_16x16x32_f16 v[30:33], v[226:229], v[42:45], v[6:9]
	s_barrier
	s_nop 4
	ds_read_b128 v[6:9], v173 offset:49152
	ds_read_b128 v[14:17], v173 offset:50176
	ds_read_b128 v[22:25], v173 offset:51200
	ds_read_b128 v[34:37], v173 offset:52224
	ds_read_b128 v[54:57], v173 offset:53248
	ds_read_b128 v[66:69], v173 offset:54272
	ds_read_b128 v[78:81], v173 offset:55296
	ds_read_b128 v[86:89], v173 offset:56320
	s_barrier
	s_waitcnt lgkmcnt(0)
	v_mfma_f32_16x16x32_f16 v[26:29], v[6:9], v[110:113], v[26:29]
	v_mfma_f32_16x16x32_f16 v[178:181], v[14:17], v[130:133], v[26:29]
	v_mfma_f32_16x16x32_f16 v[26:29], v[6:9], v[214:217], v[38:41]
	v_mfma_f32_16x16x32_f16 v[146:149], v[14:17], v[222:225], v[26:29]
	v_mfma_f32_16x16x32_f16 v[26:29], v[22:25], v[110:113], v[50:53]
	v_mfma_f32_16x16x32_f16 v[170:173], v[34:37], v[130:133], v[26:29]
	v_mfma_f32_16x16x32_f16 v[26:29], v[22:25], v[214:217], v[62:65]
	v_mfma_f32_16x16x32_f16 v[138:141], v[34:37], v[222:225], v[26:29]
	v_mfma_f32_16x16x32_f16 v[26:29], v[54:57], v[110:113], v[74:77]
	v_mfma_f32_16x16x32_f16 v[166:169], v[66:69], v[130:133], v[26:29]
	v_mfma_f32_16x16x32_f16 v[26:29], v[54:57], v[214:217], v[82:85]
	v_mfma_f32_16x16x32_f16 v[134:137], v[66:69], v[222:225], v[26:29]
	v_mfma_f32_16x16x32_f16 v[26:29], v[78:81], v[110:113], v[90:93]
	v_mfma_f32_16x16x32_f16 v[162:165], v[86:89], v[130:133], v[26:29]
	v_mfma_f32_16x16x32_f16 v[26:29], v[78:81], v[214:217], v[94:97]
	v_mfma_f32_16x16x32_f16 v[130:133], v[86:89], v[222:225], v[26:29]
	v_mfma_f32_16x16x32_f16 v[26:29], v[6:9], v[2:5], v[98:101]
	v_mfma_f32_16x16x32_f16 v[6:9], v[6:9], v[18:21], v[102:105]
	v_mfma_f32_16x16x32_f16 v[110:113], v[14:17], v[10:13], v[26:29]
	v_mfma_f32_16x16x32_f16 v[26:29], v[14:17], v[42:45], v[6:9]
	v_mfma_f32_16x16x32_f16 v[6:9], v[22:25], v[2:5], v[106:109]
	v_mfma_f32_16x16x32_f16 v[106:109], v[34:37], v[10:13], v[6:9]
	v_mfma_f32_16x16x32_f16 v[6:9], v[22:25], v[18:21], v[202:205]
	v_mfma_f32_16x16x32_f16 v[14:17], v[34:37], v[42:45], v[6:9]
	v_mfma_f32_16x16x32_f16 v[6:9], v[54:57], v[2:5], v[206:209]
	v_mfma_f32_16x16x32_f16 v[2:5], v[78:81], v[2:5], v[210:213]
	v_mfma_f32_16x16x32_f16 v[102:105], v[66:69], v[10:13], v[6:9]
	v_mfma_f32_16x16x32_f16 v[6:9], v[54:57], v[18:21], v[218:221]
	v_mfma_f32_16x16x32_f16 v[98:101], v[86:89], v[10:13], v[2:5]
	v_mfma_f32_16x16x32_f16 v[2:5], v[78:81], v[18:21], v[198:201]
	v_mfma_f32_16x16x32_f16 v[6:9], v[66:69], v[42:45], v[6:9]
	v_mfma_f32_16x16x32_f16 v[2:5], v[86:89], v[42:45], v[2:5]
	s_cmpk_gt_u32 s54, 0xff
	s_barrier
	s_cbranch_scc1 .LBB9_34
	s_barrier
	s_branch .LBB9_34

.LBB10_11:
	v_lshlrev_b32_e32 v2, 14, v2
	s_lshl_b32 s64, s61, 6
	v_lshlrev_b32_e32 v6, 14, v6
	v_and_b32_e32 v2, 0xffff8000, v2
	s_lshl_b32 s63, s63, 13
	s_and_b32 s64, s64, 0x3000
	v_and_b32_e32 v6, 0xffff8000, v6
	v_lshl_add_u32 v2, v3, 11, v2
	v_and_b32_e32 v10, 48, v172
	v_lshlrev_b32_e32 v11, 6, v172
	v_lshl_add_u32 v6, v7, 11, v6
	s_add_u32 s46, s24, s46
	v_or_b32_e32 v2, v2, v4
	v_and_or_b32 v10, v11, s56, v10
	v_lshlrev_b32_e32 v11, 2, v172
	v_or_b32_e32 v6, v6, v8
	s_addc_u32 s47, s25, s47
	v_add_u32_sdwa v2, v2, sext(v5) dst_sel:DWORD dst_unused:UNUSED_PAD src0_sel:DWORD src1_sel:WORD_0
	v_and_b32_e32 v11, 32, v11
	v_add_u32_sdwa v6, v6, sext(v9) dst_sel:DWORD dst_unused:UNUSED_PAD src0_sel:DWORD src1_sel:WORD_0
	v_ashrrev_i32_e32 v3, 31, v2
	s_add_u32 s44, s22, s44
	v_xad_u32 v170, v10, v11, 0
	s_waitcnt vmcnt(6)
	v_ashrrev_i32_e32 v7, 31, v6
	v_lshlrev_b64 v[2:3], 1, v[2:3]
	s_addc_u32 s45, s23, s45
	v_add_u32_e32 v10, s64, v170
	v_lshlrev_b64 v[6:7], 1, v[6:7]
	v_lshl_add_u64 v[136:137], s[46:47], 0, v[2:3]
	v_lshl_add_u64 v[140:141], s[44:45], 0, v[2:3]
	v_mov_b32_e32 v2, 0
	v_add_u32_e32 v171, 0x10000, v10
	v_add_u32_e32 v173, 0x10400, v10
	v_add_u32_e32 v174, 0x10800, v10
	v_add_u32_e32 v175, 0x10c00, v10
	v_add_u32_e32 v162, 0x14000, v10
	v_add_u32_e32 v163, 0x14400, v10
	v_add_u32_e32 v164, 0x14800, v10
	v_add_u32_e32 v165, 0x14c00, v10
	v_add_u32_e32 v144, 0x18000, v10
	v_add_u32_e32 v145, 0x18400, v10
	v_add_u32_e32 v146, 0x18800, v10
	v_add_u32_e32 v147, 0x18c00, v10
	v_add_u32_e32 v150, 0x1c000, v10
	v_add_u32_e32 v151, 0x1c400, v10
	v_add_u32_e32 v152, 0x1c800, v10
	v_add_u32_e32 v153, 0x1cc00, v10
	v_lshl_add_u64 v[134:135], s[46:47], 0, v[6:7]
	v_lshl_add_u64 v[138:139], s[44:45], 0, v[6:7]
	s_mov_b32 s46, -2
	s_mov_b64 s[44:45], 0
	v_mov_b32_e32 v3, v2
	v_mov_b32_e32 v4, v2
	v_mov_b32_e32 v5, v2
	v_mov_b32_e32 v6, v2
	v_mov_b32_e32 v7, v2
	v_mov_b32_e32 v8, v2
	v_mov_b32_e32 v9, v2
	v_mov_b32_e32 v10, v2
	v_mov_b32_e32 v11, v2
	v_mov_b32_e32 v12, v2
	v_mov_b32_e32 v13, v2
	v_mov_b32_e32 v14, v2
	v_mov_b32_e32 v15, v2
	v_mov_b32_e32 v16, v2
	v_mov_b32_e32 v17, v2
	v_mov_b32_e32 v18, v2
	v_mov_b32_e32 v19, v2
	v_mov_b32_e32 v20, v2
	v_mov_b32_e32 v21, v2
	v_mov_b32_e32 v22, v2
	v_mov_b32_e32 v23, v2
	v_mov_b32_e32 v24, v2
	v_mov_b32_e32 v25, v2
	v_mov_b32_e32 v26, v2
	v_mov_b32_e32 v27, v2
	v_mov_b32_e32 v28, v2
	v_mov_b32_e32 v29, v2
	v_mov_b32_e32 v30, v2
	v_mov_b32_e32 v31, v2
	v_mov_b32_e32 v32, v2
	v_mov_b32_e32 v33, v2
	v_mov_b32_e32 v34, v2
	v_mov_b32_e32 v35, v2
	v_mov_b32_e32 v36, v2
	v_mov_b32_e32 v37, v2
	v_mov_b32_e32 v38, v2
	v_mov_b32_e32 v39, v2
	v_mov_b32_e32 v40, v2
	v_mov_b32_e32 v41, v2
	v_mov_b32_e32 v42, v2
	v_mov_b32_e32 v43, v2
	v_mov_b32_e32 v44, v2
	v_mov_b32_e32 v45, v2
	v_mov_b32_e32 v46, v2
	v_mov_b32_e32 v47, v2
	v_mov_b32_e32 v48, v2
	v_mov_b32_e32 v49, v2
	v_mov_b32_e32 v50, v2
	v_mov_b32_e32 v51, v2
	v_mov_b32_e32 v52, v2
	v_mov_b32_e32 v53, v2
	v_mov_b32_e32 v54, v2
	v_mov_b32_e32 v55, v2
	v_mov_b32_e32 v56, v2
	v_mov_b32_e32 v57, v2
	v_mov_b32_e32 v58, v2
	v_mov_b32_e32 v59, v2
	v_mov_b32_e32 v60, v2
	v_mov_b32_e32 v61, v2
	v_mov_b32_e32 v62, v2
	v_mov_b32_e32 v63, v2
	v_mov_b32_e32 v64, v2
	v_mov_b32_e32 v65, v2
	v_mov_b32_e32 v66, v2
	v_mov_b32_e32 v67, v2
	v_mov_b32_e32 v68, v2
	v_mov_b32_e32 v69, v2
	v_mov_b32_e32 v70, v2
	v_mov_b32_e32 v71, v2
	v_mov_b32_e32 v72, v2
	v_mov_b32_e32 v73, v2
	v_mov_b32_e32 v74, v2
	v_mov_b32_e32 v75, v2
	v_mov_b32_e32 v76, v2
	v_mov_b32_e32 v77, v2
	v_mov_b32_e32 v78, v2
	v_mov_b32_e32 v79, v2
	v_mov_b32_e32 v80, v2
	v_mov_b32_e32 v81, v2
	v_mov_b32_e32 v82, v2
	v_mov_b32_e32 v83, v2
	v_mov_b32_e32 v84, v2
	v_mov_b32_e32 v85, v2
	v_mov_b32_e32 v86, v2
	v_mov_b32_e32 v87, v2
	v_mov_b32_e32 v88, v2
	v_mov_b32_e32 v89, v2
	v_mov_b32_e32 v90, v2
	v_mov_b32_e32 v91, v2
	v_mov_b32_e32 v92, v2
	v_mov_b32_e32 v93, v2
	v_mov_b32_e32 v94, v2
	v_mov_b32_e32 v95, v2
	v_mov_b32_e32 v96, v2
	v_mov_b32_e32 v97, v2
	v_mov_b32_e32 v98, v2
	v_mov_b32_e32 v99, v2
	v_mov_b32_e32 v100, v2
	v_mov_b32_e32 v101, v2
	v_mov_b32_e32 v102, v2
	v_mov_b32_e32 v103, v2
	v_mov_b32_e32 v104, v2
	v_mov_b32_e32 v105, v2
	v_mov_b32_e32 v106, v2
	v_mov_b32_e32 v107, v2
	v_mov_b32_e32 v108, v2
	v_mov_b32_e32 v109, v2
	v_mov_b32_e32 v110, v2
	v_mov_b32_e32 v111, v2
	v_mov_b32_e32 v112, v2
	v_mov_b32_e32 v113, v2
	v_mov_b32_e32 v114, v2
	v_mov_b32_e32 v115, v2
	v_mov_b32_e32 v116, v2
	v_mov_b32_e32 v117, v2
	v_mov_b32_e32 v118, v2
	v_mov_b32_e32 v119, v2
	v_mov_b32_e32 v120, v2
	v_mov_b32_e32 v121, v2
	v_mov_b32_e32 v122, v2
	v_mov_b32_e32 v123, v2
	v_mov_b32_e32 v124, v2
	v_mov_b32_e32 v125, v2
	v_mov_b32_e32 v126, v2
	v_mov_b32_e32 v127, v2
	v_mov_b32_e32 v128, v2
	v_mov_b32_e32 v129, v2
	v_add_u32_e32 v177, 0xc000, v148
	v_add_u32_e32 v178, 0xe000, v148
	s_nop 0
	v_readfirstlane_b32 s70, v177
	v_readfirstlane_b32 s71, v178
	v_readfirstlane_b32 s72, v142
	v_readfirstlane_b32 s73, v143
	v_readfirstlane_b32 s74, v148
	v_readfirstlane_b32 s75, v149
	v_readfirstlane_b32 s76, v154
	v_readfirstlane_b32 s77, v155
	v_readfirstlane_b32 s78, v156
	v_readfirstlane_b32 s79, v157
	v_readfirstlane_b32 s80, v158
	v_readfirstlane_b32 s81, v160
	v_readfirstlane_b32 s82, v161
	v_readfirstlane_b32 s83, v166
	v_readfirstlane_b32 s84, v168
	v_readfirstlane_b32 s85, v169
	s_barrier
	s_barrier
	ds_read_b128 v[182:185], v171
	ds_read_b128 v[186:189], v173
	ds_read_b128 v[190:193], v174
	ds_read_b128 v[194:197], v175
.LBB10_12:
	v_add_u32_e32 v177, 0xc000, v148
	v_lshl_add_u64 v[246:247], v[136:137], 0, s[44:45]
	v_add_u32_e32 v176, s63, v170
	v_lshl_add_u64 v[178:179], v[246:247], 0, s[28:29]
	s_mov_b32 m0, s70
	ds_read_b128 v[198:201], v176
	ds_read_b128 v[202:205], v176 offset:1024
	ds_read_b128 v[206:209], v176 offset:2048
	ds_read_b128 v[210:213], v176 offset:3072
	ds_read_b128 v[214:217], v176 offset:4096
	ds_read_b128 v[218:221], v176 offset:5120
	ds_read_b128 v[222:225], v176 offset:6144
	ds_read_b128 v[226:229], v176 offset:7168
	global_load_lds_dwordx4 v[178:179], off
	v_add_u32_e32 v178, 0xe000, v148
	v_lshl_add_u64 v[248:249], v[134:135], 0, s[44:45]
	s_mov_b32 m0, s71
	v_lshl_add_u64 v[230:231], v[248:249], 0, s[28:29]
	global_load_lds_dwordx4 v[230:231], off
	s_waitcnt lgkmcnt(8)
	s_barrier
	s_waitcnt lgkmcnt(0)
	v_mfma_f32_16x16x32_f16 v[126:129], v[198:201], v[182:185], v[126:129]
	v_mfma_f32_16x16x32_f16 v[122:125], v[198:201], v[190:193], v[122:125]
	v_mfma_f32_16x16x32_f16 v[118:121], v[206:209], v[182:185], v[118:121]
	v_mfma_f32_16x16x32_f16 v[114:117], v[206:209], v[190:193], v[114:117]
	v_mfma_f32_16x16x32_f16 v[110:113], v[214:217], v[182:185], v[110:113]
	v_mfma_f32_16x16x32_f16 v[106:109], v[214:217], v[190:193], v[106:109]
	v_mfma_f32_16x16x32_f16 v[102:105], v[222:225], v[182:185], v[102:105]
	v_mfma_f32_16x16x32_f16 v[98:101], v[222:225], v[190:193], v[98:101]
	v_mfma_f32_16x16x32_f16 v[126:129], v[202:205], v[186:189], v[126:129]
	v_mfma_f32_16x16x32_f16 v[122:125], v[202:205], v[194:197], v[122:125]
	v_mfma_f32_16x16x32_f16 v[118:121], v[210:213], v[186:189], v[118:121]
	v_mfma_f32_16x16x32_f16 v[114:117], v[210:213], v[194:197], v[114:117]
	v_mfma_f32_16x16x32_f16 v[110:113], v[218:221], v[186:189], v[110:113]
	v_mfma_f32_16x16x32_f16 v[106:109], v[218:221], v[194:197], v[106:109]
	v_mfma_f32_16x16x32_f16 v[102:105], v[226:229], v[186:189], v[102:105]
	v_mfma_f32_16x16x32_f16 v[98:101], v[226:229], v[194:197], v[98:101]
	s_barrier
	v_lshl_add_u64 v[250:251], v[140:141], 0, s[44:45]
	v_lshl_add_u64 v[252:253], v[250:251], 0, s[30:31]
	s_mov_b32 m0, s72
	ds_read_b128 v[230:233], v162
	ds_read_b128 v[234:237], v163
	ds_read_b128 v[238:241], v164
	ds_read_b128 v[242:245], v165
	global_load_lds_dwordx4 v[252:253], off
	v_lshl_add_u64 v[252:253], v[138:139], 0, s[44:45]
	s_mov_b32 m0, s73
	v_lshl_add_u64 v[254:255], v[252:253], 0, s[30:31]
	global_load_lds_dwordx4 v[254:255], off
	s_barrier
	s_waitcnt lgkmcnt(0)
	v_mfma_f32_16x16x32_f16 v[94:97], v[198:201], v[230:233], v[94:97]
	v_mfma_f32_16x16x32_f16 v[90:93], v[198:201], v[238:241], v[90:93]
	v_mfma_f32_16x16x32_f16 v[86:89], v[206:209], v[230:233], v[86:89]
	v_mfma_f32_16x16x32_f16 v[82:85], v[206:209], v[238:241], v[82:85]
	v_mfma_f32_16x16x32_f16 v[78:81], v[214:217], v[230:233], v[78:81]
	v_mfma_f32_16x16x32_f16 v[74:77], v[214:217], v[238:241], v[74:77]
	v_mfma_f32_16x16x32_f16 v[70:73], v[222:225], v[230:233], v[70:73]
	v_mfma_f32_16x16x32_f16 v[66:69], v[222:225], v[238:241], v[66:69]
	v_mfma_f32_16x16x32_f16 v[94:97], v[202:205], v[234:237], v[94:97]
	v_mfma_f32_16x16x32_f16 v[90:93], v[202:205], v[242:245], v[90:93]
	v_mfma_f32_16x16x32_f16 v[86:89], v[210:213], v[234:237], v[86:89]
	v_mfma_f32_16x16x32_f16 v[82:85], v[210:213], v[242:245], v[82:85]
	v_mfma_f32_16x16x32_f16 v[78:81], v[218:221], v[234:237], v[78:81]
	v_mfma_f32_16x16x32_f16 v[74:77], v[218:221], v[242:245], v[74:77]
	v_mfma_f32_16x16x32_f16 v[70:73], v[226:229], v[234:237], v[70:73]
	v_mfma_f32_16x16x32_f16 v[66:69], v[226:229], v[242:245], v[66:69]
	v_lshl_add_u64 v[254:255], v[246:247], 0, s[30:31]
	s_mov_b32 m0, s74
	s_barrier
	ds_read_b128 v[198:201], v176 offset:16384
	ds_read_b128 v[202:205], v176 offset:17408
	ds_read_b128 v[206:209], v176 offset:18432
	ds_read_b128 v[210:213], v176 offset:19456
	ds_read_b128 v[214:217], v176 offset:20480
	ds_read_b128 v[218:221], v176 offset:21504
	ds_read_b128 v[222:225], v176 offset:22528
	ds_read_b128 v[226:229], v176 offset:23552
	global_load_lds_dwordx4 v[254:255], off
	s_mov_b32 m0, s75
	v_lshl_add_u64 v[254:255], v[248:249], 0, s[30:31]
	global_load_lds_dwordx4 v[254:255], off
	s_waitcnt vmcnt(10)
	s_barrier
	s_waitcnt lgkmcnt(0)
	v_mfma_f32_16x16x32_f16 v[62:65], v[198:201], v[182:185], v[62:65]
	v_mfma_f32_16x16x32_f16 v[58:61], v[198:201], v[190:193], v[58:61]
	v_mfma_f32_16x16x32_f16 v[54:57], v[206:209], v[182:185], v[54:57]
	v_mfma_f32_16x16x32_f16 v[50:53], v[206:209], v[190:193], v[50:53]
	v_mfma_f32_16x16x32_f16 v[46:49], v[214:217], v[182:185], v[46:49]
	v_mfma_f32_16x16x32_f16 v[42:45], v[214:217], v[190:193], v[42:45]
	v_mfma_f32_16x16x32_f16 v[38:41], v[222:225], v[182:185], v[38:41]
	v_mfma_f32_16x16x32_f16 v[34:37], v[222:225], v[190:193], v[34:37]
	v_mfma_f32_16x16x32_f16 v[62:65], v[202:205], v[186:189], v[62:65]
	v_mfma_f32_16x16x32_f16 v[58:61], v[202:205], v[194:197], v[58:61]
	v_mfma_f32_16x16x32_f16 v[54:57], v[210:213], v[186:189], v[54:57]
	v_mfma_f32_16x16x32_f16 v[50:53], v[210:213], v[194:197], v[50:53]
	v_mfma_f32_16x16x32_f16 v[46:49], v[218:221], v[186:189], v[46:49]
	v_mfma_f32_16x16x32_f16 v[42:45], v[218:221], v[194:197], v[42:45]
	v_mfma_f32_16x16x32_f16 v[38:41], v[226:229], v[186:189], v[38:41]
	v_mfma_f32_16x16x32_f16 v[34:37], v[226:229], v[194:197], v[34:37]
	s_barrier
	s_mov_b32 m0, s76
	v_lshl_add_u64 v[182:183], v[250:251], 0, s[34:35]
	global_load_lds_dwordx4 v[182:183], off
	s_mov_b32 m0, s77
	v_lshl_add_u64 v[182:183], v[252:253], 0, s[34:35]
	global_load_lds_dwordx4 v[182:183], off
	s_waitcnt vmcnt(6)
	s_barrier
	v_mfma_f32_16x16x32_f16 v[30:33], v[198:201], v[230:233], v[30:33]
	v_mfma_f32_16x16x32_f16 v[26:29], v[198:201], v[238:241], v[26:29]
	v_mfma_f32_16x16x32_f16 v[22:25], v[206:209], v[230:233], v[22:25]
	v_mfma_f32_16x16x32_f16 v[18:21], v[206:209], v[238:241], v[18:21]
	v_mfma_f32_16x16x32_f16 v[14:17], v[214:217], v[230:233], v[14:17]
	v_mfma_f32_16x16x32_f16 v[10:13], v[214:217], v[238:241], v[10:13]
	v_mfma_f32_16x16x32_f16 v[6:9], v[222:225], v[230:233], v[6:9]
	v_mfma_f32_16x16x32_f16 v[2:5], v[222:225], v[238:241], v[2:5]
	v_mfma_f32_16x16x32_f16 v[30:33], v[202:205], v[234:237], v[30:33]
	v_mfma_f32_16x16x32_f16 v[26:29], v[202:205], v[242:245], v[26:29]
	v_mfma_f32_16x16x32_f16 v[22:25], v[210:213], v[234:237], v[22:25]
	v_mfma_f32_16x16x32_f16 v[18:21], v[210:213], v[242:245], v[18:21]
	ds_read_b128 v[182:185], v144
	ds_read_b128 v[186:189], v145
	ds_read_b128 v[190:193], v146
	ds_read_b128 v[194:197], v147
	v_mfma_f32_16x16x32_f16 v[14:17], v[218:221], v[234:237], v[14:17]
	v_mfma_f32_16x16x32_f16 v[10:13], v[218:221], v[242:245], v[10:13]
	v_mfma_f32_16x16x32_f16 v[6:9], v[226:229], v[234:237], v[6:9]
	v_mfma_f32_16x16x32_f16 v[2:5], v[226:229], v[242:245], v[2:5]
	s_barrier
	v_lshl_add_u64 v[230:231], v[246:247], 0, s[34:35]
	s_mov_b32 m0, s78
	ds_read_b128 v[198:201], v176 offset:32768
	ds_read_b128 v[202:205], v176 offset:33792
	ds_read_b128 v[206:209], v176 offset:34816
	ds_read_b128 v[210:213], v176 offset:35840
	ds_read_b128 v[214:217], v176 offset:36864
	ds_read_b128 v[218:221], v176 offset:37888
	ds_read_b128 v[222:225], v176 offset:38912
	ds_read_b128 v[226:229], v176 offset:39936
	global_load_lds_dwordx4 v[230:231], off
	s_mov_b32 m0, s79
	v_lshl_add_u64 v[230:231], v[248:249], 0, s[34:35]
	global_load_lds_dwordx4 v[230:231], off
	s_waitcnt lgkmcnt(8)
	s_barrier
	s_waitcnt lgkmcnt(0)
	v_mfma_f32_16x16x32_f16 v[126:129], v[198:201], v[182:185], v[126:129]
	v_mfma_f32_16x16x32_f16 v[122:125], v[198:201], v[190:193], v[122:125]
	v_mfma_f32_16x16x32_f16 v[118:121], v[206:209], v[182:185], v[118:121]
	v_mfma_f32_16x16x32_f16 v[114:117], v[206:209], v[190:193], v[114:117]
	v_mfma_f32_16x16x32_f16 v[110:113], v[214:217], v[182:185], v[110:113]
	v_mfma_f32_16x16x32_f16 v[106:109], v[214:217], v[190:193], v[106:109]
	v_mfma_f32_16x16x32_f16 v[102:105], v[222:225], v[182:185], v[102:105]
	v_mfma_f32_16x16x32_f16 v[98:101], v[222:225], v[190:193], v[98:101]
	v_mfma_f32_16x16x32_f16 v[126:129], v[202:205], v[186:189], v[126:129]
	v_mfma_f32_16x16x32_f16 v[122:125], v[202:205], v[194:197], v[122:125]
	v_mfma_f32_16x16x32_f16 v[118:121], v[210:213], v[186:189], v[118:121]
	v_mfma_f32_16x16x32_f16 v[114:117], v[210:213], v[194:197], v[114:117]
	v_mfma_f32_16x16x32_f16 v[110:113], v[218:221], v[186:189], v[110:113]
	v_mfma_f32_16x16x32_f16 v[106:109], v[218:221], v[194:197], v[106:109]
	v_mfma_f32_16x16x32_f16 v[102:105], v[226:229], v[186:189], v[102:105]
	v_mfma_f32_16x16x32_f16 v[98:101], v[226:229], v[194:197], v[98:101]
	s_barrier
	v_lshl_add_u64 v[254:255], v[250:251], 0, s[36:37]
	s_mov_b32 m0, s80
	ds_read_b128 v[230:233], v150
	ds_read_b128 v[234:237], v151
	ds_read_b128 v[238:241], v152
	ds_read_b128 v[242:245], v153
	global_load_lds_dwordx4 v[254:255], off
	s_mov_b32 m0, s81
	v_lshl_add_u64 v[254:255], v[252:253], 0, s[36:37]
	global_load_lds_dwordx4 v[254:255], off
	s_barrier
	s_waitcnt lgkmcnt(0)
	v_mfma_f32_16x16x32_f16 v[94:97], v[198:201], v[230:233], v[94:97]
	v_mfma_f32_16x16x32_f16 v[90:93], v[198:201], v[238:241], v[90:93]
	v_mfma_f32_16x16x32_f16 v[86:89], v[206:209], v[230:233], v[86:89]
	v_mfma_f32_16x16x32_f16 v[82:85], v[206:209], v[238:241], v[82:85]
	v_mfma_f32_16x16x32_f16 v[78:81], v[214:217], v[230:233], v[78:81]
	v_mfma_f32_16x16x32_f16 v[74:77], v[214:217], v[238:241], v[74:77]
	v_mfma_f32_16x16x32_f16 v[70:73], v[222:225], v[230:233], v[70:73]
	v_mfma_f32_16x16x32_f16 v[66:69], v[222:225], v[238:241], v[66:69]
	v_mfma_f32_16x16x32_f16 v[94:97], v[202:205], v[234:237], v[94:97]
	v_mfma_f32_16x16x32_f16 v[90:93], v[202:205], v[242:245], v[90:93]
	v_mfma_f32_16x16x32_f16 v[86:89], v[210:213], v[234:237], v[86:89]
	v_mfma_f32_16x16x32_f16 v[82:85], v[210:213], v[242:245], v[82:85]
	v_mfma_f32_16x16x32_f16 v[78:81], v[218:221], v[234:237], v[78:81]
	v_mfma_f32_16x16x32_f16 v[74:77], v[218:221], v[242:245], v[74:77]
	v_mfma_f32_16x16x32_f16 v[70:73], v[226:229], v[234:237], v[70:73]
	v_mfma_f32_16x16x32_f16 v[66:69], v[226:229], v[242:245], v[66:69]
	v_lshl_add_u64 v[246:247], v[246:247], 0, s[36:37]
	s_mov_b32 m0, s82
	s_barrier
	ds_read_b128 v[198:201], v176 offset:49152
	ds_read_b128 v[202:205], v176 offset:50176
	ds_read_b128 v[206:209], v176 offset:51200
	ds_read_b128 v[210:213], v176 offset:52224
	ds_read_b128 v[214:217], v176 offset:53248
	ds_read_b128 v[218:221], v176 offset:54272
	ds_read_b128 v[222:225], v176 offset:55296
	ds_read_b128 v[226:229], v176 offset:56320
	global_load_lds_dwordx4 v[246:247], off
	s_mov_b32 m0, s83
	v_lshl_add_u64 v[246:247], v[248:249], 0, s[36:37]
	global_load_lds_dwordx4 v[246:247], off
	s_waitcnt vmcnt(10)
	s_barrier
	s_waitcnt lgkmcnt(0)
	v_mfma_f32_16x16x32_f16 v[62:65], v[198:201], v[182:185], v[62:65]
	v_mfma_f32_16x16x32_f16 v[58:61], v[198:201], v[190:193], v[58:61]
	v_mfma_f32_16x16x32_f16 v[54:57], v[206:209], v[182:185], v[54:57]
	v_mfma_f32_16x16x32_f16 v[50:53], v[206:209], v[190:193], v[50:53]
	v_mfma_f32_16x16x32_f16 v[46:49], v[214:217], v[182:185], v[46:49]
	v_mfma_f32_16x16x32_f16 v[42:45], v[214:217], v[190:193], v[42:45]
	v_mfma_f32_16x16x32_f16 v[38:41], v[222:225], v[182:185], v[38:41]
	v_mfma_f32_16x16x32_f16 v[34:37], v[222:225], v[190:193], v[34:37]
	v_mfma_f32_16x16x32_f16 v[62:65], v[202:205], v[186:189], v[62:65]
	v_mfma_f32_16x16x32_f16 v[58:61], v[202:205], v[194:197], v[58:61]
	v_mfma_f32_16x16x32_f16 v[54:57], v[210:213], v[186:189], v[54:57]
	v_mfma_f32_16x16x32_f16 v[50:53], v[210:213], v[194:197], v[50:53]
	v_mfma_f32_16x16x32_f16 v[46:49], v[218:221], v[186:189], v[46:49]
	v_mfma_f32_16x16x32_f16 v[42:45], v[218:221], v[194:197], v[42:45]
	v_mfma_f32_16x16x32_f16 v[38:41], v[226:229], v[186:189], v[38:41]
	v_mfma_f32_16x16x32_f16 v[34:37], v[226:229], v[194:197], v[34:37]
	s_barrier
	s_mov_b32 m0, s84
	v_lshl_add_u64 v[182:183], v[250:251], 0, s[38:39]
	global_load_lds_dwordx4 v[182:183], off
	s_mov_b32 m0, s85
	v_lshl_add_u64 v[182:183], v[252:253], 0, s[38:39]
	global_load_lds_dwordx4 v[182:183], off
	s_waitcnt vmcnt(6)
	s_barrier
	v_mfma_f32_16x16x32_f16 v[30:33], v[198:201], v[230:233], v[30:33]
	v_mfma_f32_16x16x32_f16 v[26:29], v[198:201], v[238:241], v[26:29]
	v_mfma_f32_16x16x32_f16 v[22:25], v[206:209], v[230:233], v[22:25]
	v_mfma_f32_16x16x32_f16 v[18:21], v[206:209], v[238:241], v[18:21]
	v_mfma_f32_16x16x32_f16 v[14:17], v[214:217], v[230:233], v[14:17]
	v_mfma_f32_16x16x32_f16 v[10:13], v[214:217], v[238:241], v[10:13]
	v_mfma_f32_16x16x32_f16 v[6:9], v[222:225], v[230:233], v[6:9]
	v_mfma_f32_16x16x32_f16 v[2:5], v[222:225], v[238:241], v[2:5]
	v_mfma_f32_16x16x32_f16 v[30:33], v[202:205], v[234:237], v[30:33]
	v_mfma_f32_16x16x32_f16 v[26:29], v[202:205], v[242:245], v[26:29]
	v_mfma_f32_16x16x32_f16 v[22:25], v[210:213], v[234:237], v[22:25]
	v_mfma_f32_16x16x32_f16 v[18:21], v[210:213], v[242:245], v[18:21]
	ds_read_b128 v[182:185], v171
	ds_read_b128 v[186:189], v173
	ds_read_b128 v[190:193], v174
	ds_read_b128 v[194:197], v175
	v_mfma_f32_16x16x32_f16 v[14:17], v[218:221], v[234:237], v[14:17]
	v_mfma_f32_16x16x32_f16 v[10:13], v[218:221], v[242:245], v[10:13]
	v_mfma_f32_16x16x32_f16 v[6:9], v[226:229], v[234:237], v[6:9]
	v_mfma_f32_16x16x32_f16 v[2:5], v[226:229], v[242:245], v[2:5]
	s_add_i32 s46, s46, 2
	s_add_u32 s44, s44, 0x100
	s_addc_u32 s45, s45, 0
	s_cmp_lt_u32 s46, 28
	s_barrier
	s_cbranch_scc1 .LBB10_12
	s_add_u32 s42, s42, 0x80f80
	s_addc_u32 s43, s43, 0
	v_readfirstlane_b32 s44, v177
	v_lshl_add_u64 v[130:131], v[130:131], 1, s[42:43]
	s_mov_b32 m0, s44
	ds_read_b128 v[134:137], v171
	ds_read_b128 v[138:141], v173
	ds_read_b128 v[154:157], v174
	ds_read_b128 v[168:171], v175
	ds_read_b128 v[182:185], v176
	ds_read_b128 v[186:189], v176 offset:1024
	ds_read_b128 v[190:193], v176 offset:2048
	ds_read_b128 v[194:197], v176 offset:3072
	ds_read_b128 v[198:201], v176 offset:4096
	ds_read_b128 v[202:205], v176 offset:5120
	ds_read_b128 v[206:209], v176 offset:6144
	ds_read_b128 v[210:213], v176 offset:7168
	global_load_lds_dwordx4 v[130:131], off
	v_lshl_add_u64 v[130:131], v[132:133], 1, s[42:43]
	v_readfirstlane_b32 s42, v178
	s_mov_b32 m0, s42
	s_nop 0
	global_load_lds_dwordx4 v[130:131], off
	s_barrier
	s_waitcnt lgkmcnt(0)
	v_mfma_f32_16x16x32_f16 v[122:125], v[182:185], v[154:157], v[122:125]
	v_mfma_f32_16x16x32_f16 v[110:113], v[198:201], v[134:137], v[110:113]
	v_mfma_f32_16x16x32_f16 v[98:101], v[206:209], v[154:157], v[98:101]
	v_mfma_f32_16x16x32_f16 v[126:129], v[182:185], v[134:137], v[126:129]
	v_mfma_f32_16x16x32_f16 v[122:125], v[186:189], v[168:171], v[122:125]
	v_mfma_f32_16x16x32_f16 v[118:121], v[190:193], v[134:137], v[118:121]
	v_mfma_f32_16x16x32_f16 v[114:117], v[190:193], v[154:157], v[114:117]
	v_mfma_f32_16x16x32_f16 v[130:133], v[202:205], v[138:141], v[110:113]
	v_mfma_f32_16x16x32_f16 v[106:109], v[198:201], v[154:157], v[106:109]
	v_mfma_f32_16x16x32_f16 v[102:105], v[206:209], v[134:137], v[102:105]
	v_mfma_f32_16x16x32_f16 v[98:101], v[210:213], v[168:171], v[98:101]
	v_mfma_f32_16x16x32_f16 v[126:129], v[186:189], v[138:141], v[126:129]
	v_mfma_f32_16x16x32_f16 v[118:121], v[194:197], v[138:141], v[118:121]
	v_mfma_f32_16x16x32_f16 v[114:117], v[194:197], v[168:171], v[114:117]
	v_mfma_f32_16x16x32_f16 v[214:217], v[202:205], v[168:171], v[106:109]
	v_mfma_f32_16x16x32_f16 v[102:105], v[210:213], v[138:141], v[102:105]
	s_barrier
	ds_read_b128 v[106:109], v162
	ds_read_b128 v[110:113], v163
	ds_read_b128 v[160:163], v164
	ds_read_b128 v[218:221], v165
	s_barrier
	s_waitcnt lgkmcnt(0)
	v_mfma_f32_16x16x32_f16 v[82:85], v[190:193], v[160:163], v[82:85]
	v_mfma_f32_16x16x32_f16 v[78:81], v[198:201], v[106:109], v[78:81]
	v_mfma_f32_16x16x32_f16 v[74:77], v[198:201], v[160:163], v[74:77]
	v_mfma_f32_16x16x32_f16 v[70:73], v[206:209], v[106:109], v[70:73]
	v_mfma_f32_16x16x32_f16 v[66:69], v[206:209], v[160:163], v[66:69]
	v_mfma_f32_16x16x32_f16 v[94:97], v[182:185], v[106:109], v[94:97]
	v_mfma_f32_16x16x32_f16 v[90:93], v[182:185], v[160:163], v[90:93]
	v_mfma_f32_16x16x32_f16 v[86:89], v[190:193], v[106:109], v[86:89]
	v_mfma_f32_16x16x32_f16 v[82:85], v[194:197], v[218:221], v[82:85]
	v_mfma_f32_16x16x32_f16 v[78:81], v[202:205], v[110:113], v[78:81]
	v_mfma_f32_16x16x32_f16 v[74:77], v[202:205], v[218:221], v[74:77]
	v_mfma_f32_16x16x32_f16 v[70:73], v[210:213], v[110:113], v[70:73]
	v_mfma_f32_16x16x32_f16 v[66:69], v[210:213], v[218:221], v[66:69]
	v_mfma_f32_16x16x32_f16 v[222:225], v[186:189], v[110:113], v[94:97]
	v_mfma_f32_16x16x32_f16 v[182:185], v[186:189], v[218:221], v[90:93]
	v_mfma_f32_16x16x32_f16 v[86:89], v[194:197], v[110:113], v[86:89]
	s_barrier
	ds_read_b128 v[90:93], v176 offset:16384
	ds_read_b128 v[94:97], v176 offset:17408
	ds_read_b128 v[186:189], v176 offset:18432
	ds_read_b128 v[190:193], v176 offset:19456
	ds_read_b128 v[194:197], v176 offset:20480
	ds_read_b128 v[198:201], v176 offset:21504
	ds_read_b128 v[202:205], v176 offset:22528
	ds_read_b128 v[206:209], v176 offset:23552
	s_waitcnt vmcnt(4)
	s_barrier
	s_waitcnt lgkmcnt(0)
	v_mfma_f32_16x16x32_f16 v[46:49], v[194:197], v[134:137], v[46:49]
	v_mfma_f32_16x16x32_f16 v[42:45], v[194:197], v[154:157], v[42:45]
	v_mfma_f32_16x16x32_f16 v[38:41], v[202:205], v[134:137], v[38:41]
	v_mfma_f32_16x16x32_f16 v[34:37], v[202:205], v[154:157], v[34:37]
	v_mfma_f32_16x16x32_f16 v[62:65], v[90:93], v[134:137], v[62:65]
	v_mfma_f32_16x16x32_f16 v[58:61], v[90:93], v[154:157], v[58:61]
	v_mfma_f32_16x16x32_f16 v[54:57], v[186:189], v[134:137], v[54:57]
	v_mfma_f32_16x16x32_f16 v[50:53], v[186:189], v[154:157], v[50:53]
	v_mfma_f32_16x16x32_f16 v[46:49], v[198:201], v[138:141], v[46:49]
	v_mfma_f32_16x16x32_f16 v[42:45], v[198:201], v[168:171], v[42:45]
	v_mfma_f32_16x16x32_f16 v[38:41], v[206:209], v[138:141], v[38:41]
	v_mfma_f32_16x16x32_f16 v[34:37], v[206:209], v[168:171], v[34:37]
	v_mfma_f32_16x16x32_f16 v[210:213], v[94:97], v[138:141], v[62:65]
	v_mfma_f32_16x16x32_f16 v[226:229], v[94:97], v[168:171], v[58:61]
	v_mfma_f32_16x16x32_f16 v[230:233], v[190:193], v[138:141], v[54:57]
	v_mfma_f32_16x16x32_f16 v[234:237], v[190:193], v[168:171], v[50:53]
	v_mfma_f32_16x16x32_f16 v[2:5], v[202:205], v[160:163], v[2:5]
	v_mfma_f32_16x16x32_f16 v[30:33], v[90:93], v[106:109], v[30:33]
	v_mfma_f32_16x16x32_f16 v[26:29], v[90:93], v[160:163], v[26:29]
	v_mfma_f32_16x16x32_f16 v[22:25], v[186:189], v[106:109], v[22:25]
	v_mfma_f32_16x16x32_f16 v[18:21], v[186:189], v[160:163], v[18:21]
	v_mfma_f32_16x16x32_f16 v[14:17], v[194:197], v[106:109], v[14:17]
	v_mfma_f32_16x16x32_f16 v[10:13], v[194:197], v[160:163], v[10:13]
	v_mfma_f32_16x16x32_f16 v[6:9], v[202:205], v[106:109], v[6:9]
	v_mfma_f32_16x16x32_f16 v[2:5], v[206:209], v[218:221], v[2:5]
	v_mfma_f32_16x16x32_f16 v[138:141], v[94:97], v[110:113], v[30:33]
	v_mfma_f32_16x16x32_f16 v[168:171], v[94:97], v[218:221], v[26:29]
	v_mfma_f32_16x16x32_f16 v[238:241], v[190:193], v[110:113], v[22:25]
	v_mfma_f32_16x16x32_f16 v[186:189], v[190:193], v[218:221], v[18:21]
	v_mfma_f32_16x16x32_f16 v[190:193], v[198:201], v[110:113], v[14:17]
	v_mfma_f32_16x16x32_f16 v[194:197], v[198:201], v[218:221], v[10:13]
	v_mfma_f32_16x16x32_f16 v[198:201], v[206:209], v[110:113], v[6:9]
	s_barrier
	s_nop 0
	ds_read_b128 v[6:9], v144
	ds_read_b128 v[10:13], v145
	ds_read_b128 v[14:17], v146
	ds_read_b128 v[160:163], v147
	ds_read_b128 v[18:21], v176 offset:32768
	ds_read_b128 v[22:25], v176 offset:33792
	ds_read_b128 v[26:29], v176 offset:34816
	ds_read_b128 v[50:53], v176 offset:35840
	ds_read_b128 v[202:205], v176 offset:36864
	ds_read_b128 v[206:209], v176 offset:37888
	ds_read_b128 v[218:221], v176 offset:38912
	ds_read_b128 v[242:245], v176 offset:39936
	s_waitcnt vmcnt(2)
	s_barrier
	s_waitcnt lgkmcnt(0)
	v_mfma_f32_16x16x32_f16 v[30:33], v[18:21], v[6:9], v[126:129]
	v_mfma_f32_16x16x32_f16 v[154:157], v[22:25], v[10:13], v[30:33]
	v_mfma_f32_16x16x32_f16 v[30:33], v[18:21], v[14:17], v[122:125]
	v_mfma_f32_16x16x32_f16 v[110:113], v[22:25], v[160:163], v[30:33]
	v_mfma_f32_16x16x32_f16 v[30:33], v[26:29], v[6:9], v[118:121]
	v_mfma_f32_16x16x32_f16 v[146:149], v[50:53], v[10:13], v[30:33]
	v_mfma_f32_16x16x32_f16 v[30:33], v[26:29], v[14:17], v[114:117]
	v_mfma_f32_16x16x32_f16 v[106:109], v[50:53], v[160:163], v[30:33]
	v_mfma_f32_16x16x32_f16 v[30:33], v[202:205], v[6:9], v[130:133]
	v_mfma_f32_16x16x32_f16 v[142:145], v[206:209], v[10:13], v[30:33]
	v_mfma_f32_16x16x32_f16 v[30:33], v[202:205], v[14:17], v[214:217]
	v_mfma_f32_16x16x32_f16 v[94:97], v[206:209], v[160:163], v[30:33]
	v_mfma_f32_16x16x32_f16 v[30:33], v[218:221], v[6:9], v[102:105]
	v_mfma_f32_16x16x32_f16 v[134:137], v[242:245], v[10:13], v[30:33]
	v_mfma_f32_16x16x32_f16 v[30:33], v[218:221], v[14:17], v[98:101]
	v_mfma_f32_16x16x32_f16 v[90:93], v[242:245], v[160:163], v[30:33]
	s_barrier
	ds_read_b128 v[102:105], v150
	ds_read_b128 v[114:117], v151
	ds_read_b128 v[118:121], v152
	ds_read_b128 v[126:129], v153
	s_waitcnt vmcnt(0)
	s_barrier
	s_waitcnt lgkmcnt(0)
	v_mfma_f32_16x16x32_f16 v[30:33], v[18:21], v[102:105], v[222:225]
	v_mfma_f32_16x16x32_f16 v[18:21], v[18:21], v[118:121], v[182:185]
	v_mfma_f32_16x16x32_f16 v[62:65], v[22:25], v[114:117], v[30:33]
	v_mfma_f32_16x16x32_f16 v[30:33], v[22:25], v[126:129], v[18:21]
	v_mfma_f32_16x16x32_f16 v[18:21], v[26:29], v[102:105], v[86:89]
	v_mfma_f32_16x16x32_f16 v[58:61], v[50:53], v[114:117], v[18:21]
	v_mfma_f32_16x16x32_f16 v[18:21], v[26:29], v[118:121], v[82:85]
	v_mfma_f32_16x16x32_f16 v[26:29], v[50:53], v[126:129], v[18:21]
	v_mfma_f32_16x16x32_f16 v[18:21], v[202:205], v[102:105], v[78:81]
	v_mfma_f32_16x16x32_f16 v[54:57], v[206:209], v[114:117], v[18:21]
	v_mfma_f32_16x16x32_f16 v[18:21], v[202:205], v[118:121], v[74:77]
	v_mfma_f32_16x16x32_f16 v[22:25], v[206:209], v[126:129], v[18:21]
	v_mfma_f32_16x16x32_f16 v[18:21], v[218:221], v[102:105], v[70:73]
	v_mfma_f32_16x16x32_f16 v[50:53], v[242:245], v[114:117], v[18:21]
	v_mfma_f32_16x16x32_f16 v[18:21], v[218:221], v[118:121], v[66:69]
	v_mfma_f32_16x16x32_f16 v[18:21], v[242:245], v[126:129], v[18:21]
	s_barrier
	ds_read_b128 v[86:89], v176 offset:49152
	ds_read_b128 v[150:153], v176 offset:50176
	ds_read_b128 v[182:185], v176 offset:51200
	ds_read_b128 v[202:205], v176 offset:52224
	ds_read_b128 v[206:209], v176 offset:53248
	ds_read_b128 v[214:217], v176 offset:54272
	ds_read_b128 v[218:221], v176 offset:55296
	ds_read_b128 v[174:177], v176 offset:56320
	s_barrier
	s_waitcnt lgkmcnt(0)
	v_mfma_f32_16x16x32_f16 v[66:69], v[86:89], v[6:9], v[210:213]
	v_mfma_f32_16x16x32_f16 v[130:133], v[150:153], v[10:13], v[66:69]
	v_mfma_f32_16x16x32_f16 v[66:69], v[86:89], v[14:17], v[226:229]
	v_mfma_f32_16x16x32_f16 v[78:81], v[150:153], v[160:163], v[66:69]
	v_mfma_f32_16x16x32_f16 v[66:69], v[182:185], v[6:9], v[230:233]
	v_mfma_f32_16x16x32_f16 v[46:49], v[206:209], v[6:9], v[46:49]
	v_mfma_f32_16x16x32_f16 v[6:9], v[218:221], v[6:9], v[38:41]
	v_mfma_f32_16x16x32_f16 v[122:125], v[202:205], v[10:13], v[66:69]
	v_mfma_f32_16x16x32_f16 v[66:69], v[182:185], v[14:17], v[234:237]
	v_mfma_f32_16x16x32_f16 v[42:45], v[206:209], v[14:17], v[42:45]
	v_mfma_f32_16x16x32_f16 v[82:85], v[174:177], v[10:13], v[6:9]
	v_mfma_f32_16x16x32_f16 v[6:9], v[218:221], v[14:17], v[34:37]
	v_mfma_f32_16x16x32_f16 v[74:77], v[202:205], v[160:163], v[66:69]
	v_mfma_f32_16x16x32_f16 v[98:101], v[214:217], v[10:13], v[46:49]
	v_mfma_f32_16x16x32_f16 v[70:73], v[214:217], v[160:163], v[42:45]
	v_mfma_f32_16x16x32_f16 v[66:69], v[174:177], v[160:163], v[6:9]
	v_mfma_f32_16x16x32_f16 v[6:9], v[86:89], v[102:105], v[138:141]
	v_mfma_f32_16x16x32_f16 v[46:49], v[150:153], v[114:117], v[6:9]
	v_mfma_f32_16x16x32_f16 v[6:9], v[86:89], v[118:121], v[168:171]
	v_mfma_f32_16x16x32_f16 v[14:17], v[150:153], v[126:129], v[6:9]
	v_mfma_f32_16x16x32_f16 v[6:9], v[182:185], v[102:105], v[238:241]
	v_mfma_f32_16x16x32_f16 v[42:45], v[202:205], v[114:117], v[6:9]
	v_mfma_f32_16x16x32_f16 v[6:9], v[182:185], v[118:121], v[186:189]
	v_mfma_f32_16x16x32_f16 v[10:13], v[202:205], v[126:129], v[6:9]
	v_mfma_f32_16x16x32_f16 v[6:9], v[206:209], v[102:105], v[190:193]
	v_mfma_f32_16x16x32_f16 v[38:41], v[214:217], v[114:117], v[6:9]
	v_mfma_f32_16x16x32_f16 v[6:9], v[206:209], v[118:121], v[194:197]
	v_mfma_f32_16x16x32_f16 v[34:37], v[218:221], v[102:105], v[198:201]
	v_mfma_f32_16x16x32_f16 v[2:5], v[218:221], v[118:121], v[2:5]
	v_mfma_f32_16x16x32_f16 v[6:9], v[214:217], v[126:129], v[6:9]
	v_mfma_f32_16x16x32_f16 v[34:37], v[174:177], v[114:117], v[34:37]
	v_mfma_f32_16x16x32_f16 v[2:5], v[174:177], v[126:129], v[2:5]
	s_cmpk_gt_u32 s61, 0xff
	s_barrier
	s_cbranch_scc1 .LBB10_15
	s_barrier
